# speedup vs baseline: 1.0064x; 1.0064x over previous
.Lscan_loop_a_st:
	ds_read_b64 v[128:129], v106 offset:96
	ds_read_b64 v[130:131], v106 offset:104
	ds_read_b64 v[132:133], v106 offset:112
	s_waitcnt vmcnt(8)
	global_load_dwordx4 v[146:149], v[196:197], off
	global_load_dwordx4 v[150:153], v[196:197], off offset:512
	global_load_dwordx4 v[154:157], v[196:197], off offset:1024
	v_lshl_add_u64 v[196:197], v[196:197], 0, s[42:43]
	s_waitcnt lgkmcnt(3)
	v_mfma_scale_f32_16x16x128_f8f6f4 v[134:137], v[122:127], v[2:7], 0, v178, v115 op_sel_hi:[0,0,0] cbsz:2 blgp:2
	v_mfma_scale_f32_16x16x128_f8f6f4 v[138:141], v[122:127], v[14:19], 0, v178, v115 op_sel_hi:[0,0,0] cbsz:2 blgp:2
	v_mfma_scale_f32_16x16x128_f8f6f4 v[142:145], v[122:127], v[26:31], 0, v178, v115 op_sel_hi:[0,0,0] cbsz:2 blgp:2
	v_mfma_scale_f32_16x16x128_f8f6f4 v[134:137], v[122:127], v[38:43], v[134:137], v179, v115 op_sel_hi:[0,0,0] cbsz:2 blgp:2
	v_mfma_scale_f32_16x16x128_f8f6f4 v[138:141], v[122:127], v[50:55], v[138:141], v179, v115 op_sel_hi:[0,0,0] cbsz:2 blgp:2
	v_mfma_scale_f32_16x16x128_f8f6f4 v[142:145], v[122:127], v[62:67], v[142:145], v179, v115 op_sel_hi:[0,0,0] cbsz:2 blgp:2
	s_waitcnt lgkmcnt(0)
	v_mfma_scale_f32_16x16x128_f8f6f4 v[134:137], v[128:133], v[8:13], v[134:137], v178, v115 op_sel_hi:[0,0,0] cbsz:2 blgp:2
	v_mfma_scale_f32_16x16x128_f8f6f4 v[134:137], v[128:133], v[44:49], v[134:137], v179, v115 op_sel_hi:[0,0,0] cbsz:2 blgp:2
	v_mfma_scale_f32_16x16x128_f8f6f4 v[138:141], v[128:133], v[20:25], v[138:141], v178, v115 op_sel_hi:[0,0,0] cbsz:2 blgp:2
	v_mfma_scale_f32_16x16x128_f8f6f4 v[138:141], v[128:133], v[56:61], v[138:141], v179, v115 op_sel_hi:[0,0,0] cbsz:2 blgp:2
	v_mfma_scale_f32_16x16x128_f8f6f4 v[142:145], v[128:133], v[32:37], v[142:145], v178, v115 op_sel_hi:[0,0,0] cbsz:2 blgp:2
	v_mfma_scale_f32_16x16x128_f8f6f4 v[142:145], v[128:133], v[68:73], v[142:145], v179, v115 op_sel_hi:[0,0,0] cbsz:2 blgp:2
	v_fma_mix_f32 v158, v134, v1, v82 op_sel_hi:[0,0,1]
	v_exp_f32_e32 v158, v158
	v_fma_mix_f32 v159, v138, v99, v74 op_sel_hi:[0,0,1]
	v_exp_f32_e32 v159, v159
	v_add_f32_e32 v158, 1.0, v158
	v_rcp_f32_e32 v158, v158
	v_add_f32_e32 v159, 1.0, v159
	v_rcp_f32_e32 v159, v159
	v_fma_f32 v160, v142, v104, v105
	v_fma_mix_f32 v161, v158, v160, v78 op_sel_hi:[0,0,1]
	v_exp_f32_e32 v161, v161
	s_add_u32 s48, s48, s40
	v_add_f32_e32 v161, 1.0, v161
	v_rcp_f32_e32 v161, v161
	s_addc_u32 s49, s49, s41
	v_fma_f32 v162, v161, -2.0, 1.0
	v_sub_f32_e32 v163, v176, v162
	v_fma_f32 v176, v159, v163, v162
	v_fma_f32 v164, |v176|, s16, v117
	v_fma_f32 v165, |v176|, s17, v118
	v_fma_f32 v166, |v176|, s18, v119
	v_lshrrev_b32_e32 v167, 26, v176
	v_min3_u32 v164, v164, v165, v166
	v_bfi_b32 v168, 31, v164, v167
	v_lshrrev_b32_e32 v169, v181, v168
	global_store_short_d16_hi v185, v176, s[48:49]
	v_mul_u32_u24_dpp v170, v168, v180 quad_perm:[1,2,3,3] row_mask:0xf bank_mask:0xf bound_ctrl:1
	v_or_b32_e32 v171, v169, v170
	ds_write_b8 v184, v171 offset:416
	s_waitcnt lgkmcnt(0)
	s_barrier
	ds_read_b64 v[122:123], v106 offset:416
	ds_read_b64 v[124:125], v106 offset:424
	ds_read_b64 v[126:127], v106 offset:432
	s_barrier
	ds_read_b64 v[128:129], v106 offset:512
	ds_read_b64 v[130:131], v106 offset:520
	ds_read_b64 v[132:133], v106 offset:528
	s_waitcnt lgkmcnt(3)
	v_mfma_scale_f32_16x16x128_f8f6f4 v[134:137], v[122:127], v[2:7], 0, v178, v115 op_sel_hi:[0,0,0] cbsz:2 blgp:2
	v_mfma_scale_f32_16x16x128_f8f6f4 v[138:141], v[122:127], v[14:19], 0, v178, v115 op_sel_hi:[0,0,0] cbsz:2 blgp:2
	v_mfma_scale_f32_16x16x128_f8f6f4 v[142:145], v[122:127], v[26:31], 0, v178, v115 op_sel_hi:[0,0,0] cbsz:2 blgp:2
	v_mfma_scale_f32_16x16x128_f8f6f4 v[134:137], v[122:127], v[38:43], v[134:137], v179, v115 op_sel_hi:[0,0,0] cbsz:2 blgp:2
	v_mfma_scale_f32_16x16x128_f8f6f4 v[138:141], v[122:127], v[50:55], v[138:141], v179, v115 op_sel_hi:[0,0,0] cbsz:2 blgp:2
	v_mfma_scale_f32_16x16x128_f8f6f4 v[142:145], v[122:127], v[62:67], v[142:145], v179, v115 op_sel_hi:[0,0,0] cbsz:2 blgp:2
	s_waitcnt lgkmcnt(0)
	v_mfma_scale_f32_16x16x128_f8f6f4 v[134:137], v[128:133], v[8:13], v[134:137], v178, v115 op_sel_hi:[0,0,0] cbsz:2 blgp:2
	v_mfma_scale_f32_16x16x128_f8f6f4 v[134:137], v[128:133], v[44:49], v[134:137], v179, v115 op_sel_hi:[0,0,0] cbsz:2 blgp:2
	v_mfma_scale_f32_16x16x128_f8f6f4 v[138:141], v[128:133], v[20:25], v[138:141], v178, v115 op_sel_hi:[0,0,0] cbsz:2 blgp:2
	v_mfma_scale_f32_16x16x128_f8f6f4 v[138:141], v[128:133], v[56:61], v[138:141], v179, v115 op_sel_hi:[0,0,0] cbsz:2 blgp:2
	v_mfma_scale_f32_16x16x128_f8f6f4 v[142:145], v[128:133], v[32:37], v[142:145], v178, v115 op_sel_hi:[0,0,0] cbsz:2 blgp:2
	v_mfma_scale_f32_16x16x128_f8f6f4 v[142:145], v[128:133], v[68:73], v[142:145], v179, v115 op_sel_hi:[0,0,0] cbsz:2 blgp:2
	v_fma_mix_f32 v158, v134, v1, v82 op_sel:[0,0,1] op_sel_hi:[0,0,1]
	v_exp_f32_e32 v158, v158
	v_fma_mix_f32 v159, v138, v99, v74 op_sel:[0,0,1] op_sel_hi:[0,0,1]
	v_exp_f32_e32 v159, v159
	v_add_f32_e32 v158, 1.0, v158
	v_rcp_f32_e32 v158, v158
	v_add_f32_e32 v159, 1.0, v159
	v_rcp_f32_e32 v159, v159
	v_fma_f32 v160, v142, v104, v105
	v_fma_mix_f32 v161, v158, v160, v78 op_sel:[0,0,1] op_sel_hi:[0,0,1]
	v_exp_f32_e32 v161, v161
	s_add_u32 s48, s48, s40
	v_add_f32_e32 v161, 1.0, v161
	v_rcp_f32_e32 v161, v161
	s_addc_u32 s49, s49, s41
	v_fma_f32 v162, v161, -2.0, 1.0
	v_sub_f32_e32 v163, v176, v162
	v_fma_f32 v176, v159, v163, v162
	v_fma_f32 v164, |v176|, s16, v117
	v_fma_f32 v165, |v176|, s17, v118
	v_fma_f32 v166, |v176|, s18, v119
	v_lshrrev_b32_e32 v167, 26, v176
	v_min3_u32 v164, v164, v165, v166
	v_bfi_b32 v168, 31, v164, v167
	v_lshrrev_b32_e32 v169, v181, v168
	global_store_short_d16_hi v185, v176, s[48:49]
	v_mul_u32_u24_dpp v170, v168, v180 quad_perm:[1,2,3,3] row_mask:0xf bank_mask:0xf bound_ctrl:1
	v_or_b32_e32 v171, v169, v170
	ds_write_b8 v184, v171
	s_waitcnt lgkmcnt(0)
	s_barrier
	ds_read_b64 v[122:123], v106 offset:0
	ds_read_b64 v[124:125], v106 offset:8
	ds_read_b64 v[126:127], v106 offset:16
	s_barrier
	ds_read_b64 v[128:129], v106 offset:96
	ds_read_b64 v[130:131], v106 offset:104
	ds_read_b64 v[132:133], v106 offset:112
	s_waitcnt lgkmcnt(3)
	v_mfma_scale_f32_16x16x128_f8f6f4 v[134:137], v[122:127], v[2:7], 0, v178, v115 op_sel_hi:[0,0,0] cbsz:2 blgp:2
	v_mfma_scale_f32_16x16x128_f8f6f4 v[138:141], v[122:127], v[14:19], 0, v178, v115 op_sel_hi:[0,0,0] cbsz:2 blgp:2
	v_mfma_scale_f32_16x16x128_f8f6f4 v[142:145], v[122:127], v[26:31], 0, v178, v115 op_sel_hi:[0,0,0] cbsz:2 blgp:2
	v_mfma_scale_f32_16x16x128_f8f6f4 v[134:137], v[122:127], v[38:43], v[134:137], v179, v115 op_sel_hi:[0,0,0] cbsz:2 blgp:2
	v_mfma_scale_f32_16x16x128_f8f6f4 v[138:141], v[122:127], v[50:55], v[138:141], v179, v115 op_sel_hi:[0,0,0] cbsz:2 blgp:2
	v_mfma_scale_f32_16x16x128_f8f6f4 v[142:145], v[122:127], v[62:67], v[142:145], v179, v115 op_sel_hi:[0,0,0] cbsz:2 blgp:2
	s_waitcnt lgkmcnt(0)
	v_mfma_scale_f32_16x16x128_f8f6f4 v[134:137], v[128:133], v[8:13], v[134:137], v178, v115 op_sel_hi:[0,0,0] cbsz:2 blgp:2
	v_mfma_scale_f32_16x16x128_f8f6f4 v[134:137], v[128:133], v[44:49], v[134:137], v179, v115 op_sel_hi:[0,0,0] cbsz:2 blgp:2
	v_mfma_scale_f32_16x16x128_f8f6f4 v[138:141], v[128:133], v[20:25], v[138:141], v178, v115 op_sel_hi:[0,0,0] cbsz:2 blgp:2
	v_mfma_scale_f32_16x16x128_f8f6f4 v[138:141], v[128:133], v[56:61], v[138:141], v179, v115 op_sel_hi:[0,0,0] cbsz:2 blgp:2
	v_mfma_scale_f32_16x16x128_f8f6f4 v[142:145], v[128:133], v[32:37], v[142:145], v178, v115 op_sel_hi:[0,0,0] cbsz:2 blgp:2
	v_mfma_scale_f32_16x16x128_f8f6f4 v[142:145], v[128:133], v[68:73], v[142:145], v179, v115 op_sel_hi:[0,0,0] cbsz:2 blgp:2
	v_fma_mix_f32 v158, v134, v1, v83 op_sel_hi:[0,0,1]
	v_exp_f32_e32 v158, v158
	v_fma_mix_f32 v159, v138, v99, v75 op_sel_hi:[0,0,1]
	v_exp_f32_e32 v159, v159
	v_add_f32_e32 v158, 1.0, v158
	v_rcp_f32_e32 v158, v158
	v_add_f32_e32 v159, 1.0, v159
	v_rcp_f32_e32 v159, v159
	v_fma_f32 v160, v142, v104, v105
	v_fma_mix_f32 v161, v158, v160, v79 op_sel_hi:[0,0,1]
	v_exp_f32_e32 v161, v161
	s_add_u32 s48, s48, s40
	v_add_f32_e32 v161, 1.0, v161
	v_rcp_f32_e32 v161, v161
	s_addc_u32 s49, s49, s41
	v_fma_f32 v162, v161, -2.0, 1.0
	v_sub_f32_e32 v163, v176, v162
	v_fma_f32 v176, v159, v163, v162
	v_fma_f32 v164, |v176|, s16, v117
	v_fma_f32 v165, |v176|, s17, v118
	v_fma_f32 v166, |v176|, s18, v119
	v_lshrrev_b32_e32 v167, 26, v176
	v_min3_u32 v164, v164, v165, v166
	v_bfi_b32 v168, 31, v164, v167
	v_lshrrev_b32_e32 v169, v181, v168
	global_store_short_d16_hi v185, v176, s[48:49]
	v_mul_u32_u24_dpp v170, v168, v180 quad_perm:[1,2,3,3] row_mask:0xf bank_mask:0xf bound_ctrl:1
	v_or_b32_e32 v171, v169, v170
	ds_write_b8 v184, v171 offset:416
	s_waitcnt lgkmcnt(0)
	s_barrier
	ds_read_b64 v[122:123], v106 offset:416
	ds_read_b64 v[124:125], v106 offset:424
	ds_read_b64 v[126:127], v106 offset:432
	s_barrier
	ds_read_b64 v[128:129], v106 offset:512
	ds_read_b64 v[130:131], v106 offset:520
	ds_read_b64 v[132:133], v106 offset:528
	s_waitcnt lgkmcnt(3)
	v_mfma_scale_f32_16x16x128_f8f6f4 v[134:137], v[122:127], v[2:7], 0, v178, v115 op_sel_hi:[0,0,0] cbsz:2 blgp:2
	v_mfma_scale_f32_16x16x128_f8f6f4 v[138:141], v[122:127], v[14:19], 0, v178, v115 op_sel_hi:[0,0,0] cbsz:2 blgp:2
	v_mfma_scale_f32_16x16x128_f8f6f4 v[142:145], v[122:127], v[26:31], 0, v178, v115 op_sel_hi:[0,0,0] cbsz:2 blgp:2
	v_mfma_scale_f32_16x16x128_f8f6f4 v[134:137], v[122:127], v[38:43], v[134:137], v179, v115 op_sel_hi:[0,0,0] cbsz:2 blgp:2
	v_mfma_scale_f32_16x16x128_f8f6f4 v[138:141], v[122:127], v[50:55], v[138:141], v179, v115 op_sel_hi:[0,0,0] cbsz:2 blgp:2
	v_mfma_scale_f32_16x16x128_f8f6f4 v[142:145], v[122:127], v[62:67], v[142:145], v179, v115 op_sel_hi:[0,0,0] cbsz:2 blgp:2
	s_waitcnt lgkmcnt(0)
	v_mfma_scale_f32_16x16x128_f8f6f4 v[134:137], v[128:133], v[8:13], v[134:137], v178, v115 op_sel_hi:[0,0,0] cbsz:2 blgp:2
	v_mfma_scale_f32_16x16x128_f8f6f4 v[134:137], v[128:133], v[44:49], v[134:137], v179, v115 op_sel_hi:[0,0,0] cbsz:2 blgp:2
	v_mfma_scale_f32_16x16x128_f8f6f4 v[138:141], v[128:133], v[20:25], v[138:141], v178, v115 op_sel_hi:[0,0,0] cbsz:2 blgp:2
	v_mfma_scale_f32_16x16x128_f8f6f4 v[138:141], v[128:133], v[56:61], v[138:141], v179, v115 op_sel_hi:[0,0,0] cbsz:2 blgp:2
	v_mfma_scale_f32_16x16x128_f8f6f4 v[142:145], v[128:133], v[32:37], v[142:145], v178, v115 op_sel_hi:[0,0,0] cbsz:2 blgp:2
	v_mfma_scale_f32_16x16x128_f8f6f4 v[142:145], v[128:133], v[68:73], v[142:145], v179, v115 op_sel_hi:[0,0,0] cbsz:2 blgp:2
	v_fma_mix_f32 v158, v134, v1, v83 op_sel:[0,0,1] op_sel_hi:[0,0,1]
	v_exp_f32_e32 v158, v158
	v_fma_mix_f32 v159, v138, v99, v75 op_sel:[0,0,1] op_sel_hi:[0,0,1]
	v_exp_f32_e32 v159, v159
	v_add_f32_e32 v158, 1.0, v158
	v_rcp_f32_e32 v158, v158
	v_add_f32_e32 v159, 1.0, v159
	v_rcp_f32_e32 v159, v159
	v_fma_f32 v160, v142, v104, v105
	v_fma_mix_f32 v161, v158, v160, v79 op_sel:[0,0,1] op_sel_hi:[0,0,1]
	v_exp_f32_e32 v161, v161
	s_add_u32 s48, s48, s40
	v_add_f32_e32 v161, 1.0, v161
	v_rcp_f32_e32 v161, v161
	s_addc_u32 s49, s49, s41
	v_fma_f32 v162, v161, -2.0, 1.0
	v_sub_f32_e32 v163, v176, v162
	v_fma_f32 v176, v159, v163, v162
	v_fma_f32 v164, |v176|, s16, v117
	v_fma_f32 v165, |v176|, s17, v118
	v_fma_f32 v166, |v176|, s18, v119
	v_lshrrev_b32_e32 v167, 26, v176
	v_min3_u32 v164, v164, v165, v166
	v_bfi_b32 v168, 31, v164, v167
	v_lshrrev_b32_e32 v169, v181, v168
	global_store_short_d16_hi v185, v176, s[48:49]
	v_mul_u32_u24_dpp v170, v168, v180 quad_perm:[1,2,3,3] row_mask:0xf bank_mask:0xf bound_ctrl:1
	v_or_b32_e32 v171, v169, v170
	ds_write_b8 v184, v171
	s_waitcnt lgkmcnt(0)
	s_barrier
	ds_read_b64 v[122:123], v106 offset:0
	ds_read_b64 v[124:125], v106 offset:8
	ds_read_b64 v[126:127], v106 offset:16
	s_barrier
	ds_read_b64 v[128:129], v106 offset:96
	ds_read_b64 v[130:131], v106 offset:104
	ds_read_b64 v[132:133], v106 offset:112
	s_waitcnt lgkmcnt(3)
	v_mfma_scale_f32_16x16x128_f8f6f4 v[134:137], v[122:127], v[2:7], 0, v178, v115 op_sel_hi:[0,0,0] cbsz:2 blgp:2
	v_mfma_scale_f32_16x16x128_f8f6f4 v[138:141], v[122:127], v[14:19], 0, v178, v115 op_sel_hi:[0,0,0] cbsz:2 blgp:2
	v_mfma_scale_f32_16x16x128_f8f6f4 v[142:145], v[122:127], v[26:31], 0, v178, v115 op_sel_hi:[0,0,0] cbsz:2 blgp:2
	v_mfma_scale_f32_16x16x128_f8f6f4 v[134:137], v[122:127], v[38:43], v[134:137], v179, v115 op_sel_hi:[0,0,0] cbsz:2 blgp:2
	v_mfma_scale_f32_16x16x128_f8f6f4 v[138:141], v[122:127], v[50:55], v[138:141], v179, v115 op_sel_hi:[0,0,0] cbsz:2 blgp:2
	v_mfma_scale_f32_16x16x128_f8f6f4 v[142:145], v[122:127], v[62:67], v[142:145], v179, v115 op_sel_hi:[0,0,0] cbsz:2 blgp:2
	s_waitcnt lgkmcnt(0)
	v_mfma_scale_f32_16x16x128_f8f6f4 v[134:137], v[128:133], v[8:13], v[134:137], v178, v115 op_sel_hi:[0,0,0] cbsz:2 blgp:2
	v_mfma_scale_f32_16x16x128_f8f6f4 v[134:137], v[128:133], v[44:49], v[134:137], v179, v115 op_sel_hi:[0,0,0] cbsz:2 blgp:2
	v_mfma_scale_f32_16x16x128_f8f6f4 v[138:141], v[128:133], v[20:25], v[138:141], v178, v115 op_sel_hi:[0,0,0] cbsz:2 blgp:2
	v_mfma_scale_f32_16x16x128_f8f6f4 v[138:141], v[128:133], v[56:61], v[138:141], v179, v115 op_sel_hi:[0,0,0] cbsz:2 blgp:2
	v_mfma_scale_f32_16x16x128_f8f6f4 v[142:145], v[128:133], v[32:37], v[142:145], v178, v115 op_sel_hi:[0,0,0] cbsz:2 blgp:2
	v_mfma_scale_f32_16x16x128_f8f6f4 v[142:145], v[128:133], v[68:73], v[142:145], v179, v115 op_sel_hi:[0,0,0] cbsz:2 blgp:2
	v_fma_mix_f32 v158, v134, v1, v84 op_sel_hi:[0,0,1]
	v_exp_f32_e32 v158, v158
	v_fma_mix_f32 v159, v138, v99, v76 op_sel_hi:[0,0,1]
	v_exp_f32_e32 v159, v159
	v_add_f32_e32 v158, 1.0, v158
	v_rcp_f32_e32 v158, v158
	v_add_f32_e32 v159, 1.0, v159
	v_rcp_f32_e32 v159, v159
	v_fma_f32 v160, v142, v104, v105
	v_fma_mix_f32 v161, v158, v160, v80 op_sel_hi:[0,0,1]
	v_exp_f32_e32 v161, v161
	s_add_u32 s48, s48, s40
	v_add_f32_e32 v161, 1.0, v161
	v_rcp_f32_e32 v161, v161
	s_addc_u32 s49, s49, s41
	v_fma_f32 v162, v161, -2.0, 1.0
	v_sub_f32_e32 v163, v176, v162
	v_fma_f32 v176, v159, v163, v162
	v_fma_f32 v164, |v176|, s16, v117
	v_fma_f32 v165, |v176|, s17, v118
	v_fma_f32 v166, |v176|, s18, v119
	v_lshrrev_b32_e32 v167, 26, v176
	v_min3_u32 v164, v164, v165, v166
	v_bfi_b32 v168, 31, v164, v167
	v_lshrrev_b32_e32 v169, v181, v168
	global_store_short_d16_hi v185, v176, s[48:49]
	v_mul_u32_u24_dpp v170, v168, v180 quad_perm:[1,2,3,3] row_mask:0xf bank_mask:0xf bound_ctrl:1
	v_or_b32_e32 v171, v169, v170
	ds_write_b8 v184, v171 offset:416
	s_waitcnt lgkmcnt(0)
	s_barrier
	ds_read_b64 v[122:123], v106 offset:416
	ds_read_b64 v[124:125], v106 offset:424
	ds_read_b64 v[126:127], v106 offset:432
	s_barrier
	ds_read_b64 v[128:129], v106 offset:512
	ds_read_b64 v[130:131], v106 offset:520
	ds_read_b64 v[132:133], v106 offset:528
	s_waitcnt lgkmcnt(3)
	v_mfma_scale_f32_16x16x128_f8f6f4 v[134:137], v[122:127], v[2:7], 0, v178, v115 op_sel_hi:[0,0,0] cbsz:2 blgp:2
	v_mfma_scale_f32_16x16x128_f8f6f4 v[138:141], v[122:127], v[14:19], 0, v178, v115 op_sel_hi:[0,0,0] cbsz:2 blgp:2
	v_mfma_scale_f32_16x16x128_f8f6f4 v[142:145], v[122:127], v[26:31], 0, v178, v115 op_sel_hi:[0,0,0] cbsz:2 blgp:2
	v_mfma_scale_f32_16x16x128_f8f6f4 v[134:137], v[122:127], v[38:43], v[134:137], v179, v115 op_sel_hi:[0,0,0] cbsz:2 blgp:2
	v_mfma_scale_f32_16x16x128_f8f6f4 v[138:141], v[122:127], v[50:55], v[138:141], v179, v115 op_sel_hi:[0,0,0] cbsz:2 blgp:2
	v_mfma_scale_f32_16x16x128_f8f6f4 v[142:145], v[122:127], v[62:67], v[142:145], v179, v115 op_sel_hi:[0,0,0] cbsz:2 blgp:2
	s_waitcnt lgkmcnt(0)
	v_mfma_scale_f32_16x16x128_f8f6f4 v[134:137], v[128:133], v[8:13], v[134:137], v178, v115 op_sel_hi:[0,0,0] cbsz:2 blgp:2
	v_mfma_scale_f32_16x16x128_f8f6f4 v[134:137], v[128:133], v[44:49], v[134:137], v179, v115 op_sel_hi:[0,0,0] cbsz:2 blgp:2
	v_mfma_scale_f32_16x16x128_f8f6f4 v[138:141], v[128:133], v[20:25], v[138:141], v178, v115 op_sel_hi:[0,0,0] cbsz:2 blgp:2
	v_mfma_scale_f32_16x16x128_f8f6f4 v[138:141], v[128:133], v[56:61], v[138:141], v179, v115 op_sel_hi:[0,0,0] cbsz:2 blgp:2
	v_mfma_scale_f32_16x16x128_f8f6f4 v[142:145], v[128:133], v[32:37], v[142:145], v178, v115 op_sel_hi:[0,0,0] cbsz:2 blgp:2
	v_mfma_scale_f32_16x16x128_f8f6f4 v[142:145], v[128:133], v[68:73], v[142:145], v179, v115 op_sel_hi:[0,0,0] cbsz:2 blgp:2
	v_fma_mix_f32 v158, v134, v1, v84 op_sel:[0,0,1] op_sel_hi:[0,0,1]
	v_exp_f32_e32 v158, v158
	v_fma_mix_f32 v159, v138, v99, v76 op_sel:[0,0,1] op_sel_hi:[0,0,1]
	v_exp_f32_e32 v159, v159
	v_add_f32_e32 v158, 1.0, v158
	v_rcp_f32_e32 v158, v158
	v_add_f32_e32 v159, 1.0, v159
	v_rcp_f32_e32 v159, v159
	v_fma_f32 v160, v142, v104, v105
	v_fma_mix_f32 v161, v158, v160, v80 op_sel:[0,0,1] op_sel_hi:[0,0,1]
	v_exp_f32_e32 v161, v161
	s_add_u32 s48, s48, s40
	v_add_f32_e32 v161, 1.0, v161
	v_rcp_f32_e32 v161, v161
	s_addc_u32 s49, s49, s41
	v_fma_f32 v162, v161, -2.0, 1.0
	v_sub_f32_e32 v163, v176, v162
	v_fma_f32 v176, v159, v163, v162
	v_fma_f32 v164, |v176|, s16, v117
	v_fma_f32 v165, |v176|, s17, v118
	v_fma_f32 v166, |v176|, s18, v119
	v_lshrrev_b32_e32 v167, 26, v176
	v_min3_u32 v164, v164, v165, v166
	v_bfi_b32 v168, 31, v164, v167
	v_lshrrev_b32_e32 v169, v181, v168
	global_store_short_d16_hi v185, v176, s[48:49]
	v_mul_u32_u24_dpp v170, v168, v180 quad_perm:[1,2,3,3] row_mask:0xf bank_mask:0xf bound_ctrl:1
	v_or_b32_e32 v171, v169, v170
	ds_write_b8 v184, v171
	s_waitcnt lgkmcnt(0)
	s_barrier
	ds_read_b64 v[122:123], v106 offset:0
	ds_read_b64 v[124:125], v106 offset:8
	ds_read_b64 v[126:127], v106 offset:16
	s_barrier
	ds_read_b64 v[128:129], v106 offset:96
	ds_read_b64 v[130:131], v106 offset:104
	ds_read_b64 v[132:133], v106 offset:112
	s_waitcnt lgkmcnt(3)
	v_mfma_scale_f32_16x16x128_f8f6f4 v[134:137], v[122:127], v[2:7], 0, v178, v115 op_sel_hi:[0,0,0] cbsz:2 blgp:2
	v_mfma_scale_f32_16x16x128_f8f6f4 v[138:141], v[122:127], v[14:19], 0, v178, v115 op_sel_hi:[0,0,0] cbsz:2 blgp:2
	v_mfma_scale_f32_16x16x128_f8f6f4 v[142:145], v[122:127], v[26:31], 0, v178, v115 op_sel_hi:[0,0,0] cbsz:2 blgp:2
	v_mfma_scale_f32_16x16x128_f8f6f4 v[134:137], v[122:127], v[38:43], v[134:137], v179, v115 op_sel_hi:[0,0,0] cbsz:2 blgp:2
	v_mfma_scale_f32_16x16x128_f8f6f4 v[138:141], v[122:127], v[50:55], v[138:141], v179, v115 op_sel_hi:[0,0,0] cbsz:2 blgp:2
	v_mfma_scale_f32_16x16x128_f8f6f4 v[142:145], v[122:127], v[62:67], v[142:145], v179, v115 op_sel_hi:[0,0,0] cbsz:2 blgp:2
	s_waitcnt lgkmcnt(0)
	v_mfma_scale_f32_16x16x128_f8f6f4 v[134:137], v[128:133], v[8:13], v[134:137], v178, v115 op_sel_hi:[0,0,0] cbsz:2 blgp:2
	v_mfma_scale_f32_16x16x128_f8f6f4 v[134:137], v[128:133], v[44:49], v[134:137], v179, v115 op_sel_hi:[0,0,0] cbsz:2 blgp:2
	v_mfma_scale_f32_16x16x128_f8f6f4 v[138:141], v[128:133], v[20:25], v[138:141], v178, v115 op_sel_hi:[0,0,0] cbsz:2 blgp:2
	v_mfma_scale_f32_16x16x128_f8f6f4 v[138:141], v[128:133], v[56:61], v[138:141], v179, v115 op_sel_hi:[0,0,0] cbsz:2 blgp:2
	v_mfma_scale_f32_16x16x128_f8f6f4 v[142:145], v[128:133], v[32:37], v[142:145], v178, v115 op_sel_hi:[0,0,0] cbsz:2 blgp:2
	v_mfma_scale_f32_16x16x128_f8f6f4 v[142:145], v[128:133], v[68:73], v[142:145], v179, v115 op_sel_hi:[0,0,0] cbsz:2 blgp:2
	v_fma_mix_f32 v158, v134, v1, v85 op_sel_hi:[0,0,1]
	v_exp_f32_e32 v158, v158
	v_fma_mix_f32 v159, v138, v99, v77 op_sel_hi:[0,0,1]
	v_exp_f32_e32 v159, v159
	v_add_f32_e32 v158, 1.0, v158
	v_rcp_f32_e32 v158, v158
	v_add_f32_e32 v159, 1.0, v159
	v_rcp_f32_e32 v159, v159
	v_fma_f32 v160, v142, v104, v105
	v_fma_mix_f32 v161, v158, v160, v81 op_sel_hi:[0,0,1]
	v_exp_f32_e32 v161, v161
	s_add_u32 s48, s48, s40
	v_add_f32_e32 v161, 1.0, v161
	v_rcp_f32_e32 v161, v161
	s_addc_u32 s49, s49, s41
	v_fma_f32 v162, v161, -2.0, 1.0
	v_sub_f32_e32 v163, v176, v162
	v_fma_f32 v176, v159, v163, v162
	v_fma_f32 v164, |v176|, s16, v117
	v_fma_f32 v165, |v176|, s17, v118
	v_fma_f32 v166, |v176|, s18, v119
	v_lshrrev_b32_e32 v167, 26, v176
	v_min3_u32 v164, v164, v165, v166
	v_bfi_b32 v168, 31, v164, v167
	v_lshrrev_b32_e32 v169, v181, v168
	global_store_short_d16_hi v185, v176, s[48:49]
	v_mul_u32_u24_dpp v170, v168, v180 quad_perm:[1,2,3,3] row_mask:0xf bank_mask:0xf bound_ctrl:1
	v_or_b32_e32 v171, v169, v170
	ds_write_b8 v184, v171 offset:416
	s_waitcnt lgkmcnt(0)
	s_barrier
	ds_read_b64 v[122:123], v106 offset:416
	ds_read_b64 v[124:125], v106 offset:424
	ds_read_b64 v[126:127], v106 offset:432
	s_barrier
	ds_read_b64 v[128:129], v106 offset:512
	ds_read_b64 v[130:131], v106 offset:520
	ds_read_b64 v[132:133], v106 offset:528
	s_waitcnt lgkmcnt(3)
	v_mfma_scale_f32_16x16x128_f8f6f4 v[134:137], v[122:127], v[2:7], 0, v178, v115 op_sel_hi:[0,0,0] cbsz:2 blgp:2
	v_mfma_scale_f32_16x16x128_f8f6f4 v[138:141], v[122:127], v[14:19], 0, v178, v115 op_sel_hi:[0,0,0] cbsz:2 blgp:2
	v_mfma_scale_f32_16x16x128_f8f6f4 v[142:145], v[122:127], v[26:31], 0, v178, v115 op_sel_hi:[0,0,0] cbsz:2 blgp:2
	v_mfma_scale_f32_16x16x128_f8f6f4 v[134:137], v[122:127], v[38:43], v[134:137], v179, v115 op_sel_hi:[0,0,0] cbsz:2 blgp:2
	v_mfma_scale_f32_16x16x128_f8f6f4 v[138:141], v[122:127], v[50:55], v[138:141], v179, v115 op_sel_hi:[0,0,0] cbsz:2 blgp:2
	v_mfma_scale_f32_16x16x128_f8f6f4 v[142:145], v[122:127], v[62:67], v[142:145], v179, v115 op_sel_hi:[0,0,0] cbsz:2 blgp:2
	s_waitcnt lgkmcnt(0)
	v_mfma_scale_f32_16x16x128_f8f6f4 v[134:137], v[128:133], v[8:13], v[134:137], v178, v115 op_sel_hi:[0,0,0] cbsz:2 blgp:2
	v_mfma_scale_f32_16x16x128_f8f6f4 v[134:137], v[128:133], v[44:49], v[134:137], v179, v115 op_sel_hi:[0,0,0] cbsz:2 blgp:2
	v_mfma_scale_f32_16x16x128_f8f6f4 v[138:141], v[128:133], v[20:25], v[138:141], v178, v115 op_sel_hi:[0,0,0] cbsz:2 blgp:2
	v_mfma_scale_f32_16x16x128_f8f6f4 v[138:141], v[128:133], v[56:61], v[138:141], v179, v115 op_sel_hi:[0,0,0] cbsz:2 blgp:2
	v_mfma_scale_f32_16x16x128_f8f6f4 v[142:145], v[128:133], v[32:37], v[142:145], v178, v115 op_sel_hi:[0,0,0] cbsz:2 blgp:2
	v_mfma_scale_f32_16x16x128_f8f6f4 v[142:145], v[128:133], v[68:73], v[142:145], v179, v115 op_sel_hi:[0,0,0] cbsz:2 blgp:2
	v_fma_mix_f32 v158, v134, v1, v85 op_sel:[0,0,1] op_sel_hi:[0,0,1]
	v_exp_f32_e32 v158, v158
	v_fma_mix_f32 v159, v138, v99, v77 op_sel:[0,0,1] op_sel_hi:[0,0,1]
	v_exp_f32_e32 v159, v159
	v_add_f32_e32 v158, 1.0, v158
	v_rcp_f32_e32 v158, v158
	v_add_f32_e32 v159, 1.0, v159
	v_rcp_f32_e32 v159, v159
	v_fma_f32 v160, v142, v104, v105
	v_fma_mix_f32 v161, v158, v160, v81 op_sel:[0,0,1] op_sel_hi:[0,0,1]
	v_exp_f32_e32 v161, v161
	s_add_u32 s48, s48, s40
	v_add_f32_e32 v161, 1.0, v161
	v_rcp_f32_e32 v161, v161
	s_addc_u32 s49, s49, s41
	v_fma_f32 v162, v161, -2.0, 1.0
	v_sub_f32_e32 v163, v176, v162
	v_fma_f32 v176, v159, v163, v162
	v_fma_f32 v164, |v176|, s16, v117
	v_fma_f32 v165, |v176|, s17, v118
	v_fma_f32 v166, |v176|, s18, v119
	v_lshrrev_b32_e32 v167, 26, v176
	v_min3_u32 v164, v164, v165, v166
	v_bfi_b32 v168, 31, v164, v167
	v_lshrrev_b32_e32 v169, v181, v168
	global_store_short_d16_hi v185, v176, s[48:49]
	v_mul_u32_u24_dpp v170, v168, v180 quad_perm:[1,2,3,3] row_mask:0xf bank_mask:0xf bound_ctrl:1
	v_or_b32_e32 v171, v169, v170
	ds_write_b8 v184, v171
	s_waitcnt lgkmcnt(0)
	s_barrier
	ds_read_b64 v[122:123], v106 offset:0
	ds_read_b64 v[124:125], v106 offset:8
	ds_read_b64 v[126:127], v106 offset:16
	s_barrier
	ds_read_b64 v[128:129], v106 offset:96
	ds_read_b64 v[130:131], v106 offset:104
	ds_read_b64 v[132:133], v106 offset:112
	s_waitcnt vmcnt(8)
	global_load_dwordx4 v[82:85], v[196:197], off
	global_load_dwordx4 v[74:77], v[196:197], off offset:512
	global_load_dwordx4 v[78:81], v[196:197], off offset:1024
	v_lshl_add_u64 v[196:197], v[196:197], 0, s[42:43]
	s_waitcnt lgkmcnt(3)
	v_mfma_scale_f32_16x16x128_f8f6f4 v[134:137], v[122:127], v[2:7], 0, v178, v115 op_sel_hi:[0,0,0] cbsz:2 blgp:2
	v_mfma_scale_f32_16x16x128_f8f6f4 v[138:141], v[122:127], v[14:19], 0, v178, v115 op_sel_hi:[0,0,0] cbsz:2 blgp:2
	v_mfma_scale_f32_16x16x128_f8f6f4 v[142:145], v[122:127], v[26:31], 0, v178, v115 op_sel_hi:[0,0,0] cbsz:2 blgp:2
	v_mfma_scale_f32_16x16x128_f8f6f4 v[134:137], v[122:127], v[38:43], v[134:137], v179, v115 op_sel_hi:[0,0,0] cbsz:2 blgp:2
	v_mfma_scale_f32_16x16x128_f8f6f4 v[138:141], v[122:127], v[50:55], v[138:141], v179, v115 op_sel_hi:[0,0,0] cbsz:2 blgp:2
	v_mfma_scale_f32_16x16x128_f8f6f4 v[142:145], v[122:127], v[62:67], v[142:145], v179, v115 op_sel_hi:[0,0,0] cbsz:2 blgp:2
	s_waitcnt lgkmcnt(0)
	v_mfma_scale_f32_16x16x128_f8f6f4 v[134:137], v[128:133], v[8:13], v[134:137], v178, v115 op_sel_hi:[0,0,0] cbsz:2 blgp:2
	v_mfma_scale_f32_16x16x128_f8f6f4 v[134:137], v[128:133], v[44:49], v[134:137], v179, v115 op_sel_hi:[0,0,0] cbsz:2 blgp:2
	v_mfma_scale_f32_16x16x128_f8f6f4 v[138:141], v[128:133], v[20:25], v[138:141], v178, v115 op_sel_hi:[0,0,0] cbsz:2 blgp:2
	v_mfma_scale_f32_16x16x128_f8f6f4 v[138:141], v[128:133], v[56:61], v[138:141], v179, v115 op_sel_hi:[0,0,0] cbsz:2 blgp:2
	v_mfma_scale_f32_16x16x128_f8f6f4 v[142:145], v[128:133], v[32:37], v[142:145], v178, v115 op_sel_hi:[0,0,0] cbsz:2 blgp:2
	v_mfma_scale_f32_16x16x128_f8f6f4 v[142:145], v[128:133], v[68:73], v[142:145], v179, v115 op_sel_hi:[0,0,0] cbsz:2 blgp:2
	v_fma_mix_f32 v158, v134, v1, v146 op_sel_hi:[0,0,1]
	v_exp_f32_e32 v158, v158
	v_fma_mix_f32 v159, v138, v99, v150 op_sel_hi:[0,0,1]
	v_exp_f32_e32 v159, v159
	v_add_f32_e32 v158, 1.0, v158
	v_rcp_f32_e32 v158, v158
	v_add_f32_e32 v159, 1.0, v159
	v_rcp_f32_e32 v159, v159
	v_fma_f32 v160, v142, v104, v105
	v_fma_mix_f32 v161, v158, v160, v154 op_sel_hi:[0,0,1]
	v_exp_f32_e32 v161, v161
	s_add_u32 s48, s48, s40
	v_add_f32_e32 v161, 1.0, v161
	v_rcp_f32_e32 v161, v161
	s_addc_u32 s49, s49, s41
	v_fma_f32 v162, v161, -2.0, 1.0
	v_sub_f32_e32 v163, v176, v162
	v_fma_f32 v176, v159, v163, v162
	v_fma_f32 v164, |v176|, s16, v117
	v_fma_f32 v165, |v176|, s17, v118
	v_fma_f32 v166, |v176|, s18, v119
	v_lshrrev_b32_e32 v167, 26, v176
	v_min3_u32 v164, v164, v165, v166
	v_bfi_b32 v168, 31, v164, v167
	v_lshrrev_b32_e32 v169, v181, v168
	global_store_short_d16_hi v185, v176, s[48:49]
	v_mul_u32_u24_dpp v170, v168, v180 quad_perm:[1,2,3,3] row_mask:0xf bank_mask:0xf bound_ctrl:1
	v_or_b32_e32 v171, v169, v170
	ds_write_b8 v184, v171 offset:416
	s_waitcnt lgkmcnt(0)
	s_barrier
	ds_read_b64 v[122:123], v106 offset:416
	ds_read_b64 v[124:125], v106 offset:424
	ds_read_b64 v[126:127], v106 offset:432
	s_barrier
	ds_read_b64 v[128:129], v106 offset:512
	ds_read_b64 v[130:131], v106 offset:520
	ds_read_b64 v[132:133], v106 offset:528
	s_waitcnt lgkmcnt(3)
	v_mfma_scale_f32_16x16x128_f8f6f4 v[134:137], v[122:127], v[2:7], 0, v178, v115 op_sel_hi:[0,0,0] cbsz:2 blgp:2
	v_mfma_scale_f32_16x16x128_f8f6f4 v[138:141], v[122:127], v[14:19], 0, v178, v115 op_sel_hi:[0,0,0] cbsz:2 blgp:2
	v_mfma_scale_f32_16x16x128_f8f6f4 v[142:145], v[122:127], v[26:31], 0, v178, v115 op_sel_hi:[0,0,0] cbsz:2 blgp:2
	v_mfma_scale_f32_16x16x128_f8f6f4 v[134:137], v[122:127], v[38:43], v[134:137], v179, v115 op_sel_hi:[0,0,0] cbsz:2 blgp:2
	v_mfma_scale_f32_16x16x128_f8f6f4 v[138:141], v[122:127], v[50:55], v[138:141], v179, v115 op_sel_hi:[0,0,0] cbsz:2 blgp:2
	v_mfma_scale_f32_16x16x128_f8f6f4 v[142:145], v[122:127], v[62:67], v[142:145], v179, v115 op_sel_hi:[0,0,0] cbsz:2 blgp:2
	s_waitcnt lgkmcnt(0)
	v_mfma_scale_f32_16x16x128_f8f6f4 v[134:137], v[128:133], v[8:13], v[134:137], v178, v115 op_sel_hi:[0,0,0] cbsz:2 blgp:2
	v_mfma_scale_f32_16x16x128_f8f6f4 v[134:137], v[128:133], v[44:49], v[134:137], v179, v115 op_sel_hi:[0,0,0] cbsz:2 blgp:2
	v_mfma_scale_f32_16x16x128_f8f6f4 v[138:141], v[128:133], v[20:25], v[138:141], v178, v115 op_sel_hi:[0,0,0] cbsz:2 blgp:2
	v_mfma_scale_f32_16x16x128_f8f6f4 v[138:141], v[128:133], v[56:61], v[138:141], v179, v115 op_sel_hi:[0,0,0] cbsz:2 blgp:2
	v_mfma_scale_f32_16x16x128_f8f6f4 v[142:145], v[128:133], v[32:37], v[142:145], v178, v115 op_sel_hi:[0,0,0] cbsz:2 blgp:2
	v_mfma_scale_f32_16x16x128_f8f6f4 v[142:145], v[128:133], v[68:73], v[142:145], v179, v115 op_sel_hi:[0,0,0] cbsz:2 blgp:2
	v_fma_mix_f32 v158, v134, v1, v146 op_sel:[0,0,1] op_sel_hi:[0,0,1]
	v_exp_f32_e32 v158, v158
	v_fma_mix_f32 v159, v138, v99, v150 op_sel:[0,0,1] op_sel_hi:[0,0,1]
	v_exp_f32_e32 v159, v159
	v_add_f32_e32 v158, 1.0, v158
	v_rcp_f32_e32 v158, v158
	v_add_f32_e32 v159, 1.0, v159
	v_rcp_f32_e32 v159, v159
	v_fma_f32 v160, v142, v104, v105
	v_fma_mix_f32 v161, v158, v160, v154 op_sel:[0,0,1] op_sel_hi:[0,0,1]
	v_exp_f32_e32 v161, v161
	s_add_u32 s48, s48, s40
	v_add_f32_e32 v161, 1.0, v161
	v_rcp_f32_e32 v161, v161
	s_addc_u32 s49, s49, s41
	v_fma_f32 v162, v161, -2.0, 1.0
	v_sub_f32_e32 v163, v176, v162
	v_fma_f32 v176, v159, v163, v162
	v_fma_f32 v164, |v176|, s16, v117
	v_fma_f32 v165, |v176|, s17, v118
	v_fma_f32 v166, |v176|, s18, v119
	v_lshrrev_b32_e32 v167, 26, v176
	v_min3_u32 v164, v164, v165, v166
	v_bfi_b32 v168, 31, v164, v167
	v_lshrrev_b32_e32 v169, v181, v168
	global_store_short_d16_hi v185, v176, s[48:49]
	v_mul_u32_u24_dpp v170, v168, v180 quad_perm:[1,2,3,3] row_mask:0xf bank_mask:0xf bound_ctrl:1
	v_or_b32_e32 v171, v169, v170
	ds_write_b8 v184, v171
	s_waitcnt lgkmcnt(0)
	s_barrier
	ds_read_b64 v[122:123], v106 offset:0
	ds_read_b64 v[124:125], v106 offset:8
	ds_read_b64 v[126:127], v106 offset:16
	s_barrier
	ds_read_b64 v[128:129], v106 offset:96
	ds_read_b64 v[130:131], v106 offset:104
	ds_read_b64 v[132:133], v106 offset:112
	s_waitcnt lgkmcnt(3)
	v_mfma_scale_f32_16x16x128_f8f6f4 v[134:137], v[122:127], v[2:7], 0, v178, v115 op_sel_hi:[0,0,0] cbsz:2 blgp:2
	v_mfma_scale_f32_16x16x128_f8f6f4 v[138:141], v[122:127], v[14:19], 0, v178, v115 op_sel_hi:[0,0,0] cbsz:2 blgp:2
	v_mfma_scale_f32_16x16x128_f8f6f4 v[142:145], v[122:127], v[26:31], 0, v178, v115 op_sel_hi:[0,0,0] cbsz:2 blgp:2
	v_mfma_scale_f32_16x16x128_f8f6f4 v[134:137], v[122:127], v[38:43], v[134:137], v179, v115 op_sel_hi:[0,0,0] cbsz:2 blgp:2
	v_mfma_scale_f32_16x16x128_f8f6f4 v[138:141], v[122:127], v[50:55], v[138:141], v179, v115 op_sel_hi:[0,0,0] cbsz:2 blgp:2
	v_mfma_scale_f32_16x16x128_f8f6f4 v[142:145], v[122:127], v[62:67], v[142:145], v179, v115 op_sel_hi:[0,0,0] cbsz:2 blgp:2
	s_waitcnt lgkmcnt(0)
	v_mfma_scale_f32_16x16x128_f8f6f4 v[134:137], v[128:133], v[8:13], v[134:137], v178, v115 op_sel_hi:[0,0,0] cbsz:2 blgp:2
	v_mfma_scale_f32_16x16x128_f8f6f4 v[134:137], v[128:133], v[44:49], v[134:137], v179, v115 op_sel_hi:[0,0,0] cbsz:2 blgp:2
	v_mfma_scale_f32_16x16x128_f8f6f4 v[138:141], v[128:133], v[20:25], v[138:141], v178, v115 op_sel_hi:[0,0,0] cbsz:2 blgp:2
	v_mfma_scale_f32_16x16x128_f8f6f4 v[138:141], v[128:133], v[56:61], v[138:141], v179, v115 op_sel_hi:[0,0,0] cbsz:2 blgp:2
	v_mfma_scale_f32_16x16x128_f8f6f4 v[142:145], v[128:133], v[32:37], v[142:145], v178, v115 op_sel_hi:[0,0,0] cbsz:2 blgp:2
	v_mfma_scale_f32_16x16x128_f8f6f4 v[142:145], v[128:133], v[68:73], v[142:145], v179, v115 op_sel_hi:[0,0,0] cbsz:2 blgp:2
	v_fma_mix_f32 v158, v134, v1, v147 op_sel_hi:[0,0,1]
	v_exp_f32_e32 v158, v158
	v_fma_mix_f32 v159, v138, v99, v151 op_sel_hi:[0,0,1]
	v_exp_f32_e32 v159, v159
	v_add_f32_e32 v158, 1.0, v158
	v_rcp_f32_e32 v158, v158
	v_add_f32_e32 v159, 1.0, v159
	v_rcp_f32_e32 v159, v159
	v_fma_f32 v160, v142, v104, v105
	v_fma_mix_f32 v161, v158, v160, v155 op_sel_hi:[0,0,1]
	v_exp_f32_e32 v161, v161
	s_add_u32 s48, s48, s40
	v_add_f32_e32 v161, 1.0, v161
	v_rcp_f32_e32 v161, v161
	s_addc_u32 s49, s49, s41
	v_fma_f32 v162, v161, -2.0, 1.0
	v_sub_f32_e32 v163, v176, v162
	v_fma_f32 v176, v159, v163, v162
	v_fma_f32 v164, |v176|, s16, v117
	v_fma_f32 v165, |v176|, s17, v118
	v_fma_f32 v166, |v176|, s18, v119
	v_lshrrev_b32_e32 v167, 26, v176
	v_min3_u32 v164, v164, v165, v166
	v_bfi_b32 v168, 31, v164, v167
	v_lshrrev_b32_e32 v169, v181, v168
	global_store_short_d16_hi v185, v176, s[48:49]
	v_mul_u32_u24_dpp v170, v168, v180 quad_perm:[1,2,3,3] row_mask:0xf bank_mask:0xf bound_ctrl:1
	v_or_b32_e32 v171, v169, v170
	ds_write_b8 v184, v171 offset:416
	s_waitcnt lgkmcnt(0)
	s_barrier
	ds_read_b64 v[122:123], v106 offset:416
	ds_read_b64 v[124:125], v106 offset:424
	ds_read_b64 v[126:127], v106 offset:432
	s_barrier
	ds_read_b64 v[128:129], v106 offset:512
	ds_read_b64 v[130:131], v106 offset:520
	ds_read_b64 v[132:133], v106 offset:528
	s_waitcnt lgkmcnt(3)
	v_mfma_scale_f32_16x16x128_f8f6f4 v[134:137], v[122:127], v[2:7], 0, v178, v115 op_sel_hi:[0,0,0] cbsz:2 blgp:2
	v_mfma_scale_f32_16x16x128_f8f6f4 v[138:141], v[122:127], v[14:19], 0, v178, v115 op_sel_hi:[0,0,0] cbsz:2 blgp:2
	v_mfma_scale_f32_16x16x128_f8f6f4 v[142:145], v[122:127], v[26:31], 0, v178, v115 op_sel_hi:[0,0,0] cbsz:2 blgp:2
	v_mfma_scale_f32_16x16x128_f8f6f4 v[134:137], v[122:127], v[38:43], v[134:137], v179, v115 op_sel_hi:[0,0,0] cbsz:2 blgp:2
	v_mfma_scale_f32_16x16x128_f8f6f4 v[138:141], v[122:127], v[50:55], v[138:141], v179, v115 op_sel_hi:[0,0,0] cbsz:2 blgp:2
	v_mfma_scale_f32_16x16x128_f8f6f4 v[142:145], v[122:127], v[62:67], v[142:145], v179, v115 op_sel_hi:[0,0,0] cbsz:2 blgp:2
	s_waitcnt lgkmcnt(0)
	v_mfma_scale_f32_16x16x128_f8f6f4 v[134:137], v[128:133], v[8:13], v[134:137], v178, v115 op_sel_hi:[0,0,0] cbsz:2 blgp:2
	v_mfma_scale_f32_16x16x128_f8f6f4 v[134:137], v[128:133], v[44:49], v[134:137], v179, v115 op_sel_hi:[0,0,0] cbsz:2 blgp:2
	v_mfma_scale_f32_16x16x128_f8f6f4 v[138:141], v[128:133], v[20:25], v[138:141], v178, v115 op_sel_hi:[0,0,0] cbsz:2 blgp:2
	v_mfma_scale_f32_16x16x128_f8f6f4 v[138:141], v[128:133], v[56:61], v[138:141], v179, v115 op_sel_hi:[0,0,0] cbsz:2 blgp:2
	v_mfma_scale_f32_16x16x128_f8f6f4 v[142:145], v[128:133], v[32:37], v[142:145], v178, v115 op_sel_hi:[0,0,0] cbsz:2 blgp:2
	v_mfma_scale_f32_16x16x128_f8f6f4 v[142:145], v[128:133], v[68:73], v[142:145], v179, v115 op_sel_hi:[0,0,0] cbsz:2 blgp:2
	v_fma_mix_f32 v158, v134, v1, v147 op_sel:[0,0,1] op_sel_hi:[0,0,1]
	v_exp_f32_e32 v158, v158
	v_fma_mix_f32 v159, v138, v99, v151 op_sel:[0,0,1] op_sel_hi:[0,0,1]
	v_exp_f32_e32 v159, v159
	v_add_f32_e32 v158, 1.0, v158
	v_rcp_f32_e32 v158, v158
	v_add_f32_e32 v159, 1.0, v159
	v_rcp_f32_e32 v159, v159
	v_fma_f32 v160, v142, v104, v105
	v_fma_mix_f32 v161, v158, v160, v155 op_sel:[0,0,1] op_sel_hi:[0,0,1]
	v_exp_f32_e32 v161, v161
	s_add_u32 s48, s48, s40
	v_add_f32_e32 v161, 1.0, v161
	v_rcp_f32_e32 v161, v161
	s_addc_u32 s49, s49, s41
	v_fma_f32 v162, v161, -2.0, 1.0
	v_sub_f32_e32 v163, v176, v162
	v_fma_f32 v176, v159, v163, v162
	v_fma_f32 v164, |v176|, s16, v117
	v_fma_f32 v165, |v176|, s17, v118
	v_fma_f32 v166, |v176|, s18, v119
	v_lshrrev_b32_e32 v167, 26, v176
	v_min3_u32 v164, v164, v165, v166
	v_bfi_b32 v168, 31, v164, v167
	v_lshrrev_b32_e32 v169, v181, v168
	global_store_short_d16_hi v185, v176, s[48:49]
	v_mul_u32_u24_dpp v170, v168, v180 quad_perm:[1,2,3,3] row_mask:0xf bank_mask:0xf bound_ctrl:1
	v_or_b32_e32 v171, v169, v170
	ds_write_b8 v184, v171
	s_waitcnt lgkmcnt(0)
	s_barrier
	ds_read_b64 v[122:123], v106 offset:0
	ds_read_b64 v[124:125], v106 offset:8
	ds_read_b64 v[126:127], v106 offset:16
	s_barrier
	ds_read_b64 v[128:129], v106 offset:96
	ds_read_b64 v[130:131], v106 offset:104
	ds_read_b64 v[132:133], v106 offset:112
	s_waitcnt lgkmcnt(3)
	v_mfma_scale_f32_16x16x128_f8f6f4 v[134:137], v[122:127], v[2:7], 0, v178, v115 op_sel_hi:[0,0,0] cbsz:2 blgp:2
	v_mfma_scale_f32_16x16x128_f8f6f4 v[138:141], v[122:127], v[14:19], 0, v178, v115 op_sel_hi:[0,0,0] cbsz:2 blgp:2
	v_mfma_scale_f32_16x16x128_f8f6f4 v[142:145], v[122:127], v[26:31], 0, v178, v115 op_sel_hi:[0,0,0] cbsz:2 blgp:2
	v_mfma_scale_f32_16x16x128_f8f6f4 v[134:137], v[122:127], v[38:43], v[134:137], v179, v115 op_sel_hi:[0,0,0] cbsz:2 blgp:2
	v_mfma_scale_f32_16x16x128_f8f6f4 v[138:141], v[122:127], v[50:55], v[138:141], v179, v115 op_sel_hi:[0,0,0] cbsz:2 blgp:2
	v_mfma_scale_f32_16x16x128_f8f6f4 v[142:145], v[122:127], v[62:67], v[142:145], v179, v115 op_sel_hi:[0,0,0] cbsz:2 blgp:2
	s_waitcnt lgkmcnt(0)
	v_mfma_scale_f32_16x16x128_f8f6f4 v[134:137], v[128:133], v[8:13], v[134:137], v178, v115 op_sel_hi:[0,0,0] cbsz:2 blgp:2
	v_mfma_scale_f32_16x16x128_f8f6f4 v[134:137], v[128:133], v[44:49], v[134:137], v179, v115 op_sel_hi:[0,0,0] cbsz:2 blgp:2
	v_mfma_scale_f32_16x16x128_f8f6f4 v[138:141], v[128:133], v[20:25], v[138:141], v178, v115 op_sel_hi:[0,0,0] cbsz:2 blgp:2
	v_mfma_scale_f32_16x16x128_f8f6f4 v[138:141], v[128:133], v[56:61], v[138:141], v179, v115 op_sel_hi:[0,0,0] cbsz:2 blgp:2
	v_mfma_scale_f32_16x16x128_f8f6f4 v[142:145], v[128:133], v[32:37], v[142:145], v178, v115 op_sel_hi:[0,0,0] cbsz:2 blgp:2
	v_mfma_scale_f32_16x16x128_f8f6f4 v[142:145], v[128:133], v[68:73], v[142:145], v179, v115 op_sel_hi:[0,0,0] cbsz:2 blgp:2
	v_fma_mix_f32 v158, v134, v1, v148 op_sel_hi:[0,0,1]
	v_exp_f32_e32 v158, v158
	v_fma_mix_f32 v159, v138, v99, v152 op_sel_hi:[0,0,1]
	v_exp_f32_e32 v159, v159
	v_add_f32_e32 v158, 1.0, v158
	v_rcp_f32_e32 v158, v158
	v_add_f32_e32 v159, 1.0, v159
	v_rcp_f32_e32 v159, v159
	v_fma_f32 v160, v142, v104, v105
	v_fma_mix_f32 v161, v158, v160, v156 op_sel_hi:[0,0,1]
	v_exp_f32_e32 v161, v161
	s_add_u32 s48, s48, s40
	v_add_f32_e32 v161, 1.0, v161
	v_rcp_f32_e32 v161, v161
	s_addc_u32 s49, s49, s41
	v_fma_f32 v162, v161, -2.0, 1.0
	v_sub_f32_e32 v163, v176, v162
	v_fma_f32 v176, v159, v163, v162
	v_fma_f32 v164, |v176|, s16, v117
	v_fma_f32 v165, |v176|, s17, v118
	v_fma_f32 v166, |v176|, s18, v119
	v_lshrrev_b32_e32 v167, 26, v176
	v_min3_u32 v164, v164, v165, v166
	v_bfi_b32 v168, 31, v164, v167
	v_lshrrev_b32_e32 v169, v181, v168
	global_store_short_d16_hi v185, v176, s[48:49]
	v_mul_u32_u24_dpp v170, v168, v180 quad_perm:[1,2,3,3] row_mask:0xf bank_mask:0xf bound_ctrl:1
	v_or_b32_e32 v171, v169, v170
	ds_write_b8 v184, v171 offset:416
	s_waitcnt lgkmcnt(0)
	s_barrier
	ds_read_b64 v[122:123], v106 offset:416
	ds_read_b64 v[124:125], v106 offset:424
	ds_read_b64 v[126:127], v106 offset:432
	s_barrier
	ds_read_b64 v[128:129], v106 offset:512
	ds_read_b64 v[130:131], v106 offset:520
	ds_read_b64 v[132:133], v106 offset:528
	s_waitcnt lgkmcnt(3)
	v_mfma_scale_f32_16x16x128_f8f6f4 v[134:137], v[122:127], v[2:7], 0, v178, v115 op_sel_hi:[0,0,0] cbsz:2 blgp:2
	v_mfma_scale_f32_16x16x128_f8f6f4 v[138:141], v[122:127], v[14:19], 0, v178, v115 op_sel_hi:[0,0,0] cbsz:2 blgp:2
	v_mfma_scale_f32_16x16x128_f8f6f4 v[142:145], v[122:127], v[26:31], 0, v178, v115 op_sel_hi:[0,0,0] cbsz:2 blgp:2
	v_mfma_scale_f32_16x16x128_f8f6f4 v[134:137], v[122:127], v[38:43], v[134:137], v179, v115 op_sel_hi:[0,0,0] cbsz:2 blgp:2
	v_mfma_scale_f32_16x16x128_f8f6f4 v[138:141], v[122:127], v[50:55], v[138:141], v179, v115 op_sel_hi:[0,0,0] cbsz:2 blgp:2
	v_mfma_scale_f32_16x16x128_f8f6f4 v[142:145], v[122:127], v[62:67], v[142:145], v179, v115 op_sel_hi:[0,0,0] cbsz:2 blgp:2
	s_waitcnt lgkmcnt(0)
	v_mfma_scale_f32_16x16x128_f8f6f4 v[134:137], v[128:133], v[8:13], v[134:137], v178, v115 op_sel_hi:[0,0,0] cbsz:2 blgp:2
	v_mfma_scale_f32_16x16x128_f8f6f4 v[134:137], v[128:133], v[44:49], v[134:137], v179, v115 op_sel_hi:[0,0,0] cbsz:2 blgp:2
	v_mfma_scale_f32_16x16x128_f8f6f4 v[138:141], v[128:133], v[20:25], v[138:141], v178, v115 op_sel_hi:[0,0,0] cbsz:2 blgp:2
	v_mfma_scale_f32_16x16x128_f8f6f4 v[138:141], v[128:133], v[56:61], v[138:141], v179, v115 op_sel_hi:[0,0,0] cbsz:2 blgp:2
	v_mfma_scale_f32_16x16x128_f8f6f4 v[142:145], v[128:133], v[32:37], v[142:145], v178, v115 op_sel_hi:[0,0,0] cbsz:2 blgp:2
	v_mfma_scale_f32_16x16x128_f8f6f4 v[142:145], v[128:133], v[68:73], v[142:145], v179, v115 op_sel_hi:[0,0,0] cbsz:2 blgp:2
	v_fma_mix_f32 v158, v134, v1, v148 op_sel:[0,0,1] op_sel_hi:[0,0,1]
	v_exp_f32_e32 v158, v158
	v_fma_mix_f32 v159, v138, v99, v152 op_sel:[0,0,1] op_sel_hi:[0,0,1]
	v_exp_f32_e32 v159, v159
	v_add_f32_e32 v158, 1.0, v158
	v_rcp_f32_e32 v158, v158
	v_add_f32_e32 v159, 1.0, v159
	v_rcp_f32_e32 v159, v159
	v_fma_f32 v160, v142, v104, v105
	v_fma_mix_f32 v161, v158, v160, v156 op_sel:[0,0,1] op_sel_hi:[0,0,1]
	v_exp_f32_e32 v161, v161
	s_add_u32 s48, s48, s40
	v_add_f32_e32 v161, 1.0, v161
	v_rcp_f32_e32 v161, v161
	s_addc_u32 s49, s49, s41
	v_fma_f32 v162, v161, -2.0, 1.0
	v_sub_f32_e32 v163, v176, v162
	v_fma_f32 v176, v159, v163, v162
	v_fma_f32 v164, |v176|, s16, v117
	v_fma_f32 v165, |v176|, s17, v118
	v_fma_f32 v166, |v176|, s18, v119
	v_lshrrev_b32_e32 v167, 26, v176
	v_min3_u32 v164, v164, v165, v166
	v_bfi_b32 v168, 31, v164, v167
	v_lshrrev_b32_e32 v169, v181, v168
	global_store_short_d16_hi v185, v176, s[48:49]
	v_mul_u32_u24_dpp v170, v168, v180 quad_perm:[1,2,3,3] row_mask:0xf bank_mask:0xf bound_ctrl:1
	v_or_b32_e32 v171, v169, v170
	ds_write_b8 v184, v171
	s_waitcnt lgkmcnt(0)
	s_barrier
	ds_read_b64 v[122:123], v106 offset:0
	ds_read_b64 v[124:125], v106 offset:8
	ds_read_b64 v[126:127], v106 offset:16
	s_barrier
	ds_read_b64 v[128:129], v106 offset:96
	ds_read_b64 v[130:131], v106 offset:104
	ds_read_b64 v[132:133], v106 offset:112
	s_waitcnt lgkmcnt(3)
	v_mfma_scale_f32_16x16x128_f8f6f4 v[134:137], v[122:127], v[2:7], 0, v178, v115 op_sel_hi:[0,0,0] cbsz:2 blgp:2
	v_mfma_scale_f32_16x16x128_f8f6f4 v[138:141], v[122:127], v[14:19], 0, v178, v115 op_sel_hi:[0,0,0] cbsz:2 blgp:2
	v_mfma_scale_f32_16x16x128_f8f6f4 v[142:145], v[122:127], v[26:31], 0, v178, v115 op_sel_hi:[0,0,0] cbsz:2 blgp:2
	v_mfma_scale_f32_16x16x128_f8f6f4 v[134:137], v[122:127], v[38:43], v[134:137], v179, v115 op_sel_hi:[0,0,0] cbsz:2 blgp:2
	v_mfma_scale_f32_16x16x128_f8f6f4 v[138:141], v[122:127], v[50:55], v[138:141], v179, v115 op_sel_hi:[0,0,0] cbsz:2 blgp:2
	v_mfma_scale_f32_16x16x128_f8f6f4 v[142:145], v[122:127], v[62:67], v[142:145], v179, v115 op_sel_hi:[0,0,0] cbsz:2 blgp:2
	s_waitcnt lgkmcnt(0)
	v_mfma_scale_f32_16x16x128_f8f6f4 v[134:137], v[128:133], v[8:13], v[134:137], v178, v115 op_sel_hi:[0,0,0] cbsz:2 blgp:2
	v_mfma_scale_f32_16x16x128_f8f6f4 v[134:137], v[128:133], v[44:49], v[134:137], v179, v115 op_sel_hi:[0,0,0] cbsz:2 blgp:2
	v_mfma_scale_f32_16x16x128_f8f6f4 v[138:141], v[128:133], v[20:25], v[138:141], v178, v115 op_sel_hi:[0,0,0] cbsz:2 blgp:2
	v_mfma_scale_f32_16x16x128_f8f6f4 v[138:141], v[128:133], v[56:61], v[138:141], v179, v115 op_sel_hi:[0,0,0] cbsz:2 blgp:2
	v_mfma_scale_f32_16x16x128_f8f6f4 v[142:145], v[128:133], v[32:37], v[142:145], v178, v115 op_sel_hi:[0,0,0] cbsz:2 blgp:2
	v_mfma_scale_f32_16x16x128_f8f6f4 v[142:145], v[128:133], v[68:73], v[142:145], v179, v115 op_sel_hi:[0,0,0] cbsz:2 blgp:2
	v_fma_mix_f32 v158, v134, v1, v149 op_sel_hi:[0,0,1]
	v_exp_f32_e32 v158, v158
	v_fma_mix_f32 v159, v138, v99, v153 op_sel_hi:[0,0,1]
	v_exp_f32_e32 v159, v159
	v_add_f32_e32 v158, 1.0, v158
	v_rcp_f32_e32 v158, v158
	v_add_f32_e32 v159, 1.0, v159
	v_rcp_f32_e32 v159, v159
	v_fma_f32 v160, v142, v104, v105
	v_fma_mix_f32 v161, v158, v160, v157 op_sel_hi:[0,0,1]
	v_exp_f32_e32 v161, v161
	s_add_u32 s48, s48, s40
	v_add_f32_e32 v161, 1.0, v161
	v_rcp_f32_e32 v161, v161
	s_addc_u32 s49, s49, s41
	v_fma_f32 v162, v161, -2.0, 1.0
	v_sub_f32_e32 v163, v176, v162
	v_fma_f32 v176, v159, v163, v162
	v_fma_f32 v164, |v176|, s16, v117
	v_fma_f32 v165, |v176|, s17, v118
	v_fma_f32 v166, |v176|, s18, v119
	v_lshrrev_b32_e32 v167, 26, v176
	v_min3_u32 v164, v164, v165, v166
	v_bfi_b32 v168, 31, v164, v167
	v_lshrrev_b32_e32 v169, v181, v168
	global_store_short_d16_hi v185, v176, s[48:49]
	v_mul_u32_u24_dpp v170, v168, v180 quad_perm:[1,2,3,3] row_mask:0xf bank_mask:0xf bound_ctrl:1
	v_or_b32_e32 v171, v169, v170
	ds_write_b8 v184, v171 offset:416
	s_waitcnt lgkmcnt(0)
	s_barrier
	ds_read_b64 v[122:123], v106 offset:416
	ds_read_b64 v[124:125], v106 offset:424
	ds_read_b64 v[126:127], v106 offset:432
	s_barrier
	ds_read_b64 v[128:129], v106 offset:512
	ds_read_b64 v[130:131], v106 offset:520
	ds_read_b64 v[132:133], v106 offset:528
	s_add_i32 s44, s44, 16
	s_waitcnt lgkmcnt(3)
	v_mfma_scale_f32_16x16x128_f8f6f4 v[134:137], v[122:127], v[2:7], 0, v178, v115 op_sel_hi:[0,0,0] cbsz:2 blgp:2
	v_mfma_scale_f32_16x16x128_f8f6f4 v[138:141], v[122:127], v[14:19], 0, v178, v115 op_sel_hi:[0,0,0] cbsz:2 blgp:2
	v_mfma_scale_f32_16x16x128_f8f6f4 v[142:145], v[122:127], v[26:31], 0, v178, v115 op_sel_hi:[0,0,0] cbsz:2 blgp:2
	v_mfma_scale_f32_16x16x128_f8f6f4 v[134:137], v[122:127], v[38:43], v[134:137], v179, v115 op_sel_hi:[0,0,0] cbsz:2 blgp:2
	v_mfma_scale_f32_16x16x128_f8f6f4 v[138:141], v[122:127], v[50:55], v[138:141], v179, v115 op_sel_hi:[0,0,0] cbsz:2 blgp:2
	v_mfma_scale_f32_16x16x128_f8f6f4 v[142:145], v[122:127], v[62:67], v[142:145], v179, v115 op_sel_hi:[0,0,0] cbsz:2 blgp:2
	s_waitcnt lgkmcnt(0)
	v_mfma_scale_f32_16x16x128_f8f6f4 v[134:137], v[128:133], v[8:13], v[134:137], v178, v115 op_sel_hi:[0,0,0] cbsz:2 blgp:2
	v_mfma_scale_f32_16x16x128_f8f6f4 v[134:137], v[128:133], v[44:49], v[134:137], v179, v115 op_sel_hi:[0,0,0] cbsz:2 blgp:2
	v_mfma_scale_f32_16x16x128_f8f6f4 v[138:141], v[128:133], v[20:25], v[138:141], v178, v115 op_sel_hi:[0,0,0] cbsz:2 blgp:2
	v_mfma_scale_f32_16x16x128_f8f6f4 v[138:141], v[128:133], v[56:61], v[138:141], v179, v115 op_sel_hi:[0,0,0] cbsz:2 blgp:2
	v_mfma_scale_f32_16x16x128_f8f6f4 v[142:145], v[128:133], v[32:37], v[142:145], v178, v115 op_sel_hi:[0,0,0] cbsz:2 blgp:2
	v_mfma_scale_f32_16x16x128_f8f6f4 v[142:145], v[128:133], v[68:73], v[142:145], v179, v115 op_sel_hi:[0,0,0] cbsz:2 blgp:2
	v_fma_mix_f32 v158, v134, v1, v149 op_sel:[0,0,1] op_sel_hi:[0,0,1]
	v_exp_f32_e32 v158, v158
	v_fma_mix_f32 v159, v138, v99, v153 op_sel:[0,0,1] op_sel_hi:[0,0,1]
	v_exp_f32_e32 v159, v159
	v_add_f32_e32 v158, 1.0, v158
	v_rcp_f32_e32 v158, v158
	v_add_f32_e32 v159, 1.0, v159
	v_rcp_f32_e32 v159, v159
	v_fma_f32 v160, v142, v104, v105
	v_fma_mix_f32 v161, v158, v160, v157 op_sel:[0,0,1] op_sel_hi:[0,0,1]
	v_exp_f32_e32 v161, v161
	s_add_u32 s48, s48, s40
	v_add_f32_e32 v161, 1.0, v161
	v_rcp_f32_e32 v161, v161
	s_addc_u32 s49, s49, s41
	v_fma_f32 v162, v161, -2.0, 1.0
	v_sub_f32_e32 v163, v176, v162
	v_fma_f32 v176, v159, v163, v162
	v_fma_f32 v164, |v176|, s16, v117
	v_fma_f32 v165, |v176|, s17, v118
	v_fma_f32 v166, |v176|, s18, v119
	v_lshrrev_b32_e32 v167, 26, v176
	v_min3_u32 v164, v164, v165, v166
	v_bfi_b32 v168, 31, v164, v167
	v_lshrrev_b32_e32 v169, v181, v168
	global_store_short_d16_hi v185, v176, s[48:49]
	v_mul_u32_u24_dpp v170, v168, v180 quad_perm:[1,2,3,3] row_mask:0xf bank_mask:0xf bound_ctrl:1
	v_or_b32_e32 v171, v169, v170
	ds_write_b8 v184, v171
	s_waitcnt lgkmcnt(0)
	s_barrier
	ds_read_b64 v[122:123], v106 offset:0
	ds_read_b64 v[124:125], v106 offset:8
	ds_read_b64 v[126:127], v106 offset:16
	s_cmp_lt_i32 s44, s45
	s_barrier
	s_cbranch_scc1 .Lscan_loop_a_st
	s_branch .Lscan_exit_st
.Lscan_loop_b_st:
	ds_read_b64 v[128:129], v106 offset:96
	ds_read_b64 v[130:131], v106 offset:104
	ds_read_b64 v[132:133], v106 offset:112
	s_waitcnt vmcnt(8)
	global_load_dwordx4 v[146:149], v[196:197], off
	global_load_dwordx4 v[150:153], v[196:197], off offset:512
	global_load_dwordx4 v[154:157], v[196:197], off offset:1024
	v_lshl_add_u64 v[196:197], v[196:197], 0, s[42:43]
	s_waitcnt lgkmcnt(3)
	v_mfma_scale_f32_16x16x128_f8f6f4 v[134:137], v[122:127], v[2:7], 0, v178, v115 op_sel_hi:[0,0,0] cbsz:2 blgp:2
	v_mfma_scale_f32_16x16x128_f8f6f4 v[138:141], v[122:127], v[14:19], 0, v178, v115 op_sel_hi:[0,0,0] cbsz:2 blgp:2
	v_mfma_scale_f32_16x16x128_f8f6f4 v[142:145], v[122:127], v[26:31], 0, v178, v115 op_sel_hi:[0,0,0] cbsz:2 blgp:2
	v_mfma_scale_f32_16x16x128_f8f6f4 v[134:137], v[122:127], v[38:43], v[134:137], v179, v115 op_sel_hi:[0,0,0] cbsz:2 blgp:2
	v_mfma_scale_f32_16x16x128_f8f6f4 v[138:141], v[122:127], v[50:55], v[138:141], v179, v115 op_sel_hi:[0,0,0] cbsz:2 blgp:2
	v_mfma_scale_f32_16x16x128_f8f6f4 v[142:145], v[122:127], v[62:67], v[142:145], v179, v115 op_sel_hi:[0,0,0] cbsz:2 blgp:2
	s_waitcnt lgkmcnt(0)
	v_mfma_scale_f32_16x16x128_f8f6f4 v[134:137], v[128:133], v[8:13], v[134:137], v178, v115 op_sel_hi:[0,0,0] cbsz:2 blgp:2
	v_mfma_scale_f32_16x16x128_f8f6f4 v[134:137], v[128:133], v[44:49], v[134:137], v179, v115 op_sel_hi:[0,0,0] cbsz:2 blgp:2
	v_mfma_scale_f32_16x16x128_f8f6f4 v[138:141], v[128:133], v[20:25], v[138:141], v178, v115 op_sel_hi:[0,0,0] cbsz:2 blgp:2
	v_mfma_scale_f32_16x16x128_f8f6f4 v[138:141], v[128:133], v[56:61], v[138:141], v179, v115 op_sel_hi:[0,0,0] cbsz:2 blgp:2
	v_mfma_scale_f32_16x16x128_f8f6f4 v[142:145], v[128:133], v[32:37], v[142:145], v178, v115 op_sel_hi:[0,0,0] cbsz:2 blgp:2
	v_mfma_scale_f32_16x16x128_f8f6f4 v[142:145], v[128:133], v[68:73], v[142:145], v179, v115 op_sel_hi:[0,0,0] cbsz:2 blgp:2
	v_fma_mix_f32 v158, v134, v1, v82 op_sel_hi:[0,0,1]
	v_exp_f32_e32 v158, v158
	v_fma_mix_f32 v159, v138, v99, v74 op_sel_hi:[0,0,1]
	v_exp_f32_e32 v159, v159
	v_add_f32_e32 v158, 1.0, v158
	v_rcp_f32_e32 v158, v158
	v_add_f32_e32 v159, 1.0, v159
	v_rcp_f32_e32 v159, v159
	v_fma_f32 v160, v142, v104, v105
	v_fma_mix_f32 v161, v158, v160, v78 op_sel_hi:[0,0,1]
	v_exp_f32_e32 v161, v161
	s_add_u32 s48, s48, s40
	v_add_f32_e32 v161, 1.0, v161
	v_rcp_f32_e32 v161, v161
	s_addc_u32 s49, s49, s41
	v_fma_f32 v162, v161, -2.0, 1.0
	v_sub_f32_e32 v163, v176, v162
	v_fma_f32 v176, v159, v163, v162
	v_fma_f32 v164, |v176|, s16, v117
	v_fma_f32 v165, |v176|, s17, v118
	v_fma_f32 v166, |v176|, s18, v119
	v_lshrrev_b32_e32 v167, 26, v176
	v_min3_u32 v164, v164, v165, v166
	v_bfi_b32 v168, 31, v164, v167
	v_lshrrev_b32_e32 v169, v181, v168
	global_store_short_d16_hi v185, v176, s[48:49]
	v_mul_u32_u24_dpp v170, v168, v180 quad_perm:[1,2,3,3] row_mask:0xf bank_mask:0xf bound_ctrl:1
	v_or_b32_e32 v171, v169, v170
	ds_write_b8 v184, v171 offset:416
	s_barrier
	ds_read_b64 v[122:123], v106 offset:416
	ds_read_b64 v[124:125], v106 offset:424
	ds_read_b64 v[126:127], v106 offset:432
	s_waitcnt lgkmcnt(3)
	s_barrier
	ds_read_b64 v[128:129], v106 offset:512
	ds_read_b64 v[130:131], v106 offset:520
	ds_read_b64 v[132:133], v106 offset:528
	s_waitcnt lgkmcnt(3)
	v_mfma_scale_f32_16x16x128_f8f6f4 v[134:137], v[122:127], v[2:7], 0, v178, v115 op_sel_hi:[0,0,0] cbsz:2 blgp:2
	v_mfma_scale_f32_16x16x128_f8f6f4 v[138:141], v[122:127], v[14:19], 0, v178, v115 op_sel_hi:[0,0,0] cbsz:2 blgp:2
	v_mfma_scale_f32_16x16x128_f8f6f4 v[142:145], v[122:127], v[26:31], 0, v178, v115 op_sel_hi:[0,0,0] cbsz:2 blgp:2
	v_mfma_scale_f32_16x16x128_f8f6f4 v[134:137], v[122:127], v[38:43], v[134:137], v179, v115 op_sel_hi:[0,0,0] cbsz:2 blgp:2
	v_mfma_scale_f32_16x16x128_f8f6f4 v[138:141], v[122:127], v[50:55], v[138:141], v179, v115 op_sel_hi:[0,0,0] cbsz:2 blgp:2
	v_mfma_scale_f32_16x16x128_f8f6f4 v[142:145], v[122:127], v[62:67], v[142:145], v179, v115 op_sel_hi:[0,0,0] cbsz:2 blgp:2
	s_waitcnt lgkmcnt(0)
	v_mfma_scale_f32_16x16x128_f8f6f4 v[134:137], v[128:133], v[8:13], v[134:137], v178, v115 op_sel_hi:[0,0,0] cbsz:2 blgp:2
	v_mfma_scale_f32_16x16x128_f8f6f4 v[134:137], v[128:133], v[44:49], v[134:137], v179, v115 op_sel_hi:[0,0,0] cbsz:2 blgp:2
	v_mfma_scale_f32_16x16x128_f8f6f4 v[138:141], v[128:133], v[20:25], v[138:141], v178, v115 op_sel_hi:[0,0,0] cbsz:2 blgp:2
	v_mfma_scale_f32_16x16x128_f8f6f4 v[138:141], v[128:133], v[56:61], v[138:141], v179, v115 op_sel_hi:[0,0,0] cbsz:2 blgp:2
	v_mfma_scale_f32_16x16x128_f8f6f4 v[142:145], v[128:133], v[32:37], v[142:145], v178, v115 op_sel_hi:[0,0,0] cbsz:2 blgp:2
	v_mfma_scale_f32_16x16x128_f8f6f4 v[142:145], v[128:133], v[68:73], v[142:145], v179, v115 op_sel_hi:[0,0,0] cbsz:2 blgp:2
	v_fma_mix_f32 v158, v134, v1, v82 op_sel:[0,0,1] op_sel_hi:[0,0,1]
	v_exp_f32_e32 v158, v158
	v_fma_mix_f32 v159, v138, v99, v74 op_sel:[0,0,1] op_sel_hi:[0,0,1]
	v_exp_f32_e32 v159, v159
	v_add_f32_e32 v158, 1.0, v158
	v_rcp_f32_e32 v158, v158
	v_add_f32_e32 v159, 1.0, v159
	v_rcp_f32_e32 v159, v159
	v_fma_f32 v160, v142, v104, v105
	v_fma_mix_f32 v161, v158, v160, v78 op_sel:[0,0,1] op_sel_hi:[0,0,1]
	v_exp_f32_e32 v161, v161
	s_add_u32 s48, s48, s40
	v_add_f32_e32 v161, 1.0, v161
	v_rcp_f32_e32 v161, v161
	s_addc_u32 s49, s49, s41
	v_fma_f32 v162, v161, -2.0, 1.0
	v_sub_f32_e32 v163, v176, v162
	v_fma_f32 v176, v159, v163, v162
	v_fma_f32 v164, |v176|, s16, v117
	v_fma_f32 v165, |v176|, s17, v118
	v_fma_f32 v166, |v176|, s18, v119
	v_lshrrev_b32_e32 v167, 26, v176
	v_min3_u32 v164, v164, v165, v166
	v_bfi_b32 v168, 31, v164, v167
	v_lshrrev_b32_e32 v169, v181, v168
	global_store_short_d16_hi v185, v176, s[48:49]
	v_mul_u32_u24_dpp v170, v168, v180 quad_perm:[1,2,3,3] row_mask:0xf bank_mask:0xf bound_ctrl:1
	v_or_b32_e32 v171, v169, v170
	ds_write_b8 v184, v171
	s_barrier
	ds_read_b64 v[122:123], v106 offset:0
	ds_read_b64 v[124:125], v106 offset:8
	ds_read_b64 v[126:127], v106 offset:16
	s_waitcnt lgkmcnt(3)
	s_barrier
	ds_read_b64 v[128:129], v106 offset:96
	ds_read_b64 v[130:131], v106 offset:104
	ds_read_b64 v[132:133], v106 offset:112
	s_waitcnt lgkmcnt(3)
	v_mfma_scale_f32_16x16x128_f8f6f4 v[134:137], v[122:127], v[2:7], 0, v178, v115 op_sel_hi:[0,0,0] cbsz:2 blgp:2
	v_mfma_scale_f32_16x16x128_f8f6f4 v[138:141], v[122:127], v[14:19], 0, v178, v115 op_sel_hi:[0,0,0] cbsz:2 blgp:2
	v_mfma_scale_f32_16x16x128_f8f6f4 v[142:145], v[122:127], v[26:31], 0, v178, v115 op_sel_hi:[0,0,0] cbsz:2 blgp:2
	v_mfma_scale_f32_16x16x128_f8f6f4 v[134:137], v[122:127], v[38:43], v[134:137], v179, v115 op_sel_hi:[0,0,0] cbsz:2 blgp:2
	v_mfma_scale_f32_16x16x128_f8f6f4 v[138:141], v[122:127], v[50:55], v[138:141], v179, v115 op_sel_hi:[0,0,0] cbsz:2 blgp:2
	v_mfma_scale_f32_16x16x128_f8f6f4 v[142:145], v[122:127], v[62:67], v[142:145], v179, v115 op_sel_hi:[0,0,0] cbsz:2 blgp:2
	s_waitcnt lgkmcnt(0)
	v_mfma_scale_f32_16x16x128_f8f6f4 v[134:137], v[128:133], v[8:13], v[134:137], v178, v115 op_sel_hi:[0,0,0] cbsz:2 blgp:2
	v_mfma_scale_f32_16x16x128_f8f6f4 v[134:137], v[128:133], v[44:49], v[134:137], v179, v115 op_sel_hi:[0,0,0] cbsz:2 blgp:2
	v_mfma_scale_f32_16x16x128_f8f6f4 v[138:141], v[128:133], v[20:25], v[138:141], v178, v115 op_sel_hi:[0,0,0] cbsz:2 blgp:2
	v_mfma_scale_f32_16x16x128_f8f6f4 v[138:141], v[128:133], v[56:61], v[138:141], v179, v115 op_sel_hi:[0,0,0] cbsz:2 blgp:2
	v_mfma_scale_f32_16x16x128_f8f6f4 v[142:145], v[128:133], v[32:37], v[142:145], v178, v115 op_sel_hi:[0,0,0] cbsz:2 blgp:2
	v_mfma_scale_f32_16x16x128_f8f6f4 v[142:145], v[128:133], v[68:73], v[142:145], v179, v115 op_sel_hi:[0,0,0] cbsz:2 blgp:2
	v_fma_mix_f32 v158, v134, v1, v83 op_sel_hi:[0,0,1]
	v_exp_f32_e32 v158, v158
	v_fma_mix_f32 v159, v138, v99, v75 op_sel_hi:[0,0,1]
	v_exp_f32_e32 v159, v159
	v_add_f32_e32 v158, 1.0, v158
	v_rcp_f32_e32 v158, v158
	v_add_f32_e32 v159, 1.0, v159
	v_rcp_f32_e32 v159, v159
	v_fma_f32 v160, v142, v104, v105
	v_fma_mix_f32 v161, v158, v160, v79 op_sel_hi:[0,0,1]
	v_exp_f32_e32 v161, v161
	s_add_u32 s48, s48, s40
	v_add_f32_e32 v161, 1.0, v161
	v_rcp_f32_e32 v161, v161
	s_addc_u32 s49, s49, s41
	v_fma_f32 v162, v161, -2.0, 1.0
	v_sub_f32_e32 v163, v176, v162
	v_fma_f32 v176, v159, v163, v162
	v_fma_f32 v164, |v176|, s16, v117
	v_fma_f32 v165, |v176|, s17, v118
	v_fma_f32 v166, |v176|, s18, v119
	v_lshrrev_b32_e32 v167, 26, v176
	v_min3_u32 v164, v164, v165, v166
	v_bfi_b32 v168, 31, v164, v167
	v_lshrrev_b32_e32 v169, v181, v168
	global_store_short_d16_hi v185, v176, s[48:49]
	v_mul_u32_u24_dpp v170, v168, v180 quad_perm:[1,2,3,3] row_mask:0xf bank_mask:0xf bound_ctrl:1
	v_or_b32_e32 v171, v169, v170
	ds_write_b8 v184, v171 offset:416
	s_barrier
	ds_read_b64 v[122:123], v106 offset:416
	ds_read_b64 v[124:125], v106 offset:424
	ds_read_b64 v[126:127], v106 offset:432
	s_waitcnt lgkmcnt(3)
	s_barrier
	ds_read_b64 v[128:129], v106 offset:512
	ds_read_b64 v[130:131], v106 offset:520
	ds_read_b64 v[132:133], v106 offset:528
	s_waitcnt lgkmcnt(3)
	v_mfma_scale_f32_16x16x128_f8f6f4 v[134:137], v[122:127], v[2:7], 0, v178, v115 op_sel_hi:[0,0,0] cbsz:2 blgp:2
	v_mfma_scale_f32_16x16x128_f8f6f4 v[138:141], v[122:127], v[14:19], 0, v178, v115 op_sel_hi:[0,0,0] cbsz:2 blgp:2
	v_mfma_scale_f32_16x16x128_f8f6f4 v[142:145], v[122:127], v[26:31], 0, v178, v115 op_sel_hi:[0,0,0] cbsz:2 blgp:2
	v_mfma_scale_f32_16x16x128_f8f6f4 v[134:137], v[122:127], v[38:43], v[134:137], v179, v115 op_sel_hi:[0,0,0] cbsz:2 blgp:2
	v_mfma_scale_f32_16x16x128_f8f6f4 v[138:141], v[122:127], v[50:55], v[138:141], v179, v115 op_sel_hi:[0,0,0] cbsz:2 blgp:2
	v_mfma_scale_f32_16x16x128_f8f6f4 v[142:145], v[122:127], v[62:67], v[142:145], v179, v115 op_sel_hi:[0,0,0] cbsz:2 blgp:2
	s_waitcnt lgkmcnt(0)
	v_mfma_scale_f32_16x16x128_f8f6f4 v[134:137], v[128:133], v[8:13], v[134:137], v178, v115 op_sel_hi:[0,0,0] cbsz:2 blgp:2
	v_mfma_scale_f32_16x16x128_f8f6f4 v[134:137], v[128:133], v[44:49], v[134:137], v179, v115 op_sel_hi:[0,0,0] cbsz:2 blgp:2
	v_mfma_scale_f32_16x16x128_f8f6f4 v[138:141], v[128:133], v[20:25], v[138:141], v178, v115 op_sel_hi:[0,0,0] cbsz:2 blgp:2
	v_mfma_scale_f32_16x16x128_f8f6f4 v[138:141], v[128:133], v[56:61], v[138:141], v179, v115 op_sel_hi:[0,0,0] cbsz:2 blgp:2
	v_mfma_scale_f32_16x16x128_f8f6f4 v[142:145], v[128:133], v[32:37], v[142:145], v178, v115 op_sel_hi:[0,0,0] cbsz:2 blgp:2
	v_mfma_scale_f32_16x16x128_f8f6f4 v[142:145], v[128:133], v[68:73], v[142:145], v179, v115 op_sel_hi:[0,0,0] cbsz:2 blgp:2
	v_fma_mix_f32 v158, v134, v1, v83 op_sel:[0,0,1] op_sel_hi:[0,0,1]
	v_exp_f32_e32 v158, v158
	v_fma_mix_f32 v159, v138, v99, v75 op_sel:[0,0,1] op_sel_hi:[0,0,1]
	v_exp_f32_e32 v159, v159
	v_add_f32_e32 v158, 1.0, v158
	v_rcp_f32_e32 v158, v158
	v_add_f32_e32 v159, 1.0, v159
	v_rcp_f32_e32 v159, v159
	v_fma_f32 v160, v142, v104, v105
	v_fma_mix_f32 v161, v158, v160, v79 op_sel:[0,0,1] op_sel_hi:[0,0,1]
	v_exp_f32_e32 v161, v161
	s_add_u32 s48, s48, s40
	v_add_f32_e32 v161, 1.0, v161
	v_rcp_f32_e32 v161, v161
	s_addc_u32 s49, s49, s41
	v_fma_f32 v162, v161, -2.0, 1.0
	v_sub_f32_e32 v163, v176, v162
	v_fma_f32 v176, v159, v163, v162
	v_fma_f32 v164, |v176|, s16, v117
	v_fma_f32 v165, |v176|, s17, v118
	v_fma_f32 v166, |v176|, s18, v119
	v_lshrrev_b32_e32 v167, 26, v176
	v_min3_u32 v164, v164, v165, v166
	v_bfi_b32 v168, 31, v164, v167
	v_lshrrev_b32_e32 v169, v181, v168
	global_store_short_d16_hi v185, v176, s[48:49]
	v_mul_u32_u24_dpp v170, v168, v180 quad_perm:[1,2,3,3] row_mask:0xf bank_mask:0xf bound_ctrl:1
	v_or_b32_e32 v171, v169, v170
	ds_write_b8 v184, v171
	s_barrier
	ds_read_b64 v[122:123], v106 offset:0
	ds_read_b64 v[124:125], v106 offset:8
	ds_read_b64 v[126:127], v106 offset:16
	s_waitcnt lgkmcnt(3)
	s_barrier
	ds_read_b64 v[128:129], v106 offset:96
	ds_read_b64 v[130:131], v106 offset:104
	ds_read_b64 v[132:133], v106 offset:112
	s_waitcnt lgkmcnt(3)
	v_mfma_scale_f32_16x16x128_f8f6f4 v[134:137], v[122:127], v[2:7], 0, v178, v115 op_sel_hi:[0,0,0] cbsz:2 blgp:2
	v_mfma_scale_f32_16x16x128_f8f6f4 v[138:141], v[122:127], v[14:19], 0, v178, v115 op_sel_hi:[0,0,0] cbsz:2 blgp:2
	v_mfma_scale_f32_16x16x128_f8f6f4 v[142:145], v[122:127], v[26:31], 0, v178, v115 op_sel_hi:[0,0,0] cbsz:2 blgp:2
	v_mfma_scale_f32_16x16x128_f8f6f4 v[134:137], v[122:127], v[38:43], v[134:137], v179, v115 op_sel_hi:[0,0,0] cbsz:2 blgp:2
	v_mfma_scale_f32_16x16x128_f8f6f4 v[138:141], v[122:127], v[50:55], v[138:141], v179, v115 op_sel_hi:[0,0,0] cbsz:2 blgp:2
	v_mfma_scale_f32_16x16x128_f8f6f4 v[142:145], v[122:127], v[62:67], v[142:145], v179, v115 op_sel_hi:[0,0,0] cbsz:2 blgp:2
	s_waitcnt lgkmcnt(0)
	v_mfma_scale_f32_16x16x128_f8f6f4 v[134:137], v[128:133], v[8:13], v[134:137], v178, v115 op_sel_hi:[0,0,0] cbsz:2 blgp:2
	v_mfma_scale_f32_16x16x128_f8f6f4 v[134:137], v[128:133], v[44:49], v[134:137], v179, v115 op_sel_hi:[0,0,0] cbsz:2 blgp:2
	v_mfma_scale_f32_16x16x128_f8f6f4 v[138:141], v[128:133], v[20:25], v[138:141], v178, v115 op_sel_hi:[0,0,0] cbsz:2 blgp:2
	v_mfma_scale_f32_16x16x128_f8f6f4 v[138:141], v[128:133], v[56:61], v[138:141], v179, v115 op_sel_hi:[0,0,0] cbsz:2 blgp:2
	v_mfma_scale_f32_16x16x128_f8f6f4 v[142:145], v[128:133], v[32:37], v[142:145], v178, v115 op_sel_hi:[0,0,0] cbsz:2 blgp:2
	v_mfma_scale_f32_16x16x128_f8f6f4 v[142:145], v[128:133], v[68:73], v[142:145], v179, v115 op_sel_hi:[0,0,0] cbsz:2 blgp:2
	v_fma_mix_f32 v158, v134, v1, v84 op_sel_hi:[0,0,1]
	v_exp_f32_e32 v158, v158
	v_fma_mix_f32 v159, v138, v99, v76 op_sel_hi:[0,0,1]
	v_exp_f32_e32 v159, v159
	v_add_f32_e32 v158, 1.0, v158
	v_rcp_f32_e32 v158, v158
	v_add_f32_e32 v159, 1.0, v159
	v_rcp_f32_e32 v159, v159
	v_fma_f32 v160, v142, v104, v105
	v_fma_mix_f32 v161, v158, v160, v80 op_sel_hi:[0,0,1]
	v_exp_f32_e32 v161, v161
	s_add_u32 s48, s48, s40
	v_add_f32_e32 v161, 1.0, v161
	v_rcp_f32_e32 v161, v161
	s_addc_u32 s49, s49, s41
	v_fma_f32 v162, v161, -2.0, 1.0
	v_sub_f32_e32 v163, v176, v162
	v_fma_f32 v176, v159, v163, v162
	v_fma_f32 v164, |v176|, s16, v117
	v_fma_f32 v165, |v176|, s17, v118
	v_fma_f32 v166, |v176|, s18, v119
	v_lshrrev_b32_e32 v167, 26, v176
	v_min3_u32 v164, v164, v165, v166
	v_bfi_b32 v168, 31, v164, v167
	v_lshrrev_b32_e32 v169, v181, v168
	global_store_short_d16_hi v185, v176, s[48:49]
	v_mul_u32_u24_dpp v170, v168, v180 quad_perm:[1,2,3,3] row_mask:0xf bank_mask:0xf bound_ctrl:1
	v_or_b32_e32 v171, v169, v170
	ds_write_b8 v184, v171 offset:416
	s_barrier
	ds_read_b64 v[122:123], v106 offset:416
	ds_read_b64 v[124:125], v106 offset:424
	ds_read_b64 v[126:127], v106 offset:432
	s_waitcnt lgkmcnt(3)
	s_barrier
	ds_read_b64 v[128:129], v106 offset:512
	ds_read_b64 v[130:131], v106 offset:520
	ds_read_b64 v[132:133], v106 offset:528
	s_waitcnt lgkmcnt(3)
	v_mfma_scale_f32_16x16x128_f8f6f4 v[134:137], v[122:127], v[2:7], 0, v178, v115 op_sel_hi:[0,0,0] cbsz:2 blgp:2
	v_mfma_scale_f32_16x16x128_f8f6f4 v[138:141], v[122:127], v[14:19], 0, v178, v115 op_sel_hi:[0,0,0] cbsz:2 blgp:2
	v_mfma_scale_f32_16x16x128_f8f6f4 v[142:145], v[122:127], v[26:31], 0, v178, v115 op_sel_hi:[0,0,0] cbsz:2 blgp:2
	v_mfma_scale_f32_16x16x128_f8f6f4 v[134:137], v[122:127], v[38:43], v[134:137], v179, v115 op_sel_hi:[0,0,0] cbsz:2 blgp:2
	v_mfma_scale_f32_16x16x128_f8f6f4 v[138:141], v[122:127], v[50:55], v[138:141], v179, v115 op_sel_hi:[0,0,0] cbsz:2 blgp:2
	v_mfma_scale_f32_16x16x128_f8f6f4 v[142:145], v[122:127], v[62:67], v[142:145], v179, v115 op_sel_hi:[0,0,0] cbsz:2 blgp:2
	s_waitcnt lgkmcnt(0)
	v_mfma_scale_f32_16x16x128_f8f6f4 v[134:137], v[128:133], v[8:13], v[134:137], v178, v115 op_sel_hi:[0,0,0] cbsz:2 blgp:2
	v_mfma_scale_f32_16x16x128_f8f6f4 v[134:137], v[128:133], v[44:49], v[134:137], v179, v115 op_sel_hi:[0,0,0] cbsz:2 blgp:2
	v_mfma_scale_f32_16x16x128_f8f6f4 v[138:141], v[128:133], v[20:25], v[138:141], v178, v115 op_sel_hi:[0,0,0] cbsz:2 blgp:2
	v_mfma_scale_f32_16x16x128_f8f6f4 v[138:141], v[128:133], v[56:61], v[138:141], v179, v115 op_sel_hi:[0,0,0] cbsz:2 blgp:2
	v_mfma_scale_f32_16x16x128_f8f6f4 v[142:145], v[128:133], v[32:37], v[142:145], v178, v115 op_sel_hi:[0,0,0] cbsz:2 blgp:2
	v_mfma_scale_f32_16x16x128_f8f6f4 v[142:145], v[128:133], v[68:73], v[142:145], v179, v115 op_sel_hi:[0,0,0] cbsz:2 blgp:2
	v_fma_mix_f32 v158, v134, v1, v84 op_sel:[0,0,1] op_sel_hi:[0,0,1]
	v_exp_f32_e32 v158, v158
	v_fma_mix_f32 v159, v138, v99, v76 op_sel:[0,0,1] op_sel_hi:[0,0,1]
	v_exp_f32_e32 v159, v159
	v_add_f32_e32 v158, 1.0, v158
	v_rcp_f32_e32 v158, v158
	v_add_f32_e32 v159, 1.0, v159
	v_rcp_f32_e32 v159, v159
	v_fma_f32 v160, v142, v104, v105
	v_fma_mix_f32 v161, v158, v160, v80 op_sel:[0,0,1] op_sel_hi:[0,0,1]
	v_exp_f32_e32 v161, v161
	s_add_u32 s48, s48, s40
	v_add_f32_e32 v161, 1.0, v161
	v_rcp_f32_e32 v161, v161
	s_addc_u32 s49, s49, s41
	v_fma_f32 v162, v161, -2.0, 1.0
	v_sub_f32_e32 v163, v176, v162
	v_fma_f32 v176, v159, v163, v162
	v_fma_f32 v164, |v176|, s16, v117
	v_fma_f32 v165, |v176|, s17, v118
	v_fma_f32 v166, |v176|, s18, v119
	v_lshrrev_b32_e32 v167, 26, v176
	v_min3_u32 v164, v164, v165, v166
	v_bfi_b32 v168, 31, v164, v167
	v_lshrrev_b32_e32 v169, v181, v168
	global_store_short_d16_hi v185, v176, s[48:49]
	v_mul_u32_u24_dpp v170, v168, v180 quad_perm:[1,2,3,3] row_mask:0xf bank_mask:0xf bound_ctrl:1
	v_or_b32_e32 v171, v169, v170
	ds_write_b8 v184, v171
	s_barrier
	ds_read_b64 v[122:123], v106 offset:0
	ds_read_b64 v[124:125], v106 offset:8
	ds_read_b64 v[126:127], v106 offset:16
	s_waitcnt lgkmcnt(3)
	s_barrier
	ds_read_b64 v[128:129], v106 offset:96
	ds_read_b64 v[130:131], v106 offset:104
	ds_read_b64 v[132:133], v106 offset:112
	s_waitcnt lgkmcnt(3)
	v_mfma_scale_f32_16x16x128_f8f6f4 v[134:137], v[122:127], v[2:7], 0, v178, v115 op_sel_hi:[0,0,0] cbsz:2 blgp:2
	v_mfma_scale_f32_16x16x128_f8f6f4 v[138:141], v[122:127], v[14:19], 0, v178, v115 op_sel_hi:[0,0,0] cbsz:2 blgp:2
	v_mfma_scale_f32_16x16x128_f8f6f4 v[142:145], v[122:127], v[26:31], 0, v178, v115 op_sel_hi:[0,0,0] cbsz:2 blgp:2
	v_mfma_scale_f32_16x16x128_f8f6f4 v[134:137], v[122:127], v[38:43], v[134:137], v179, v115 op_sel_hi:[0,0,0] cbsz:2 blgp:2
	v_mfma_scale_f32_16x16x128_f8f6f4 v[138:141], v[122:127], v[50:55], v[138:141], v179, v115 op_sel_hi:[0,0,0] cbsz:2 blgp:2
	v_mfma_scale_f32_16x16x128_f8f6f4 v[142:145], v[122:127], v[62:67], v[142:145], v179, v115 op_sel_hi:[0,0,0] cbsz:2 blgp:2
	s_waitcnt lgkmcnt(0)
	v_mfma_scale_f32_16x16x128_f8f6f4 v[134:137], v[128:133], v[8:13], v[134:137], v178, v115 op_sel_hi:[0,0,0] cbsz:2 blgp:2
	v_mfma_scale_f32_16x16x128_f8f6f4 v[134:137], v[128:133], v[44:49], v[134:137], v179, v115 op_sel_hi:[0,0,0] cbsz:2 blgp:2
	v_mfma_scale_f32_16x16x128_f8f6f4 v[138:141], v[128:133], v[20:25], v[138:141], v178, v115 op_sel_hi:[0,0,0] cbsz:2 blgp:2
	v_mfma_scale_f32_16x16x128_f8f6f4 v[138:141], v[128:133], v[56:61], v[138:141], v179, v115 op_sel_hi:[0,0,0] cbsz:2 blgp:2
	v_mfma_scale_f32_16x16x128_f8f6f4 v[142:145], v[128:133], v[32:37], v[142:145], v178, v115 op_sel_hi:[0,0,0] cbsz:2 blgp:2
	v_mfma_scale_f32_16x16x128_f8f6f4 v[142:145], v[128:133], v[68:73], v[142:145], v179, v115 op_sel_hi:[0,0,0] cbsz:2 blgp:2
	v_fma_mix_f32 v158, v134, v1, v85 op_sel_hi:[0,0,1]
	v_exp_f32_e32 v158, v158
	v_fma_mix_f32 v159, v138, v99, v77 op_sel_hi:[0,0,1]
	v_exp_f32_e32 v159, v159
	v_add_f32_e32 v158, 1.0, v158
	v_rcp_f32_e32 v158, v158
	v_add_f32_e32 v159, 1.0, v159
	v_rcp_f32_e32 v159, v159
	v_fma_f32 v160, v142, v104, v105
	v_fma_mix_f32 v161, v158, v160, v81 op_sel_hi:[0,0,1]
	v_exp_f32_e32 v161, v161
	s_add_u32 s48, s48, s40
	v_add_f32_e32 v161, 1.0, v161
	v_rcp_f32_e32 v161, v161
	s_addc_u32 s49, s49, s41
	v_fma_f32 v162, v161, -2.0, 1.0
	v_sub_f32_e32 v163, v176, v162
	v_fma_f32 v176, v159, v163, v162
	v_fma_f32 v164, |v176|, s16, v117
	v_fma_f32 v165, |v176|, s17, v118
	v_fma_f32 v166, |v176|, s18, v119
	v_lshrrev_b32_e32 v167, 26, v176
	v_min3_u32 v164, v164, v165, v166
	v_bfi_b32 v168, 31, v164, v167
	v_lshrrev_b32_e32 v169, v181, v168
	global_store_short_d16_hi v185, v176, s[48:49]
	v_mul_u32_u24_dpp v170, v168, v180 quad_perm:[1,2,3,3] row_mask:0xf bank_mask:0xf bound_ctrl:1
	v_or_b32_e32 v171, v169, v170
	ds_write_b8 v184, v171 offset:416
	s_barrier
	ds_read_b64 v[122:123], v106 offset:416
	ds_read_b64 v[124:125], v106 offset:424
	ds_read_b64 v[126:127], v106 offset:432
	s_waitcnt lgkmcnt(3)
	s_barrier
	ds_read_b64 v[128:129], v106 offset:512
	ds_read_b64 v[130:131], v106 offset:520
	ds_read_b64 v[132:133], v106 offset:528
	s_waitcnt lgkmcnt(3)
	v_mfma_scale_f32_16x16x128_f8f6f4 v[134:137], v[122:127], v[2:7], 0, v178, v115 op_sel_hi:[0,0,0] cbsz:2 blgp:2
	v_mfma_scale_f32_16x16x128_f8f6f4 v[138:141], v[122:127], v[14:19], 0, v178, v115 op_sel_hi:[0,0,0] cbsz:2 blgp:2
	v_mfma_scale_f32_16x16x128_f8f6f4 v[142:145], v[122:127], v[26:31], 0, v178, v115 op_sel_hi:[0,0,0] cbsz:2 blgp:2
	v_mfma_scale_f32_16x16x128_f8f6f4 v[134:137], v[122:127], v[38:43], v[134:137], v179, v115 op_sel_hi:[0,0,0] cbsz:2 blgp:2
	v_mfma_scale_f32_16x16x128_f8f6f4 v[138:141], v[122:127], v[50:55], v[138:141], v179, v115 op_sel_hi:[0,0,0] cbsz:2 blgp:2
	v_mfma_scale_f32_16x16x128_f8f6f4 v[142:145], v[122:127], v[62:67], v[142:145], v179, v115 op_sel_hi:[0,0,0] cbsz:2 blgp:2
	s_waitcnt lgkmcnt(0)
	v_mfma_scale_f32_16x16x128_f8f6f4 v[134:137], v[128:133], v[8:13], v[134:137], v178, v115 op_sel_hi:[0,0,0] cbsz:2 blgp:2
	v_mfma_scale_f32_16x16x128_f8f6f4 v[134:137], v[128:133], v[44:49], v[134:137], v179, v115 op_sel_hi:[0,0,0] cbsz:2 blgp:2
	v_mfma_scale_f32_16x16x128_f8f6f4 v[138:141], v[128:133], v[20:25], v[138:141], v178, v115 op_sel_hi:[0,0,0] cbsz:2 blgp:2
	v_mfma_scale_f32_16x16x128_f8f6f4 v[138:141], v[128:133], v[56:61], v[138:141], v179, v115 op_sel_hi:[0,0,0] cbsz:2 blgp:2
	v_mfma_scale_f32_16x16x128_f8f6f4 v[142:145], v[128:133], v[32:37], v[142:145], v178, v115 op_sel_hi:[0,0,0] cbsz:2 blgp:2
	v_mfma_scale_f32_16x16x128_f8f6f4 v[142:145], v[128:133], v[68:73], v[142:145], v179, v115 op_sel_hi:[0,0,0] cbsz:2 blgp:2
	v_fma_mix_f32 v158, v134, v1, v85 op_sel:[0,0,1] op_sel_hi:[0,0,1]
	v_exp_f32_e32 v158, v158
	v_fma_mix_f32 v159, v138, v99, v77 op_sel:[0,0,1] op_sel_hi:[0,0,1]
	v_exp_f32_e32 v159, v159
	v_add_f32_e32 v158, 1.0, v158
	v_rcp_f32_e32 v158, v158
	v_add_f32_e32 v159, 1.0, v159
	v_rcp_f32_e32 v159, v159
	v_fma_f32 v160, v142, v104, v105
	v_fma_mix_f32 v161, v158, v160, v81 op_sel:[0,0,1] op_sel_hi:[0,0,1]
	v_exp_f32_e32 v161, v161
	s_add_u32 s48, s48, s40
	v_add_f32_e32 v161, 1.0, v161
	v_rcp_f32_e32 v161, v161
	s_addc_u32 s49, s49, s41
	v_fma_f32 v162, v161, -2.0, 1.0
	v_sub_f32_e32 v163, v176, v162
	v_fma_f32 v176, v159, v163, v162
	v_fma_f32 v164, |v176|, s16, v117
	v_fma_f32 v165, |v176|, s17, v118
	v_fma_f32 v166, |v176|, s18, v119
	v_lshrrev_b32_e32 v167, 26, v176
	v_min3_u32 v164, v164, v165, v166
	v_bfi_b32 v168, 31, v164, v167
	v_lshrrev_b32_e32 v169, v181, v168
	global_store_short_d16_hi v185, v176, s[48:49]
	v_mul_u32_u24_dpp v170, v168, v180 quad_perm:[1,2,3,3] row_mask:0xf bank_mask:0xf bound_ctrl:1
	v_or_b32_e32 v171, v169, v170
	ds_write_b8 v184, v171
	s_barrier
	ds_read_b64 v[122:123], v106 offset:0
	ds_read_b64 v[124:125], v106 offset:8
	ds_read_b64 v[126:127], v106 offset:16
	s_waitcnt lgkmcnt(3)
	s_barrier
	ds_read_b64 v[128:129], v106 offset:96
	ds_read_b64 v[130:131], v106 offset:104
	ds_read_b64 v[132:133], v106 offset:112
	s_waitcnt vmcnt(8)
	global_load_dwordx4 v[82:85], v[196:197], off
	global_load_dwordx4 v[74:77], v[196:197], off offset:512
	global_load_dwordx4 v[78:81], v[196:197], off offset:1024
	v_lshl_add_u64 v[196:197], v[196:197], 0, s[42:43]
	s_waitcnt lgkmcnt(3)
	v_mfma_scale_f32_16x16x128_f8f6f4 v[134:137], v[122:127], v[2:7], 0, v178, v115 op_sel_hi:[0,0,0] cbsz:2 blgp:2
	v_mfma_scale_f32_16x16x128_f8f6f4 v[138:141], v[122:127], v[14:19], 0, v178, v115 op_sel_hi:[0,0,0] cbsz:2 blgp:2
	v_mfma_scale_f32_16x16x128_f8f6f4 v[142:145], v[122:127], v[26:31], 0, v178, v115 op_sel_hi:[0,0,0] cbsz:2 blgp:2
	v_mfma_scale_f32_16x16x128_f8f6f4 v[134:137], v[122:127], v[38:43], v[134:137], v179, v115 op_sel_hi:[0,0,0] cbsz:2 blgp:2
	v_mfma_scale_f32_16x16x128_f8f6f4 v[138:141], v[122:127], v[50:55], v[138:141], v179, v115 op_sel_hi:[0,0,0] cbsz:2 blgp:2
	v_mfma_scale_f32_16x16x128_f8f6f4 v[142:145], v[122:127], v[62:67], v[142:145], v179, v115 op_sel_hi:[0,0,0] cbsz:2 blgp:2
	s_waitcnt lgkmcnt(0)
	v_mfma_scale_f32_16x16x128_f8f6f4 v[134:137], v[128:133], v[8:13], v[134:137], v178, v115 op_sel_hi:[0,0,0] cbsz:2 blgp:2
	v_mfma_scale_f32_16x16x128_f8f6f4 v[134:137], v[128:133], v[44:49], v[134:137], v179, v115 op_sel_hi:[0,0,0] cbsz:2 blgp:2
	v_mfma_scale_f32_16x16x128_f8f6f4 v[138:141], v[128:133], v[20:25], v[138:141], v178, v115 op_sel_hi:[0,0,0] cbsz:2 blgp:2
	v_mfma_scale_f32_16x16x128_f8f6f4 v[138:141], v[128:133], v[56:61], v[138:141], v179, v115 op_sel_hi:[0,0,0] cbsz:2 blgp:2
	v_mfma_scale_f32_16x16x128_f8f6f4 v[142:145], v[128:133], v[32:37], v[142:145], v178, v115 op_sel_hi:[0,0,0] cbsz:2 blgp:2
	v_mfma_scale_f32_16x16x128_f8f6f4 v[142:145], v[128:133], v[68:73], v[142:145], v179, v115 op_sel_hi:[0,0,0] cbsz:2 blgp:2
	v_fma_mix_f32 v158, v134, v1, v146 op_sel_hi:[0,0,1]
	v_exp_f32_e32 v158, v158
	v_fma_mix_f32 v159, v138, v99, v150 op_sel_hi:[0,0,1]
	v_exp_f32_e32 v159, v159
	v_add_f32_e32 v158, 1.0, v158
	v_rcp_f32_e32 v158, v158
	v_add_f32_e32 v159, 1.0, v159
	v_rcp_f32_e32 v159, v159
	v_fma_f32 v160, v142, v104, v105
	v_fma_mix_f32 v161, v158, v160, v154 op_sel_hi:[0,0,1]
	v_exp_f32_e32 v161, v161
	s_add_u32 s48, s48, s40
	v_add_f32_e32 v161, 1.0, v161
	v_rcp_f32_e32 v161, v161
	s_addc_u32 s49, s49, s41
	v_fma_f32 v162, v161, -2.0, 1.0
	v_sub_f32_e32 v163, v176, v162
	v_fma_f32 v176, v159, v163, v162
	v_fma_f32 v164, |v176|, s16, v117
	v_fma_f32 v165, |v176|, s17, v118
	v_fma_f32 v166, |v176|, s18, v119
	v_lshrrev_b32_e32 v167, 26, v176
	v_min3_u32 v164, v164, v165, v166
	v_bfi_b32 v168, 31, v164, v167
	v_lshrrev_b32_e32 v169, v181, v168
	global_store_short_d16_hi v185, v176, s[48:49]
	v_mul_u32_u24_dpp v170, v168, v180 quad_perm:[1,2,3,3] row_mask:0xf bank_mask:0xf bound_ctrl:1
	v_or_b32_e32 v171, v169, v170
	ds_write_b8 v184, v171 offset:416
	s_barrier
	ds_read_b64 v[122:123], v106 offset:416
	ds_read_b64 v[124:125], v106 offset:424
	ds_read_b64 v[126:127], v106 offset:432
	s_waitcnt lgkmcnt(3)
	s_barrier
	ds_read_b64 v[128:129], v106 offset:512
	ds_read_b64 v[130:131], v106 offset:520
	ds_read_b64 v[132:133], v106 offset:528
	s_waitcnt lgkmcnt(3)
	v_mfma_scale_f32_16x16x128_f8f6f4 v[134:137], v[122:127], v[2:7], 0, v178, v115 op_sel_hi:[0,0,0] cbsz:2 blgp:2
	v_mfma_scale_f32_16x16x128_f8f6f4 v[138:141], v[122:127], v[14:19], 0, v178, v115 op_sel_hi:[0,0,0] cbsz:2 blgp:2
	v_mfma_scale_f32_16x16x128_f8f6f4 v[142:145], v[122:127], v[26:31], 0, v178, v115 op_sel_hi:[0,0,0] cbsz:2 blgp:2
	v_mfma_scale_f32_16x16x128_f8f6f4 v[134:137], v[122:127], v[38:43], v[134:137], v179, v115 op_sel_hi:[0,0,0] cbsz:2 blgp:2
	v_mfma_scale_f32_16x16x128_f8f6f4 v[138:141], v[122:127], v[50:55], v[138:141], v179, v115 op_sel_hi:[0,0,0] cbsz:2 blgp:2
	v_mfma_scale_f32_16x16x128_f8f6f4 v[142:145], v[122:127], v[62:67], v[142:145], v179, v115 op_sel_hi:[0,0,0] cbsz:2 blgp:2
	s_waitcnt lgkmcnt(0)
	v_mfma_scale_f32_16x16x128_f8f6f4 v[134:137], v[128:133], v[8:13], v[134:137], v178, v115 op_sel_hi:[0,0,0] cbsz:2 blgp:2
	v_mfma_scale_f32_16x16x128_f8f6f4 v[134:137], v[128:133], v[44:49], v[134:137], v179, v115 op_sel_hi:[0,0,0] cbsz:2 blgp:2
	v_mfma_scale_f32_16x16x128_f8f6f4 v[138:141], v[128:133], v[20:25], v[138:141], v178, v115 op_sel_hi:[0,0,0] cbsz:2 blgp:2
	v_mfma_scale_f32_16x16x128_f8f6f4 v[138:141], v[128:133], v[56:61], v[138:141], v179, v115 op_sel_hi:[0,0,0] cbsz:2 blgp:2
	v_mfma_scale_f32_16x16x128_f8f6f4 v[142:145], v[128:133], v[32:37], v[142:145], v178, v115 op_sel_hi:[0,0,0] cbsz:2 blgp:2
	v_mfma_scale_f32_16x16x128_f8f6f4 v[142:145], v[128:133], v[68:73], v[142:145], v179, v115 op_sel_hi:[0,0,0] cbsz:2 blgp:2
	v_fma_mix_f32 v158, v134, v1, v146 op_sel:[0,0,1] op_sel_hi:[0,0,1]
	v_exp_f32_e32 v158, v158
	v_fma_mix_f32 v159, v138, v99, v150 op_sel:[0,0,1] op_sel_hi:[0,0,1]
	v_exp_f32_e32 v159, v159
	v_add_f32_e32 v158, 1.0, v158
	v_rcp_f32_e32 v158, v158
	v_add_f32_e32 v159, 1.0, v159
	v_rcp_f32_e32 v159, v159
	v_fma_f32 v160, v142, v104, v105
	v_fma_mix_f32 v161, v158, v160, v154 op_sel:[0,0,1] op_sel_hi:[0,0,1]
	v_exp_f32_e32 v161, v161
	s_add_u32 s48, s48, s40
	v_add_f32_e32 v161, 1.0, v161
	v_rcp_f32_e32 v161, v161
	s_addc_u32 s49, s49, s41
	v_fma_f32 v162, v161, -2.0, 1.0
	v_sub_f32_e32 v163, v176, v162
	v_fma_f32 v176, v159, v163, v162
	v_fma_f32 v164, |v176|, s16, v117
	v_fma_f32 v165, |v176|, s17, v118
	v_fma_f32 v166, |v176|, s18, v119
	v_lshrrev_b32_e32 v167, 26, v176
	v_min3_u32 v164, v164, v165, v166
	v_bfi_b32 v168, 31, v164, v167
	v_lshrrev_b32_e32 v169, v181, v168
	global_store_short_d16_hi v185, v176, s[48:49]
	v_mul_u32_u24_dpp v170, v168, v180 quad_perm:[1,2,3,3] row_mask:0xf bank_mask:0xf bound_ctrl:1
	v_or_b32_e32 v171, v169, v170
	ds_write_b8 v184, v171
	s_barrier
	ds_read_b64 v[122:123], v106 offset:0
	ds_read_b64 v[124:125], v106 offset:8
	ds_read_b64 v[126:127], v106 offset:16
	s_waitcnt lgkmcnt(3)
	s_barrier
	ds_read_b64 v[128:129], v106 offset:96
	ds_read_b64 v[130:131], v106 offset:104
	ds_read_b64 v[132:133], v106 offset:112
	s_waitcnt lgkmcnt(3)
	v_mfma_scale_f32_16x16x128_f8f6f4 v[134:137], v[122:127], v[2:7], 0, v178, v115 op_sel_hi:[0,0,0] cbsz:2 blgp:2
	v_mfma_scale_f32_16x16x128_f8f6f4 v[138:141], v[122:127], v[14:19], 0, v178, v115 op_sel_hi:[0,0,0] cbsz:2 blgp:2
	v_mfma_scale_f32_16x16x128_f8f6f4 v[142:145], v[122:127], v[26:31], 0, v178, v115 op_sel_hi:[0,0,0] cbsz:2 blgp:2
	v_mfma_scale_f32_16x16x128_f8f6f4 v[134:137], v[122:127], v[38:43], v[134:137], v179, v115 op_sel_hi:[0,0,0] cbsz:2 blgp:2
	v_mfma_scale_f32_16x16x128_f8f6f4 v[138:141], v[122:127], v[50:55], v[138:141], v179, v115 op_sel_hi:[0,0,0] cbsz:2 blgp:2
	v_mfma_scale_f32_16x16x128_f8f6f4 v[142:145], v[122:127], v[62:67], v[142:145], v179, v115 op_sel_hi:[0,0,0] cbsz:2 blgp:2
	s_waitcnt lgkmcnt(0)
	v_mfma_scale_f32_16x16x128_f8f6f4 v[134:137], v[128:133], v[8:13], v[134:137], v178, v115 op_sel_hi:[0,0,0] cbsz:2 blgp:2
	v_mfma_scale_f32_16x16x128_f8f6f4 v[134:137], v[128:133], v[44:49], v[134:137], v179, v115 op_sel_hi:[0,0,0] cbsz:2 blgp:2
	v_mfma_scale_f32_16x16x128_f8f6f4 v[138:141], v[128:133], v[20:25], v[138:141], v178, v115 op_sel_hi:[0,0,0] cbsz:2 blgp:2
	v_mfma_scale_f32_16x16x128_f8f6f4 v[138:141], v[128:133], v[56:61], v[138:141], v179, v115 op_sel_hi:[0,0,0] cbsz:2 blgp:2
	v_mfma_scale_f32_16x16x128_f8f6f4 v[142:145], v[128:133], v[32:37], v[142:145], v178, v115 op_sel_hi:[0,0,0] cbsz:2 blgp:2
	v_mfma_scale_f32_16x16x128_f8f6f4 v[142:145], v[128:133], v[68:73], v[142:145], v179, v115 op_sel_hi:[0,0,0] cbsz:2 blgp:2
	v_fma_mix_f32 v158, v134, v1, v147 op_sel_hi:[0,0,1]
	v_exp_f32_e32 v158, v158
	v_fma_mix_f32 v159, v138, v99, v151 op_sel_hi:[0,0,1]
	v_exp_f32_e32 v159, v159
	v_add_f32_e32 v158, 1.0, v158
	v_rcp_f32_e32 v158, v158
	v_add_f32_e32 v159, 1.0, v159
	v_rcp_f32_e32 v159, v159
	v_fma_f32 v160, v142, v104, v105
	v_fma_mix_f32 v161, v158, v160, v155 op_sel_hi:[0,0,1]
	v_exp_f32_e32 v161, v161
	s_add_u32 s48, s48, s40
	v_add_f32_e32 v161, 1.0, v161
	v_rcp_f32_e32 v161, v161
	s_addc_u32 s49, s49, s41
	v_fma_f32 v162, v161, -2.0, 1.0
	v_sub_f32_e32 v163, v176, v162
	v_fma_f32 v176, v159, v163, v162
	v_fma_f32 v164, |v176|, s16, v117
	v_fma_f32 v165, |v176|, s17, v118
	v_fma_f32 v166, |v176|, s18, v119
	v_lshrrev_b32_e32 v167, 26, v176
	v_min3_u32 v164, v164, v165, v166
	v_bfi_b32 v168, 31, v164, v167
	v_lshrrev_b32_e32 v169, v181, v168
	global_store_short_d16_hi v185, v176, s[48:49]
	v_mul_u32_u24_dpp v170, v168, v180 quad_perm:[1,2,3,3] row_mask:0xf bank_mask:0xf bound_ctrl:1
	v_or_b32_e32 v171, v169, v170
	ds_write_b8 v184, v171 offset:416
	s_barrier
	ds_read_b64 v[122:123], v106 offset:416
	ds_read_b64 v[124:125], v106 offset:424
	ds_read_b64 v[126:127], v106 offset:432
	s_waitcnt lgkmcnt(3)
	s_barrier
	ds_read_b64 v[128:129], v106 offset:512
	ds_read_b64 v[130:131], v106 offset:520
	ds_read_b64 v[132:133], v106 offset:528
	s_waitcnt lgkmcnt(3)
	v_mfma_scale_f32_16x16x128_f8f6f4 v[134:137], v[122:127], v[2:7], 0, v178, v115 op_sel_hi:[0,0,0] cbsz:2 blgp:2
	v_mfma_scale_f32_16x16x128_f8f6f4 v[138:141], v[122:127], v[14:19], 0, v178, v115 op_sel_hi:[0,0,0] cbsz:2 blgp:2
	v_mfma_scale_f32_16x16x128_f8f6f4 v[142:145], v[122:127], v[26:31], 0, v178, v115 op_sel_hi:[0,0,0] cbsz:2 blgp:2
	v_mfma_scale_f32_16x16x128_f8f6f4 v[134:137], v[122:127], v[38:43], v[134:137], v179, v115 op_sel_hi:[0,0,0] cbsz:2 blgp:2
	v_mfma_scale_f32_16x16x128_f8f6f4 v[138:141], v[122:127], v[50:55], v[138:141], v179, v115 op_sel_hi:[0,0,0] cbsz:2 blgp:2
	v_mfma_scale_f32_16x16x128_f8f6f4 v[142:145], v[122:127], v[62:67], v[142:145], v179, v115 op_sel_hi:[0,0,0] cbsz:2 blgp:2
	s_waitcnt lgkmcnt(0)
	v_mfma_scale_f32_16x16x128_f8f6f4 v[134:137], v[128:133], v[8:13], v[134:137], v178, v115 op_sel_hi:[0,0,0] cbsz:2 blgp:2
	v_mfma_scale_f32_16x16x128_f8f6f4 v[134:137], v[128:133], v[44:49], v[134:137], v179, v115 op_sel_hi:[0,0,0] cbsz:2 blgp:2
	v_mfma_scale_f32_16x16x128_f8f6f4 v[138:141], v[128:133], v[20:25], v[138:141], v178, v115 op_sel_hi:[0,0,0] cbsz:2 blgp:2
	v_mfma_scale_f32_16x16x128_f8f6f4 v[138:141], v[128:133], v[56:61], v[138:141], v179, v115 op_sel_hi:[0,0,0] cbsz:2 blgp:2
	v_mfma_scale_f32_16x16x128_f8f6f4 v[142:145], v[128:133], v[32:37], v[142:145], v178, v115 op_sel_hi:[0,0,0] cbsz:2 blgp:2
	v_mfma_scale_f32_16x16x128_f8f6f4 v[142:145], v[128:133], v[68:73], v[142:145], v179, v115 op_sel_hi:[0,0,0] cbsz:2 blgp:2
	v_fma_mix_f32 v158, v134, v1, v147 op_sel:[0,0,1] op_sel_hi:[0,0,1]
	v_exp_f32_e32 v158, v158
	v_fma_mix_f32 v159, v138, v99, v151 op_sel:[0,0,1] op_sel_hi:[0,0,1]
	v_exp_f32_e32 v159, v159
	v_add_f32_e32 v158, 1.0, v158
	v_rcp_f32_e32 v158, v158
	v_add_f32_e32 v159, 1.0, v159
	v_rcp_f32_e32 v159, v159
	v_fma_f32 v160, v142, v104, v105
	v_fma_mix_f32 v161, v158, v160, v155 op_sel:[0,0,1] op_sel_hi:[0,0,1]
	v_exp_f32_e32 v161, v161
	s_add_u32 s48, s48, s40
	v_add_f32_e32 v161, 1.0, v161
	v_rcp_f32_e32 v161, v161
	s_addc_u32 s49, s49, s41
	v_fma_f32 v162, v161, -2.0, 1.0
	v_sub_f32_e32 v163, v176, v162
	v_fma_f32 v176, v159, v163, v162
	v_fma_f32 v164, |v176|, s16, v117
	v_fma_f32 v165, |v176|, s17, v118
	v_fma_f32 v166, |v176|, s18, v119
	v_lshrrev_b32_e32 v167, 26, v176
	v_min3_u32 v164, v164, v165, v166
	v_bfi_b32 v168, 31, v164, v167
	v_lshrrev_b32_e32 v169, v181, v168
	global_store_short_d16_hi v185, v176, s[48:49]
	v_mul_u32_u24_dpp v170, v168, v180 quad_perm:[1,2,3,3] row_mask:0xf bank_mask:0xf bound_ctrl:1
	v_or_b32_e32 v171, v169, v170
	ds_write_b8 v184, v171
	s_barrier
	ds_read_b64 v[122:123], v106 offset:0
	ds_read_b64 v[124:125], v106 offset:8
	ds_read_b64 v[126:127], v106 offset:16
	s_waitcnt lgkmcnt(3)
	s_barrier
	ds_read_b64 v[128:129], v106 offset:96
	ds_read_b64 v[130:131], v106 offset:104
	ds_read_b64 v[132:133], v106 offset:112
	s_waitcnt lgkmcnt(3)
	v_mfma_scale_f32_16x16x128_f8f6f4 v[134:137], v[122:127], v[2:7], 0, v178, v115 op_sel_hi:[0,0,0] cbsz:2 blgp:2
	v_mfma_scale_f32_16x16x128_f8f6f4 v[138:141], v[122:127], v[14:19], 0, v178, v115 op_sel_hi:[0,0,0] cbsz:2 blgp:2
	v_mfma_scale_f32_16x16x128_f8f6f4 v[142:145], v[122:127], v[26:31], 0, v178, v115 op_sel_hi:[0,0,0] cbsz:2 blgp:2
	v_mfma_scale_f32_16x16x128_f8f6f4 v[134:137], v[122:127], v[38:43], v[134:137], v179, v115 op_sel_hi:[0,0,0] cbsz:2 blgp:2
	v_mfma_scale_f32_16x16x128_f8f6f4 v[138:141], v[122:127], v[50:55], v[138:141], v179, v115 op_sel_hi:[0,0,0] cbsz:2 blgp:2
	v_mfma_scale_f32_16x16x128_f8f6f4 v[142:145], v[122:127], v[62:67], v[142:145], v179, v115 op_sel_hi:[0,0,0] cbsz:2 blgp:2
	s_waitcnt lgkmcnt(0)
	v_mfma_scale_f32_16x16x128_f8f6f4 v[134:137], v[128:133], v[8:13], v[134:137], v178, v115 op_sel_hi:[0,0,0] cbsz:2 blgp:2
	v_mfma_scale_f32_16x16x128_f8f6f4 v[134:137], v[128:133], v[44:49], v[134:137], v179, v115 op_sel_hi:[0,0,0] cbsz:2 blgp:2
	v_mfma_scale_f32_16x16x128_f8f6f4 v[138:141], v[128:133], v[20:25], v[138:141], v178, v115 op_sel_hi:[0,0,0] cbsz:2 blgp:2
	v_mfma_scale_f32_16x16x128_f8f6f4 v[138:141], v[128:133], v[56:61], v[138:141], v179, v115 op_sel_hi:[0,0,0] cbsz:2 blgp:2
	v_mfma_scale_f32_16x16x128_f8f6f4 v[142:145], v[128:133], v[32:37], v[142:145], v178, v115 op_sel_hi:[0,0,0] cbsz:2 blgp:2
	v_mfma_scale_f32_16x16x128_f8f6f4 v[142:145], v[128:133], v[68:73], v[142:145], v179, v115 op_sel_hi:[0,0,0] cbsz:2 blgp:2
	v_fma_mix_f32 v158, v134, v1, v148 op_sel_hi:[0,0,1]
	v_exp_f32_e32 v158, v158
	v_fma_mix_f32 v159, v138, v99, v152 op_sel_hi:[0,0,1]
	v_exp_f32_e32 v159, v159
	v_add_f32_e32 v158, 1.0, v158
	v_rcp_f32_e32 v158, v158
	v_add_f32_e32 v159, 1.0, v159
	v_rcp_f32_e32 v159, v159
	v_fma_f32 v160, v142, v104, v105
	v_fma_mix_f32 v161, v158, v160, v156 op_sel_hi:[0,0,1]
	v_exp_f32_e32 v161, v161
	s_add_u32 s48, s48, s40
	v_add_f32_e32 v161, 1.0, v161
	v_rcp_f32_e32 v161, v161
	s_addc_u32 s49, s49, s41
	v_fma_f32 v162, v161, -2.0, 1.0
	v_sub_f32_e32 v163, v176, v162
	v_fma_f32 v176, v159, v163, v162
	v_fma_f32 v164, |v176|, s16, v117
	v_fma_f32 v165, |v176|, s17, v118
	v_fma_f32 v166, |v176|, s18, v119
	v_lshrrev_b32_e32 v167, 26, v176
	v_min3_u32 v164, v164, v165, v166
	v_bfi_b32 v168, 31, v164, v167
	v_lshrrev_b32_e32 v169, v181, v168
	global_store_short_d16_hi v185, v176, s[48:49]
	v_mul_u32_u24_dpp v170, v168, v180 quad_perm:[1,2,3,3] row_mask:0xf bank_mask:0xf bound_ctrl:1
	v_or_b32_e32 v171, v169, v170
	ds_write_b8 v184, v171 offset:416
	s_barrier
	ds_read_b64 v[122:123], v106 offset:416
	ds_read_b64 v[124:125], v106 offset:424
	ds_read_b64 v[126:127], v106 offset:432
	s_waitcnt lgkmcnt(3)
	s_barrier
	ds_read_b64 v[128:129], v106 offset:512
	ds_read_b64 v[130:131], v106 offset:520
	ds_read_b64 v[132:133], v106 offset:528
	s_waitcnt lgkmcnt(3)
	v_mfma_scale_f32_16x16x128_f8f6f4 v[134:137], v[122:127], v[2:7], 0, v178, v115 op_sel_hi:[0,0,0] cbsz:2 blgp:2
	v_mfma_scale_f32_16x16x128_f8f6f4 v[138:141], v[122:127], v[14:19], 0, v178, v115 op_sel_hi:[0,0,0] cbsz:2 blgp:2
	v_mfma_scale_f32_16x16x128_f8f6f4 v[142:145], v[122:127], v[26:31], 0, v178, v115 op_sel_hi:[0,0,0] cbsz:2 blgp:2
	v_mfma_scale_f32_16x16x128_f8f6f4 v[134:137], v[122:127], v[38:43], v[134:137], v179, v115 op_sel_hi:[0,0,0] cbsz:2 blgp:2
	v_mfma_scale_f32_16x16x128_f8f6f4 v[138:141], v[122:127], v[50:55], v[138:141], v179, v115 op_sel_hi:[0,0,0] cbsz:2 blgp:2
	v_mfma_scale_f32_16x16x128_f8f6f4 v[142:145], v[122:127], v[62:67], v[142:145], v179, v115 op_sel_hi:[0,0,0] cbsz:2 blgp:2
	s_waitcnt lgkmcnt(0)
	v_mfma_scale_f32_16x16x128_f8f6f4 v[134:137], v[128:133], v[8:13], v[134:137], v178, v115 op_sel_hi:[0,0,0] cbsz:2 blgp:2
	v_mfma_scale_f32_16x16x128_f8f6f4 v[134:137], v[128:133], v[44:49], v[134:137], v179, v115 op_sel_hi:[0,0,0] cbsz:2 blgp:2
	v_mfma_scale_f32_16x16x128_f8f6f4 v[138:141], v[128:133], v[20:25], v[138:141], v178, v115 op_sel_hi:[0,0,0] cbsz:2 blgp:2
	v_mfma_scale_f32_16x16x128_f8f6f4 v[138:141], v[128:133], v[56:61], v[138:141], v179, v115 op_sel_hi:[0,0,0] cbsz:2 blgp:2
	v_mfma_scale_f32_16x16x128_f8f6f4 v[142:145], v[128:133], v[32:37], v[142:145], v178, v115 op_sel_hi:[0,0,0] cbsz:2 blgp:2
	v_mfma_scale_f32_16x16x128_f8f6f4 v[142:145], v[128:133], v[68:73], v[142:145], v179, v115 op_sel_hi:[0,0,0] cbsz:2 blgp:2
	v_fma_mix_f32 v158, v134, v1, v148 op_sel:[0,0,1] op_sel_hi:[0,0,1]
	v_exp_f32_e32 v158, v158
	v_fma_mix_f32 v159, v138, v99, v152 op_sel:[0,0,1] op_sel_hi:[0,0,1]
	v_exp_f32_e32 v159, v159
	v_add_f32_e32 v158, 1.0, v158
	v_rcp_f32_e32 v158, v158
	v_add_f32_e32 v159, 1.0, v159
	v_rcp_f32_e32 v159, v159
	v_fma_f32 v160, v142, v104, v105
	v_fma_mix_f32 v161, v158, v160, v156 op_sel:[0,0,1] op_sel_hi:[0,0,1]
	v_exp_f32_e32 v161, v161
	s_add_u32 s48, s48, s40
	v_add_f32_e32 v161, 1.0, v161
	v_rcp_f32_e32 v161, v161
	s_addc_u32 s49, s49, s41
	v_fma_f32 v162, v161, -2.0, 1.0
	v_sub_f32_e32 v163, v176, v162
	v_fma_f32 v176, v159, v163, v162
	v_fma_f32 v164, |v176|, s16, v117
	v_fma_f32 v165, |v176|, s17, v118
	v_fma_f32 v166, |v176|, s18, v119
	v_lshrrev_b32_e32 v167, 26, v176
	v_min3_u32 v164, v164, v165, v166
	v_bfi_b32 v168, 31, v164, v167
	v_lshrrev_b32_e32 v169, v181, v168
	global_store_short_d16_hi v185, v176, s[48:49]
	v_mul_u32_u24_dpp v170, v168, v180 quad_perm:[1,2,3,3] row_mask:0xf bank_mask:0xf bound_ctrl:1
	v_or_b32_e32 v171, v169, v170
	ds_write_b8 v184, v171
	s_barrier
	ds_read_b64 v[122:123], v106 offset:0
	ds_read_b64 v[124:125], v106 offset:8
	ds_read_b64 v[126:127], v106 offset:16
	s_waitcnt lgkmcnt(3)
	s_barrier
	ds_read_b64 v[128:129], v106 offset:96
	ds_read_b64 v[130:131], v106 offset:104
	ds_read_b64 v[132:133], v106 offset:112
	s_waitcnt lgkmcnt(3)
	v_mfma_scale_f32_16x16x128_f8f6f4 v[134:137], v[122:127], v[2:7], 0, v178, v115 op_sel_hi:[0,0,0] cbsz:2 blgp:2
	v_mfma_scale_f32_16x16x128_f8f6f4 v[138:141], v[122:127], v[14:19], 0, v178, v115 op_sel_hi:[0,0,0] cbsz:2 blgp:2
	v_mfma_scale_f32_16x16x128_f8f6f4 v[142:145], v[122:127], v[26:31], 0, v178, v115 op_sel_hi:[0,0,0] cbsz:2 blgp:2
	v_mfma_scale_f32_16x16x128_f8f6f4 v[134:137], v[122:127], v[38:43], v[134:137], v179, v115 op_sel_hi:[0,0,0] cbsz:2 blgp:2
	v_mfma_scale_f32_16x16x128_f8f6f4 v[138:141], v[122:127], v[50:55], v[138:141], v179, v115 op_sel_hi:[0,0,0] cbsz:2 blgp:2
	v_mfma_scale_f32_16x16x128_f8f6f4 v[142:145], v[122:127], v[62:67], v[142:145], v179, v115 op_sel_hi:[0,0,0] cbsz:2 blgp:2
	s_waitcnt lgkmcnt(0)
	v_mfma_scale_f32_16x16x128_f8f6f4 v[134:137], v[128:133], v[8:13], v[134:137], v178, v115 op_sel_hi:[0,0,0] cbsz:2 blgp:2
	v_mfma_scale_f32_16x16x128_f8f6f4 v[134:137], v[128:133], v[44:49], v[134:137], v179, v115 op_sel_hi:[0,0,0] cbsz:2 blgp:2
	v_mfma_scale_f32_16x16x128_f8f6f4 v[138:141], v[128:133], v[20:25], v[138:141], v178, v115 op_sel_hi:[0,0,0] cbsz:2 blgp:2
	v_mfma_scale_f32_16x16x128_f8f6f4 v[138:141], v[128:133], v[56:61], v[138:141], v179, v115 op_sel_hi:[0,0,0] cbsz:2 blgp:2
	v_mfma_scale_f32_16x16x128_f8f6f4 v[142:145], v[128:133], v[32:37], v[142:145], v178, v115 op_sel_hi:[0,0,0] cbsz:2 blgp:2
	v_mfma_scale_f32_16x16x128_f8f6f4 v[142:145], v[128:133], v[68:73], v[142:145], v179, v115 op_sel_hi:[0,0,0] cbsz:2 blgp:2
	v_fma_mix_f32 v158, v134, v1, v149 op_sel_hi:[0,0,1]
	v_exp_f32_e32 v158, v158
	v_fma_mix_f32 v159, v138, v99, v153 op_sel_hi:[0,0,1]
	v_exp_f32_e32 v159, v159
	v_add_f32_e32 v158, 1.0, v158
	v_rcp_f32_e32 v158, v158
	v_add_f32_e32 v159, 1.0, v159
	v_rcp_f32_e32 v159, v159
	v_fma_f32 v160, v142, v104, v105
	v_fma_mix_f32 v161, v158, v160, v157 op_sel_hi:[0,0,1]
	v_exp_f32_e32 v161, v161
	s_add_u32 s48, s48, s40
	v_add_f32_e32 v161, 1.0, v161
	v_rcp_f32_e32 v161, v161
	s_addc_u32 s49, s49, s41
	v_fma_f32 v162, v161, -2.0, 1.0
	v_sub_f32_e32 v163, v176, v162
	v_fma_f32 v176, v159, v163, v162
	v_fma_f32 v164, |v176|, s16, v117
	v_fma_f32 v165, |v176|, s17, v118
	v_fma_f32 v166, |v176|, s18, v119
	v_lshrrev_b32_e32 v167, 26, v176
	v_min3_u32 v164, v164, v165, v166
	v_bfi_b32 v168, 31, v164, v167
	v_lshrrev_b32_e32 v169, v181, v168
	global_store_short_d16_hi v185, v176, s[48:49]
	v_mul_u32_u24_dpp v170, v168, v180 quad_perm:[1,2,3,3] row_mask:0xf bank_mask:0xf bound_ctrl:1
	v_or_b32_e32 v171, v169, v170
	ds_write_b8 v184, v171 offset:416
	s_barrier
	ds_read_b64 v[122:123], v106 offset:416
	ds_read_b64 v[124:125], v106 offset:424
	ds_read_b64 v[126:127], v106 offset:432
	s_waitcnt lgkmcnt(3)
	s_barrier
	ds_read_b64 v[128:129], v106 offset:512
	ds_read_b64 v[130:131], v106 offset:520
	ds_read_b64 v[132:133], v106 offset:528
	s_add_i32 s44, s44, 16
	s_waitcnt lgkmcnt(3)
	v_mfma_scale_f32_16x16x128_f8f6f4 v[134:137], v[122:127], v[2:7], 0, v178, v115 op_sel_hi:[0,0,0] cbsz:2 blgp:2
	v_mfma_scale_f32_16x16x128_f8f6f4 v[138:141], v[122:127], v[14:19], 0, v178, v115 op_sel_hi:[0,0,0] cbsz:2 blgp:2
	v_mfma_scale_f32_16x16x128_f8f6f4 v[142:145], v[122:127], v[26:31], 0, v178, v115 op_sel_hi:[0,0,0] cbsz:2 blgp:2
	v_mfma_scale_f32_16x16x128_f8f6f4 v[134:137], v[122:127], v[38:43], v[134:137], v179, v115 op_sel_hi:[0,0,0] cbsz:2 blgp:2
	v_mfma_scale_f32_16x16x128_f8f6f4 v[138:141], v[122:127], v[50:55], v[138:141], v179, v115 op_sel_hi:[0,0,0] cbsz:2 blgp:2
	v_mfma_scale_f32_16x16x128_f8f6f4 v[142:145], v[122:127], v[62:67], v[142:145], v179, v115 op_sel_hi:[0,0,0] cbsz:2 blgp:2
	s_waitcnt lgkmcnt(0)
	v_mfma_scale_f32_16x16x128_f8f6f4 v[134:137], v[128:133], v[8:13], v[134:137], v178, v115 op_sel_hi:[0,0,0] cbsz:2 blgp:2
	v_mfma_scale_f32_16x16x128_f8f6f4 v[134:137], v[128:133], v[44:49], v[134:137], v179, v115 op_sel_hi:[0,0,0] cbsz:2 blgp:2
	v_mfma_scale_f32_16x16x128_f8f6f4 v[138:141], v[128:133], v[20:25], v[138:141], v178, v115 op_sel_hi:[0,0,0] cbsz:2 blgp:2
	v_mfma_scale_f32_16x16x128_f8f6f4 v[138:141], v[128:133], v[56:61], v[138:141], v179, v115 op_sel_hi:[0,0,0] cbsz:2 blgp:2
	v_mfma_scale_f32_16x16x128_f8f6f4 v[142:145], v[128:133], v[32:37], v[142:145], v178, v115 op_sel_hi:[0,0,0] cbsz:2 blgp:2
	v_mfma_scale_f32_16x16x128_f8f6f4 v[142:145], v[128:133], v[68:73], v[142:145], v179, v115 op_sel_hi:[0,0,0] cbsz:2 blgp:2
	v_fma_mix_f32 v158, v134, v1, v149 op_sel:[0,0,1] op_sel_hi:[0,0,1]
	v_exp_f32_e32 v158, v158
	v_fma_mix_f32 v159, v138, v99, v153 op_sel:[0,0,1] op_sel_hi:[0,0,1]
	v_exp_f32_e32 v159, v159
	v_add_f32_e32 v158, 1.0, v158
	v_rcp_f32_e32 v158, v158
	v_add_f32_e32 v159, 1.0, v159
	v_rcp_f32_e32 v159, v159
	v_fma_f32 v160, v142, v104, v105
	v_fma_mix_f32 v161, v158, v160, v157 op_sel:[0,0,1] op_sel_hi:[0,0,1]
	v_exp_f32_e32 v161, v161
	s_add_u32 s48, s48, s40
	v_add_f32_e32 v161, 1.0, v161
	v_rcp_f32_e32 v161, v161
	s_addc_u32 s49, s49, s41
	v_fma_f32 v162, v161, -2.0, 1.0
	v_sub_f32_e32 v163, v176, v162
	v_fma_f32 v176, v159, v163, v162
	v_fma_f32 v164, |v176|, s16, v117
	v_fma_f32 v165, |v176|, s17, v118
	v_fma_f32 v166, |v176|, s18, v119
	v_lshrrev_b32_e32 v167, 26, v176
	v_min3_u32 v164, v164, v165, v166
	v_bfi_b32 v168, 31, v164, v167
	v_lshrrev_b32_e32 v169, v181, v168
	global_store_short_d16_hi v185, v176, s[48:49]
	v_mul_u32_u24_dpp v170, v168, v180 quad_perm:[1,2,3,3] row_mask:0xf bank_mask:0xf bound_ctrl:1
	v_or_b32_e32 v171, v169, v170
	ds_write_b8 v184, v171
	s_barrier
	ds_read_b64 v[122:123], v106 offset:0
	ds_read_b64 v[124:125], v106 offset:8
	ds_read_b64 v[126:127], v106 offset:16
	s_cmp_lt_i32 s44, s45
	s_waitcnt lgkmcnt(3)
	s_barrier
	s_cbranch_scc1 .Lscan_loop_b_st

.Lscan_loop_a_f2:
	ds_read_b64 v[128:129], v105 offset:96
	ds_read_b64 v[130:131], v105 offset:104
	ds_read_b64 v[132:133], v105 offset:112
	s_waitcnt vmcnt(8)
	global_load_dwordx4 v[146:149], v[196:197], off
	global_load_dwordx4 v[150:153], v[196:197], off offset:512
	global_load_dwordx4 v[154:157], v[196:197], off offset:1024
	v_lshl_add_u64 v[196:197], v[196:197], 0, s[42:43]
	s_waitcnt lgkmcnt(3)
	v_mfma_scale_f32_16x16x128_f8f6f4 v[134:137], v[122:127], v[2:7], 0, v178, v112 op_sel_hi:[0,0,0] cbsz:2 blgp:2
	v_mfma_scale_f32_16x16x128_f8f6f4 v[138:141], v[122:127], v[14:19], 0, v178, v112 op_sel_hi:[0,0,0] cbsz:2 blgp:2
	v_mfma_scale_f32_16x16x128_f8f6f4 v[142:145], v[122:127], v[26:31], 0, v178, v112 op_sel_hi:[0,0,0] cbsz:2 blgp:2
	v_mfma_scale_f32_16x16x128_f8f6f4 v[134:137], v[122:127], v[38:43], v[134:137], v179, v112 op_sel_hi:[0,0,0] cbsz:2 blgp:2
	v_mfma_scale_f32_16x16x128_f8f6f4 v[138:141], v[122:127], v[50:55], v[138:141], v179, v112 op_sel_hi:[0,0,0] cbsz:2 blgp:2
	v_mfma_scale_f32_16x16x128_f8f6f4 v[142:145], v[122:127], v[62:67], v[142:145], v179, v112 op_sel_hi:[0,0,0] cbsz:2 blgp:2
	s_waitcnt lgkmcnt(0)
	v_mfma_scale_f32_16x16x128_f8f6f4 v[134:137], v[128:133], v[8:13], v[134:137], v178, v112 op_sel_hi:[0,0,0] cbsz:2 blgp:2
	v_mfma_scale_f32_16x16x128_f8f6f4 v[134:137], v[128:133], v[44:49], v[134:137], v179, v112 op_sel_hi:[0,0,0] cbsz:2 blgp:2
	v_mfma_scale_f32_16x16x128_f8f6f4 v[138:141], v[128:133], v[20:25], v[138:141], v178, v112 op_sel_hi:[0,0,0] cbsz:2 blgp:2
	v_mfma_scale_f32_16x16x128_f8f6f4 v[138:141], v[128:133], v[56:61], v[138:141], v179, v112 op_sel_hi:[0,0,0] cbsz:2 blgp:2
	v_mfma_scale_f32_16x16x128_f8f6f4 v[142:145], v[128:133], v[32:37], v[142:145], v178, v112 op_sel_hi:[0,0,0] cbsz:2 blgp:2
	v_mfma_scale_f32_16x16x128_f8f6f4 v[142:145], v[128:133], v[68:73], v[142:145], v179, v112 op_sel_hi:[0,0,0] cbsz:2 blgp:2
	v_fma_mix_f32 v158, v134, v100, v82 op_sel_hi:[0,0,1]
	v_exp_f32_e32 v158, v158
	v_fma_mix_f32 v159, v138, v101, v74 op_sel_hi:[0,0,1]
	v_exp_f32_e32 v159, v159
	v_add_f32_e32 v158, 1.0, v158
	v_rcp_f32_e32 v158, v158
	v_add_f32_e32 v159, 1.0, v159
	v_rcp_f32_e32 v159, v159
	v_fma_f32 v160, v142, v102, v103
	v_fma_mix_f32 v161, v158, v160, v78 op_sel_hi:[0,0,1]
	v_exp_f32_e32 v161, v161
	s_add_u32 s48, s48, s40
	v_add_f32_e32 v161, 1.0, v161
	v_rcp_f32_e32 v161, v161
	s_addc_u32 s49, s49, s41
	v_fma_f32 v162, v161, -2.0, 1.0
	v_sub_f32_e32 v163, v176, v162
	v_fma_f32 v176, v159, v163, v162
	v_fma_f32 v164, |v176|, s17, v113
	v_fma_f32 v165, |v176|, s18, v114
	v_fma_f32 v166, |v176|, s19, v115
	v_lshrrev_b32_e32 v167, 26, v176
	v_min3_u32 v164, v164, v165, v166
	v_bfi_b32 v168, 31, v164, v167
	v_lshrrev_b32_e32 v169, v181, v168
	global_store_short_d16_hi v185, v176, s[48:49]
	v_mul_u32_u24_dpp v170, v168, v180 quad_perm:[1,2,3,3] row_mask:0xf bank_mask:0xf bound_ctrl:1
	v_or_b32_e32 v171, v169, v170
	ds_write_b8 v184, v171 offset:416
	s_waitcnt lgkmcnt(0)
	s_barrier
	ds_read_b64 v[122:123], v105 offset:416
	ds_read_b64 v[124:125], v105 offset:424
	ds_read_b64 v[126:127], v105 offset:432
	s_barrier
	ds_read_b64 v[128:129], v105 offset:512
	ds_read_b64 v[130:131], v105 offset:520
	ds_read_b64 v[132:133], v105 offset:528
	s_waitcnt lgkmcnt(3)
	v_mfma_scale_f32_16x16x128_f8f6f4 v[134:137], v[122:127], v[2:7], 0, v178, v112 op_sel_hi:[0,0,0] cbsz:2 blgp:2
	v_mfma_scale_f32_16x16x128_f8f6f4 v[138:141], v[122:127], v[14:19], 0, v178, v112 op_sel_hi:[0,0,0] cbsz:2 blgp:2
	v_mfma_scale_f32_16x16x128_f8f6f4 v[142:145], v[122:127], v[26:31], 0, v178, v112 op_sel_hi:[0,0,0] cbsz:2 blgp:2
	v_mfma_scale_f32_16x16x128_f8f6f4 v[134:137], v[122:127], v[38:43], v[134:137], v179, v112 op_sel_hi:[0,0,0] cbsz:2 blgp:2
	v_mfma_scale_f32_16x16x128_f8f6f4 v[138:141], v[122:127], v[50:55], v[138:141], v179, v112 op_sel_hi:[0,0,0] cbsz:2 blgp:2
	v_mfma_scale_f32_16x16x128_f8f6f4 v[142:145], v[122:127], v[62:67], v[142:145], v179, v112 op_sel_hi:[0,0,0] cbsz:2 blgp:2
	s_waitcnt lgkmcnt(0)
	v_mfma_scale_f32_16x16x128_f8f6f4 v[134:137], v[128:133], v[8:13], v[134:137], v178, v112 op_sel_hi:[0,0,0] cbsz:2 blgp:2
	v_mfma_scale_f32_16x16x128_f8f6f4 v[134:137], v[128:133], v[44:49], v[134:137], v179, v112 op_sel_hi:[0,0,0] cbsz:2 blgp:2
	v_mfma_scale_f32_16x16x128_f8f6f4 v[138:141], v[128:133], v[20:25], v[138:141], v178, v112 op_sel_hi:[0,0,0] cbsz:2 blgp:2
	v_mfma_scale_f32_16x16x128_f8f6f4 v[138:141], v[128:133], v[56:61], v[138:141], v179, v112 op_sel_hi:[0,0,0] cbsz:2 blgp:2
	v_mfma_scale_f32_16x16x128_f8f6f4 v[142:145], v[128:133], v[32:37], v[142:145], v178, v112 op_sel_hi:[0,0,0] cbsz:2 blgp:2
	v_mfma_scale_f32_16x16x128_f8f6f4 v[142:145], v[128:133], v[68:73], v[142:145], v179, v112 op_sel_hi:[0,0,0] cbsz:2 blgp:2
	v_fma_mix_f32 v158, v134, v100, v82 op_sel:[0,0,1] op_sel_hi:[0,0,1]
	v_exp_f32_e32 v158, v158
	v_fma_mix_f32 v159, v138, v101, v74 op_sel:[0,0,1] op_sel_hi:[0,0,1]
	v_exp_f32_e32 v159, v159
	v_add_f32_e32 v158, 1.0, v158
	v_rcp_f32_e32 v158, v158
	v_add_f32_e32 v159, 1.0, v159
	v_rcp_f32_e32 v159, v159
	v_fma_f32 v160, v142, v102, v103
	v_fma_mix_f32 v161, v158, v160, v78 op_sel:[0,0,1] op_sel_hi:[0,0,1]
	v_exp_f32_e32 v161, v161
	s_add_u32 s48, s48, s40
	v_add_f32_e32 v161, 1.0, v161
	v_rcp_f32_e32 v161, v161
	s_addc_u32 s49, s49, s41
	v_fma_f32 v162, v161, -2.0, 1.0
	v_sub_f32_e32 v163, v176, v162
	v_fma_f32 v176, v159, v163, v162
	v_fma_f32 v164, |v176|, s17, v113
	v_fma_f32 v165, |v176|, s18, v114
	v_fma_f32 v166, |v176|, s19, v115
	v_lshrrev_b32_e32 v167, 26, v176
	v_min3_u32 v164, v164, v165, v166
	v_bfi_b32 v168, 31, v164, v167
	v_lshrrev_b32_e32 v169, v181, v168
	global_store_short_d16_hi v185, v176, s[48:49]
	v_mul_u32_u24_dpp v170, v168, v180 quad_perm:[1,2,3,3] row_mask:0xf bank_mask:0xf bound_ctrl:1
	v_or_b32_e32 v171, v169, v170
	ds_write_b8 v184, v171
	s_waitcnt lgkmcnt(0)
	s_barrier
	ds_read_b64 v[122:123], v105 offset:0
	ds_read_b64 v[124:125], v105 offset:8
	ds_read_b64 v[126:127], v105 offset:16
	s_barrier
	ds_read_b64 v[128:129], v105 offset:96
	ds_read_b64 v[130:131], v105 offset:104
	ds_read_b64 v[132:133], v105 offset:112
	s_waitcnt lgkmcnt(3)
	v_mfma_scale_f32_16x16x128_f8f6f4 v[134:137], v[122:127], v[2:7], 0, v178, v112 op_sel_hi:[0,0,0] cbsz:2 blgp:2
	v_mfma_scale_f32_16x16x128_f8f6f4 v[138:141], v[122:127], v[14:19], 0, v178, v112 op_sel_hi:[0,0,0] cbsz:2 blgp:2
	v_mfma_scale_f32_16x16x128_f8f6f4 v[142:145], v[122:127], v[26:31], 0, v178, v112 op_sel_hi:[0,0,0] cbsz:2 blgp:2
	v_mfma_scale_f32_16x16x128_f8f6f4 v[134:137], v[122:127], v[38:43], v[134:137], v179, v112 op_sel_hi:[0,0,0] cbsz:2 blgp:2
	v_mfma_scale_f32_16x16x128_f8f6f4 v[138:141], v[122:127], v[50:55], v[138:141], v179, v112 op_sel_hi:[0,0,0] cbsz:2 blgp:2
	v_mfma_scale_f32_16x16x128_f8f6f4 v[142:145], v[122:127], v[62:67], v[142:145], v179, v112 op_sel_hi:[0,0,0] cbsz:2 blgp:2
	s_waitcnt lgkmcnt(0)
	v_mfma_scale_f32_16x16x128_f8f6f4 v[134:137], v[128:133], v[8:13], v[134:137], v178, v112 op_sel_hi:[0,0,0] cbsz:2 blgp:2
	v_mfma_scale_f32_16x16x128_f8f6f4 v[134:137], v[128:133], v[44:49], v[134:137], v179, v112 op_sel_hi:[0,0,0] cbsz:2 blgp:2
	v_mfma_scale_f32_16x16x128_f8f6f4 v[138:141], v[128:133], v[20:25], v[138:141], v178, v112 op_sel_hi:[0,0,0] cbsz:2 blgp:2
	v_mfma_scale_f32_16x16x128_f8f6f4 v[138:141], v[128:133], v[56:61], v[138:141], v179, v112 op_sel_hi:[0,0,0] cbsz:2 blgp:2
	v_mfma_scale_f32_16x16x128_f8f6f4 v[142:145], v[128:133], v[32:37], v[142:145], v178, v112 op_sel_hi:[0,0,0] cbsz:2 blgp:2
	v_mfma_scale_f32_16x16x128_f8f6f4 v[142:145], v[128:133], v[68:73], v[142:145], v179, v112 op_sel_hi:[0,0,0] cbsz:2 blgp:2
	v_fma_mix_f32 v158, v134, v100, v83 op_sel_hi:[0,0,1]
	v_exp_f32_e32 v158, v158
	v_fma_mix_f32 v159, v138, v101, v75 op_sel_hi:[0,0,1]
	v_exp_f32_e32 v159, v159
	v_add_f32_e32 v158, 1.0, v158
	v_rcp_f32_e32 v158, v158
	v_add_f32_e32 v159, 1.0, v159
	v_rcp_f32_e32 v159, v159
	v_fma_f32 v160, v142, v102, v103
	v_fma_mix_f32 v161, v158, v160, v79 op_sel_hi:[0,0,1]
	v_exp_f32_e32 v161, v161
	s_add_u32 s48, s48, s40
	v_add_f32_e32 v161, 1.0, v161
	v_rcp_f32_e32 v161, v161
	s_addc_u32 s49, s49, s41
	v_fma_f32 v162, v161, -2.0, 1.0
	v_sub_f32_e32 v163, v176, v162
	v_fma_f32 v176, v159, v163, v162
	v_fma_f32 v164, |v176|, s17, v113
	v_fma_f32 v165, |v176|, s18, v114
	v_fma_f32 v166, |v176|, s19, v115
	v_lshrrev_b32_e32 v167, 26, v176
	v_min3_u32 v164, v164, v165, v166
	v_bfi_b32 v168, 31, v164, v167
	v_lshrrev_b32_e32 v169, v181, v168
	global_store_short_d16_hi v185, v176, s[48:49]
	v_mul_u32_u24_dpp v170, v168, v180 quad_perm:[1,2,3,3] row_mask:0xf bank_mask:0xf bound_ctrl:1
	v_or_b32_e32 v171, v169, v170
	ds_write_b8 v184, v171 offset:416
	s_waitcnt lgkmcnt(0)
	s_barrier
	ds_read_b64 v[122:123], v105 offset:416
	ds_read_b64 v[124:125], v105 offset:424
	ds_read_b64 v[126:127], v105 offset:432
	s_barrier
	ds_read_b64 v[128:129], v105 offset:512
	ds_read_b64 v[130:131], v105 offset:520
	ds_read_b64 v[132:133], v105 offset:528
	s_waitcnt lgkmcnt(3)
	v_mfma_scale_f32_16x16x128_f8f6f4 v[134:137], v[122:127], v[2:7], 0, v178, v112 op_sel_hi:[0,0,0] cbsz:2 blgp:2
	v_mfma_scale_f32_16x16x128_f8f6f4 v[138:141], v[122:127], v[14:19], 0, v178, v112 op_sel_hi:[0,0,0] cbsz:2 blgp:2
	v_mfma_scale_f32_16x16x128_f8f6f4 v[142:145], v[122:127], v[26:31], 0, v178, v112 op_sel_hi:[0,0,0] cbsz:2 blgp:2
	v_mfma_scale_f32_16x16x128_f8f6f4 v[134:137], v[122:127], v[38:43], v[134:137], v179, v112 op_sel_hi:[0,0,0] cbsz:2 blgp:2
	v_mfma_scale_f32_16x16x128_f8f6f4 v[138:141], v[122:127], v[50:55], v[138:141], v179, v112 op_sel_hi:[0,0,0] cbsz:2 blgp:2
	v_mfma_scale_f32_16x16x128_f8f6f4 v[142:145], v[122:127], v[62:67], v[142:145], v179, v112 op_sel_hi:[0,0,0] cbsz:2 blgp:2
	s_waitcnt lgkmcnt(0)
	v_mfma_scale_f32_16x16x128_f8f6f4 v[134:137], v[128:133], v[8:13], v[134:137], v178, v112 op_sel_hi:[0,0,0] cbsz:2 blgp:2
	v_mfma_scale_f32_16x16x128_f8f6f4 v[134:137], v[128:133], v[44:49], v[134:137], v179, v112 op_sel_hi:[0,0,0] cbsz:2 blgp:2
	v_mfma_scale_f32_16x16x128_f8f6f4 v[138:141], v[128:133], v[20:25], v[138:141], v178, v112 op_sel_hi:[0,0,0] cbsz:2 blgp:2
	v_mfma_scale_f32_16x16x128_f8f6f4 v[138:141], v[128:133], v[56:61], v[138:141], v179, v112 op_sel_hi:[0,0,0] cbsz:2 blgp:2
	v_mfma_scale_f32_16x16x128_f8f6f4 v[142:145], v[128:133], v[32:37], v[142:145], v178, v112 op_sel_hi:[0,0,0] cbsz:2 blgp:2
	v_mfma_scale_f32_16x16x128_f8f6f4 v[142:145], v[128:133], v[68:73], v[142:145], v179, v112 op_sel_hi:[0,0,0] cbsz:2 blgp:2
	v_fma_mix_f32 v158, v134, v100, v83 op_sel:[0,0,1] op_sel_hi:[0,0,1]
	v_exp_f32_e32 v158, v158
	v_fma_mix_f32 v159, v138, v101, v75 op_sel:[0,0,1] op_sel_hi:[0,0,1]
	v_exp_f32_e32 v159, v159
	v_add_f32_e32 v158, 1.0, v158
	v_rcp_f32_e32 v158, v158
	v_add_f32_e32 v159, 1.0, v159
	v_rcp_f32_e32 v159, v159
	v_fma_f32 v160, v142, v102, v103
	v_fma_mix_f32 v161, v158, v160, v79 op_sel:[0,0,1] op_sel_hi:[0,0,1]
	v_exp_f32_e32 v161, v161
	s_add_u32 s48, s48, s40
	v_add_f32_e32 v161, 1.0, v161
	v_rcp_f32_e32 v161, v161
	s_addc_u32 s49, s49, s41
	v_fma_f32 v162, v161, -2.0, 1.0
	v_sub_f32_e32 v163, v176, v162
	v_fma_f32 v176, v159, v163, v162
	v_fma_f32 v164, |v176|, s17, v113
	v_fma_f32 v165, |v176|, s18, v114
	v_fma_f32 v166, |v176|, s19, v115
	v_lshrrev_b32_e32 v167, 26, v176
	v_min3_u32 v164, v164, v165, v166
	v_bfi_b32 v168, 31, v164, v167
	v_lshrrev_b32_e32 v169, v181, v168
	global_store_short_d16_hi v185, v176, s[48:49]
	v_mul_u32_u24_dpp v170, v168, v180 quad_perm:[1,2,3,3] row_mask:0xf bank_mask:0xf bound_ctrl:1
	v_or_b32_e32 v171, v169, v170
	ds_write_b8 v184, v171
	s_waitcnt lgkmcnt(0)
	s_barrier
	ds_read_b64 v[122:123], v105 offset:0
	ds_read_b64 v[124:125], v105 offset:8
	ds_read_b64 v[126:127], v105 offset:16
	s_barrier
	ds_read_b64 v[128:129], v105 offset:96
	ds_read_b64 v[130:131], v105 offset:104
	ds_read_b64 v[132:133], v105 offset:112
	s_waitcnt lgkmcnt(3)
	v_mfma_scale_f32_16x16x128_f8f6f4 v[134:137], v[122:127], v[2:7], 0, v178, v112 op_sel_hi:[0,0,0] cbsz:2 blgp:2
	v_mfma_scale_f32_16x16x128_f8f6f4 v[138:141], v[122:127], v[14:19], 0, v178, v112 op_sel_hi:[0,0,0] cbsz:2 blgp:2
	v_mfma_scale_f32_16x16x128_f8f6f4 v[142:145], v[122:127], v[26:31], 0, v178, v112 op_sel_hi:[0,0,0] cbsz:2 blgp:2
	v_mfma_scale_f32_16x16x128_f8f6f4 v[134:137], v[122:127], v[38:43], v[134:137], v179, v112 op_sel_hi:[0,0,0] cbsz:2 blgp:2
	v_mfma_scale_f32_16x16x128_f8f6f4 v[138:141], v[122:127], v[50:55], v[138:141], v179, v112 op_sel_hi:[0,0,0] cbsz:2 blgp:2
	v_mfma_scale_f32_16x16x128_f8f6f4 v[142:145], v[122:127], v[62:67], v[142:145], v179, v112 op_sel_hi:[0,0,0] cbsz:2 blgp:2
	s_waitcnt lgkmcnt(0)
	v_mfma_scale_f32_16x16x128_f8f6f4 v[134:137], v[128:133], v[8:13], v[134:137], v178, v112 op_sel_hi:[0,0,0] cbsz:2 blgp:2
	v_mfma_scale_f32_16x16x128_f8f6f4 v[134:137], v[128:133], v[44:49], v[134:137], v179, v112 op_sel_hi:[0,0,0] cbsz:2 blgp:2
	v_mfma_scale_f32_16x16x128_f8f6f4 v[138:141], v[128:133], v[20:25], v[138:141], v178, v112 op_sel_hi:[0,0,0] cbsz:2 blgp:2
	v_mfma_scale_f32_16x16x128_f8f6f4 v[138:141], v[128:133], v[56:61], v[138:141], v179, v112 op_sel_hi:[0,0,0] cbsz:2 blgp:2
	v_mfma_scale_f32_16x16x128_f8f6f4 v[142:145], v[128:133], v[32:37], v[142:145], v178, v112 op_sel_hi:[0,0,0] cbsz:2 blgp:2
	v_mfma_scale_f32_16x16x128_f8f6f4 v[142:145], v[128:133], v[68:73], v[142:145], v179, v112 op_sel_hi:[0,0,0] cbsz:2 blgp:2
	v_fma_mix_f32 v158, v134, v100, v84 op_sel_hi:[0,0,1]
	v_exp_f32_e32 v158, v158
	v_fma_mix_f32 v159, v138, v101, v76 op_sel_hi:[0,0,1]
	v_exp_f32_e32 v159, v159
	v_add_f32_e32 v158, 1.0, v158
	v_rcp_f32_e32 v158, v158
	v_add_f32_e32 v159, 1.0, v159
	v_rcp_f32_e32 v159, v159
	v_fma_f32 v160, v142, v102, v103
	v_fma_mix_f32 v161, v158, v160, v80 op_sel_hi:[0,0,1]
	v_exp_f32_e32 v161, v161
	s_add_u32 s48, s48, s40
	v_add_f32_e32 v161, 1.0, v161
	v_rcp_f32_e32 v161, v161
	s_addc_u32 s49, s49, s41
	v_fma_f32 v162, v161, -2.0, 1.0
	v_sub_f32_e32 v163, v176, v162
	v_fma_f32 v176, v159, v163, v162
	v_fma_f32 v164, |v176|, s17, v113
	v_fma_f32 v165, |v176|, s18, v114
	v_fma_f32 v166, |v176|, s19, v115
	v_lshrrev_b32_e32 v167, 26, v176
	v_min3_u32 v164, v164, v165, v166
	v_bfi_b32 v168, 31, v164, v167
	v_lshrrev_b32_e32 v169, v181, v168
	global_store_short_d16_hi v185, v176, s[48:49]
	v_mul_u32_u24_dpp v170, v168, v180 quad_perm:[1,2,3,3] row_mask:0xf bank_mask:0xf bound_ctrl:1
	v_or_b32_e32 v171, v169, v170
	ds_write_b8 v184, v171 offset:416
	s_waitcnt lgkmcnt(0)
	s_barrier
	ds_read_b64 v[122:123], v105 offset:416
	ds_read_b64 v[124:125], v105 offset:424
	ds_read_b64 v[126:127], v105 offset:432
	s_barrier
	ds_read_b64 v[128:129], v105 offset:512
	ds_read_b64 v[130:131], v105 offset:520
	ds_read_b64 v[132:133], v105 offset:528
	s_waitcnt lgkmcnt(3)
	v_mfma_scale_f32_16x16x128_f8f6f4 v[134:137], v[122:127], v[2:7], 0, v178, v112 op_sel_hi:[0,0,0] cbsz:2 blgp:2
	v_mfma_scale_f32_16x16x128_f8f6f4 v[138:141], v[122:127], v[14:19], 0, v178, v112 op_sel_hi:[0,0,0] cbsz:2 blgp:2
	v_mfma_scale_f32_16x16x128_f8f6f4 v[142:145], v[122:127], v[26:31], 0, v178, v112 op_sel_hi:[0,0,0] cbsz:2 blgp:2
	v_mfma_scale_f32_16x16x128_f8f6f4 v[134:137], v[122:127], v[38:43], v[134:137], v179, v112 op_sel_hi:[0,0,0] cbsz:2 blgp:2
	v_mfma_scale_f32_16x16x128_f8f6f4 v[138:141], v[122:127], v[50:55], v[138:141], v179, v112 op_sel_hi:[0,0,0] cbsz:2 blgp:2
	v_mfma_scale_f32_16x16x128_f8f6f4 v[142:145], v[122:127], v[62:67], v[142:145], v179, v112 op_sel_hi:[0,0,0] cbsz:2 blgp:2
	s_waitcnt lgkmcnt(0)
	v_mfma_scale_f32_16x16x128_f8f6f4 v[134:137], v[128:133], v[8:13], v[134:137], v178, v112 op_sel_hi:[0,0,0] cbsz:2 blgp:2
	v_mfma_scale_f32_16x16x128_f8f6f4 v[134:137], v[128:133], v[44:49], v[134:137], v179, v112 op_sel_hi:[0,0,0] cbsz:2 blgp:2
	v_mfma_scale_f32_16x16x128_f8f6f4 v[138:141], v[128:133], v[20:25], v[138:141], v178, v112 op_sel_hi:[0,0,0] cbsz:2 blgp:2
	v_mfma_scale_f32_16x16x128_f8f6f4 v[138:141], v[128:133], v[56:61], v[138:141], v179, v112 op_sel_hi:[0,0,0] cbsz:2 blgp:2
	v_mfma_scale_f32_16x16x128_f8f6f4 v[142:145], v[128:133], v[32:37], v[142:145], v178, v112 op_sel_hi:[0,0,0] cbsz:2 blgp:2
	v_mfma_scale_f32_16x16x128_f8f6f4 v[142:145], v[128:133], v[68:73], v[142:145], v179, v112 op_sel_hi:[0,0,0] cbsz:2 blgp:2
	v_fma_mix_f32 v158, v134, v100, v84 op_sel:[0,0,1] op_sel_hi:[0,0,1]
	v_exp_f32_e32 v158, v158
	v_fma_mix_f32 v159, v138, v101, v76 op_sel:[0,0,1] op_sel_hi:[0,0,1]
	v_exp_f32_e32 v159, v159
	v_add_f32_e32 v158, 1.0, v158
	v_rcp_f32_e32 v158, v158
	v_add_f32_e32 v159, 1.0, v159
	v_rcp_f32_e32 v159, v159
	v_fma_f32 v160, v142, v102, v103
	v_fma_mix_f32 v161, v158, v160, v80 op_sel:[0,0,1] op_sel_hi:[0,0,1]
	v_exp_f32_e32 v161, v161
	s_add_u32 s48, s48, s40
	v_add_f32_e32 v161, 1.0, v161
	v_rcp_f32_e32 v161, v161
	s_addc_u32 s49, s49, s41
	v_fma_f32 v162, v161, -2.0, 1.0
	v_sub_f32_e32 v163, v176, v162
	v_fma_f32 v176, v159, v163, v162
	v_fma_f32 v164, |v176|, s17, v113
	v_fma_f32 v165, |v176|, s18, v114
	v_fma_f32 v166, |v176|, s19, v115
	v_lshrrev_b32_e32 v167, 26, v176
	v_min3_u32 v164, v164, v165, v166
	v_bfi_b32 v168, 31, v164, v167
	v_lshrrev_b32_e32 v169, v181, v168
	global_store_short_d16_hi v185, v176, s[48:49]
	v_mul_u32_u24_dpp v170, v168, v180 quad_perm:[1,2,3,3] row_mask:0xf bank_mask:0xf bound_ctrl:1
	v_or_b32_e32 v171, v169, v170
	ds_write_b8 v184, v171
	s_waitcnt lgkmcnt(0)
	s_barrier
	ds_read_b64 v[122:123], v105 offset:0
	ds_read_b64 v[124:125], v105 offset:8
	ds_read_b64 v[126:127], v105 offset:16
	s_barrier
	ds_read_b64 v[128:129], v105 offset:96
	ds_read_b64 v[130:131], v105 offset:104
	ds_read_b64 v[132:133], v105 offset:112
	s_waitcnt lgkmcnt(3)
	v_mfma_scale_f32_16x16x128_f8f6f4 v[134:137], v[122:127], v[2:7], 0, v178, v112 op_sel_hi:[0,0,0] cbsz:2 blgp:2
	v_mfma_scale_f32_16x16x128_f8f6f4 v[138:141], v[122:127], v[14:19], 0, v178, v112 op_sel_hi:[0,0,0] cbsz:2 blgp:2
	v_mfma_scale_f32_16x16x128_f8f6f4 v[142:145], v[122:127], v[26:31], 0, v178, v112 op_sel_hi:[0,0,0] cbsz:2 blgp:2
	v_mfma_scale_f32_16x16x128_f8f6f4 v[134:137], v[122:127], v[38:43], v[134:137], v179, v112 op_sel_hi:[0,0,0] cbsz:2 blgp:2
	v_mfma_scale_f32_16x16x128_f8f6f4 v[138:141], v[122:127], v[50:55], v[138:141], v179, v112 op_sel_hi:[0,0,0] cbsz:2 blgp:2
	v_mfma_scale_f32_16x16x128_f8f6f4 v[142:145], v[122:127], v[62:67], v[142:145], v179, v112 op_sel_hi:[0,0,0] cbsz:2 blgp:2
	s_waitcnt lgkmcnt(0)
	v_mfma_scale_f32_16x16x128_f8f6f4 v[134:137], v[128:133], v[8:13], v[134:137], v178, v112 op_sel_hi:[0,0,0] cbsz:2 blgp:2
	v_mfma_scale_f32_16x16x128_f8f6f4 v[134:137], v[128:133], v[44:49], v[134:137], v179, v112 op_sel_hi:[0,0,0] cbsz:2 blgp:2
	v_mfma_scale_f32_16x16x128_f8f6f4 v[138:141], v[128:133], v[20:25], v[138:141], v178, v112 op_sel_hi:[0,0,0] cbsz:2 blgp:2
	v_mfma_scale_f32_16x16x128_f8f6f4 v[138:141], v[128:133], v[56:61], v[138:141], v179, v112 op_sel_hi:[0,0,0] cbsz:2 blgp:2
	v_mfma_scale_f32_16x16x128_f8f6f4 v[142:145], v[128:133], v[32:37], v[142:145], v178, v112 op_sel_hi:[0,0,0] cbsz:2 blgp:2
	v_mfma_scale_f32_16x16x128_f8f6f4 v[142:145], v[128:133], v[68:73], v[142:145], v179, v112 op_sel_hi:[0,0,0] cbsz:2 blgp:2
	v_fma_mix_f32 v158, v134, v100, v85 op_sel_hi:[0,0,1]
	v_exp_f32_e32 v158, v158
	v_fma_mix_f32 v159, v138, v101, v77 op_sel_hi:[0,0,1]
	v_exp_f32_e32 v159, v159
	v_add_f32_e32 v158, 1.0, v158
	v_rcp_f32_e32 v158, v158
	v_add_f32_e32 v159, 1.0, v159
	v_rcp_f32_e32 v159, v159
	v_fma_f32 v160, v142, v102, v103
	v_fma_mix_f32 v161, v158, v160, v81 op_sel_hi:[0,0,1]
	v_exp_f32_e32 v161, v161
	s_add_u32 s48, s48, s40
	v_add_f32_e32 v161, 1.0, v161
	v_rcp_f32_e32 v161, v161
	s_addc_u32 s49, s49, s41
	v_fma_f32 v162, v161, -2.0, 1.0
	v_sub_f32_e32 v163, v176, v162
	v_fma_f32 v176, v159, v163, v162
	v_fma_f32 v164, |v176|, s17, v113
	v_fma_f32 v165, |v176|, s18, v114
	v_fma_f32 v166, |v176|, s19, v115
	v_lshrrev_b32_e32 v167, 26, v176
	v_min3_u32 v164, v164, v165, v166
	v_bfi_b32 v168, 31, v164, v167
	v_lshrrev_b32_e32 v169, v181, v168
	global_store_short_d16_hi v185, v176, s[48:49]
	v_mul_u32_u24_dpp v170, v168, v180 quad_perm:[1,2,3,3] row_mask:0xf bank_mask:0xf bound_ctrl:1
	v_or_b32_e32 v171, v169, v170
	ds_write_b8 v184, v171 offset:416
	s_waitcnt lgkmcnt(0)
	s_barrier
	ds_read_b64 v[122:123], v105 offset:416
	ds_read_b64 v[124:125], v105 offset:424
	ds_read_b64 v[126:127], v105 offset:432
	s_barrier
	ds_read_b64 v[128:129], v105 offset:512
	ds_read_b64 v[130:131], v105 offset:520
	ds_read_b64 v[132:133], v105 offset:528
	s_waitcnt lgkmcnt(3)
	v_mfma_scale_f32_16x16x128_f8f6f4 v[134:137], v[122:127], v[2:7], 0, v178, v112 op_sel_hi:[0,0,0] cbsz:2 blgp:2
	v_mfma_scale_f32_16x16x128_f8f6f4 v[138:141], v[122:127], v[14:19], 0, v178, v112 op_sel_hi:[0,0,0] cbsz:2 blgp:2
	v_mfma_scale_f32_16x16x128_f8f6f4 v[142:145], v[122:127], v[26:31], 0, v178, v112 op_sel_hi:[0,0,0] cbsz:2 blgp:2
	v_mfma_scale_f32_16x16x128_f8f6f4 v[134:137], v[122:127], v[38:43], v[134:137], v179, v112 op_sel_hi:[0,0,0] cbsz:2 blgp:2
	v_mfma_scale_f32_16x16x128_f8f6f4 v[138:141], v[122:127], v[50:55], v[138:141], v179, v112 op_sel_hi:[0,0,0] cbsz:2 blgp:2
	v_mfma_scale_f32_16x16x128_f8f6f4 v[142:145], v[122:127], v[62:67], v[142:145], v179, v112 op_sel_hi:[0,0,0] cbsz:2 blgp:2
	s_waitcnt lgkmcnt(0)
	v_mfma_scale_f32_16x16x128_f8f6f4 v[134:137], v[128:133], v[8:13], v[134:137], v178, v112 op_sel_hi:[0,0,0] cbsz:2 blgp:2
	v_mfma_scale_f32_16x16x128_f8f6f4 v[134:137], v[128:133], v[44:49], v[134:137], v179, v112 op_sel_hi:[0,0,0] cbsz:2 blgp:2
	v_mfma_scale_f32_16x16x128_f8f6f4 v[138:141], v[128:133], v[20:25], v[138:141], v178, v112 op_sel_hi:[0,0,0] cbsz:2 blgp:2
	v_mfma_scale_f32_16x16x128_f8f6f4 v[138:141], v[128:133], v[56:61], v[138:141], v179, v112 op_sel_hi:[0,0,0] cbsz:2 blgp:2
	v_mfma_scale_f32_16x16x128_f8f6f4 v[142:145], v[128:133], v[32:37], v[142:145], v178, v112 op_sel_hi:[0,0,0] cbsz:2 blgp:2
	v_mfma_scale_f32_16x16x128_f8f6f4 v[142:145], v[128:133], v[68:73], v[142:145], v179, v112 op_sel_hi:[0,0,0] cbsz:2 blgp:2
	v_fma_mix_f32 v158, v134, v100, v85 op_sel:[0,0,1] op_sel_hi:[0,0,1]
	v_exp_f32_e32 v158, v158
	v_fma_mix_f32 v159, v138, v101, v77 op_sel:[0,0,1] op_sel_hi:[0,0,1]
	v_exp_f32_e32 v159, v159
	v_add_f32_e32 v158, 1.0, v158
	v_rcp_f32_e32 v158, v158
	v_add_f32_e32 v159, 1.0, v159
	v_rcp_f32_e32 v159, v159
	v_fma_f32 v160, v142, v102, v103
	v_fma_mix_f32 v161, v158, v160, v81 op_sel:[0,0,1] op_sel_hi:[0,0,1]
	v_exp_f32_e32 v161, v161
	s_add_u32 s48, s48, s40
	v_add_f32_e32 v161, 1.0, v161
	v_rcp_f32_e32 v161, v161
	s_addc_u32 s49, s49, s41
	v_fma_f32 v162, v161, -2.0, 1.0
	v_sub_f32_e32 v163, v176, v162
	v_fma_f32 v176, v159, v163, v162
	v_fma_f32 v164, |v176|, s17, v113
	v_fma_f32 v165, |v176|, s18, v114
	v_fma_f32 v166, |v176|, s19, v115
	v_lshrrev_b32_e32 v167, 26, v176
	v_min3_u32 v164, v164, v165, v166
	v_bfi_b32 v168, 31, v164, v167
	v_lshrrev_b32_e32 v169, v181, v168
	global_store_short_d16_hi v185, v176, s[48:49]
	v_mul_u32_u24_dpp v170, v168, v180 quad_perm:[1,2,3,3] row_mask:0xf bank_mask:0xf bound_ctrl:1
	v_or_b32_e32 v171, v169, v170
	ds_write_b8 v184, v171
	s_waitcnt lgkmcnt(0)
	s_barrier
	ds_read_b64 v[122:123], v105 offset:0
	ds_read_b64 v[124:125], v105 offset:8
	ds_read_b64 v[126:127], v105 offset:16
	s_barrier
	ds_read_b64 v[128:129], v105 offset:96
	ds_read_b64 v[130:131], v105 offset:104
	ds_read_b64 v[132:133], v105 offset:112
	s_waitcnt vmcnt(8)
	global_load_dwordx4 v[82:85], v[196:197], off
	global_load_dwordx4 v[74:77], v[196:197], off offset:512
	global_load_dwordx4 v[78:81], v[196:197], off offset:1024
	v_lshl_add_u64 v[196:197], v[196:197], 0, s[42:43]
	s_waitcnt lgkmcnt(3)
	v_mfma_scale_f32_16x16x128_f8f6f4 v[134:137], v[122:127], v[2:7], 0, v178, v112 op_sel_hi:[0,0,0] cbsz:2 blgp:2
	v_mfma_scale_f32_16x16x128_f8f6f4 v[138:141], v[122:127], v[14:19], 0, v178, v112 op_sel_hi:[0,0,0] cbsz:2 blgp:2
	v_mfma_scale_f32_16x16x128_f8f6f4 v[142:145], v[122:127], v[26:31], 0, v178, v112 op_sel_hi:[0,0,0] cbsz:2 blgp:2
	v_mfma_scale_f32_16x16x128_f8f6f4 v[134:137], v[122:127], v[38:43], v[134:137], v179, v112 op_sel_hi:[0,0,0] cbsz:2 blgp:2
	v_mfma_scale_f32_16x16x128_f8f6f4 v[138:141], v[122:127], v[50:55], v[138:141], v179, v112 op_sel_hi:[0,0,0] cbsz:2 blgp:2
	v_mfma_scale_f32_16x16x128_f8f6f4 v[142:145], v[122:127], v[62:67], v[142:145], v179, v112 op_sel_hi:[0,0,0] cbsz:2 blgp:2
	s_waitcnt lgkmcnt(0)
	v_mfma_scale_f32_16x16x128_f8f6f4 v[134:137], v[128:133], v[8:13], v[134:137], v178, v112 op_sel_hi:[0,0,0] cbsz:2 blgp:2
	v_mfma_scale_f32_16x16x128_f8f6f4 v[134:137], v[128:133], v[44:49], v[134:137], v179, v112 op_sel_hi:[0,0,0] cbsz:2 blgp:2
	v_mfma_scale_f32_16x16x128_f8f6f4 v[138:141], v[128:133], v[20:25], v[138:141], v178, v112 op_sel_hi:[0,0,0] cbsz:2 blgp:2
	v_mfma_scale_f32_16x16x128_f8f6f4 v[138:141], v[128:133], v[56:61], v[138:141], v179, v112 op_sel_hi:[0,0,0] cbsz:2 blgp:2
	v_mfma_scale_f32_16x16x128_f8f6f4 v[142:145], v[128:133], v[32:37], v[142:145], v178, v112 op_sel_hi:[0,0,0] cbsz:2 blgp:2
	v_mfma_scale_f32_16x16x128_f8f6f4 v[142:145], v[128:133], v[68:73], v[142:145], v179, v112 op_sel_hi:[0,0,0] cbsz:2 blgp:2
	v_fma_mix_f32 v158, v134, v100, v146 op_sel_hi:[0,0,1]
	v_exp_f32_e32 v158, v158
	v_fma_mix_f32 v159, v138, v101, v150 op_sel_hi:[0,0,1]
	v_exp_f32_e32 v159, v159
	v_add_f32_e32 v158, 1.0, v158
	v_rcp_f32_e32 v158, v158
	v_add_f32_e32 v159, 1.0, v159
	v_rcp_f32_e32 v159, v159
	v_fma_f32 v160, v142, v102, v103
	v_fma_mix_f32 v161, v158, v160, v154 op_sel_hi:[0,0,1]
	v_exp_f32_e32 v161, v161
	s_add_u32 s48, s48, s40
	v_add_f32_e32 v161, 1.0, v161
	v_rcp_f32_e32 v161, v161
	s_addc_u32 s49, s49, s41
	v_fma_f32 v162, v161, -2.0, 1.0
	v_sub_f32_e32 v163, v176, v162
	v_fma_f32 v176, v159, v163, v162
	v_fma_f32 v164, |v176|, s17, v113
	v_fma_f32 v165, |v176|, s18, v114
	v_fma_f32 v166, |v176|, s19, v115
	v_lshrrev_b32_e32 v167, 26, v176
	v_min3_u32 v164, v164, v165, v166
	v_bfi_b32 v168, 31, v164, v167
	v_lshrrev_b32_e32 v169, v181, v168
	global_store_short_d16_hi v185, v176, s[48:49]
	v_mul_u32_u24_dpp v170, v168, v180 quad_perm:[1,2,3,3] row_mask:0xf bank_mask:0xf bound_ctrl:1
	v_or_b32_e32 v171, v169, v170
	ds_write_b8 v184, v171 offset:416
	s_waitcnt lgkmcnt(0)
	s_barrier
	ds_read_b64 v[122:123], v105 offset:416
	ds_read_b64 v[124:125], v105 offset:424
	ds_read_b64 v[126:127], v105 offset:432
	s_barrier
	ds_read_b64 v[128:129], v105 offset:512
	ds_read_b64 v[130:131], v105 offset:520
	ds_read_b64 v[132:133], v105 offset:528
	s_waitcnt lgkmcnt(3)
	v_mfma_scale_f32_16x16x128_f8f6f4 v[134:137], v[122:127], v[2:7], 0, v178, v112 op_sel_hi:[0,0,0] cbsz:2 blgp:2
	v_mfma_scale_f32_16x16x128_f8f6f4 v[138:141], v[122:127], v[14:19], 0, v178, v112 op_sel_hi:[0,0,0] cbsz:2 blgp:2
	v_mfma_scale_f32_16x16x128_f8f6f4 v[142:145], v[122:127], v[26:31], 0, v178, v112 op_sel_hi:[0,0,0] cbsz:2 blgp:2
	v_mfma_scale_f32_16x16x128_f8f6f4 v[134:137], v[122:127], v[38:43], v[134:137], v179, v112 op_sel_hi:[0,0,0] cbsz:2 blgp:2
	v_mfma_scale_f32_16x16x128_f8f6f4 v[138:141], v[122:127], v[50:55], v[138:141], v179, v112 op_sel_hi:[0,0,0] cbsz:2 blgp:2
	v_mfma_scale_f32_16x16x128_f8f6f4 v[142:145], v[122:127], v[62:67], v[142:145], v179, v112 op_sel_hi:[0,0,0] cbsz:2 blgp:2
	s_waitcnt lgkmcnt(0)
	v_mfma_scale_f32_16x16x128_f8f6f4 v[134:137], v[128:133], v[8:13], v[134:137], v178, v112 op_sel_hi:[0,0,0] cbsz:2 blgp:2
	v_mfma_scale_f32_16x16x128_f8f6f4 v[134:137], v[128:133], v[44:49], v[134:137], v179, v112 op_sel_hi:[0,0,0] cbsz:2 blgp:2
	v_mfma_scale_f32_16x16x128_f8f6f4 v[138:141], v[128:133], v[20:25], v[138:141], v178, v112 op_sel_hi:[0,0,0] cbsz:2 blgp:2
	v_mfma_scale_f32_16x16x128_f8f6f4 v[138:141], v[128:133], v[56:61], v[138:141], v179, v112 op_sel_hi:[0,0,0] cbsz:2 blgp:2
	v_mfma_scale_f32_16x16x128_f8f6f4 v[142:145], v[128:133], v[32:37], v[142:145], v178, v112 op_sel_hi:[0,0,0] cbsz:2 blgp:2
	v_mfma_scale_f32_16x16x128_f8f6f4 v[142:145], v[128:133], v[68:73], v[142:145], v179, v112 op_sel_hi:[0,0,0] cbsz:2 blgp:2
	v_fma_mix_f32 v158, v134, v100, v146 op_sel:[0,0,1] op_sel_hi:[0,0,1]
	v_exp_f32_e32 v158, v158
	v_fma_mix_f32 v159, v138, v101, v150 op_sel:[0,0,1] op_sel_hi:[0,0,1]
	v_exp_f32_e32 v159, v159
	v_add_f32_e32 v158, 1.0, v158
	v_rcp_f32_e32 v158, v158
	v_add_f32_e32 v159, 1.0, v159
	v_rcp_f32_e32 v159, v159
	v_fma_f32 v160, v142, v102, v103
	v_fma_mix_f32 v161, v158, v160, v154 op_sel:[0,0,1] op_sel_hi:[0,0,1]
	v_exp_f32_e32 v161, v161
	s_add_u32 s48, s48, s40
	v_add_f32_e32 v161, 1.0, v161
	v_rcp_f32_e32 v161, v161
	s_addc_u32 s49, s49, s41
	v_fma_f32 v162, v161, -2.0, 1.0
	v_sub_f32_e32 v163, v176, v162
	v_fma_f32 v176, v159, v163, v162
	v_fma_f32 v164, |v176|, s17, v113
	v_fma_f32 v165, |v176|, s18, v114
	v_fma_f32 v166, |v176|, s19, v115
	v_lshrrev_b32_e32 v167, 26, v176
	v_min3_u32 v164, v164, v165, v166
	v_bfi_b32 v168, 31, v164, v167
	v_lshrrev_b32_e32 v169, v181, v168
	global_store_short_d16_hi v185, v176, s[48:49]
	v_mul_u32_u24_dpp v170, v168, v180 quad_perm:[1,2,3,3] row_mask:0xf bank_mask:0xf bound_ctrl:1
	v_or_b32_e32 v171, v169, v170
	ds_write_b8 v184, v171
	s_waitcnt lgkmcnt(0)
	s_barrier
	ds_read_b64 v[122:123], v105 offset:0
	ds_read_b64 v[124:125], v105 offset:8
	ds_read_b64 v[126:127], v105 offset:16
	s_barrier
	ds_read_b64 v[128:129], v105 offset:96
	ds_read_b64 v[130:131], v105 offset:104
	ds_read_b64 v[132:133], v105 offset:112
	s_waitcnt lgkmcnt(3)
	v_mfma_scale_f32_16x16x128_f8f6f4 v[134:137], v[122:127], v[2:7], 0, v178, v112 op_sel_hi:[0,0,0] cbsz:2 blgp:2
	v_mfma_scale_f32_16x16x128_f8f6f4 v[138:141], v[122:127], v[14:19], 0, v178, v112 op_sel_hi:[0,0,0] cbsz:2 blgp:2
	v_mfma_scale_f32_16x16x128_f8f6f4 v[142:145], v[122:127], v[26:31], 0, v178, v112 op_sel_hi:[0,0,0] cbsz:2 blgp:2
	v_mfma_scale_f32_16x16x128_f8f6f4 v[134:137], v[122:127], v[38:43], v[134:137], v179, v112 op_sel_hi:[0,0,0] cbsz:2 blgp:2
	v_mfma_scale_f32_16x16x128_f8f6f4 v[138:141], v[122:127], v[50:55], v[138:141], v179, v112 op_sel_hi:[0,0,0] cbsz:2 blgp:2
	v_mfma_scale_f32_16x16x128_f8f6f4 v[142:145], v[122:127], v[62:67], v[142:145], v179, v112 op_sel_hi:[0,0,0] cbsz:2 blgp:2
	s_waitcnt lgkmcnt(0)
	v_mfma_scale_f32_16x16x128_f8f6f4 v[134:137], v[128:133], v[8:13], v[134:137], v178, v112 op_sel_hi:[0,0,0] cbsz:2 blgp:2
	v_mfma_scale_f32_16x16x128_f8f6f4 v[134:137], v[128:133], v[44:49], v[134:137], v179, v112 op_sel_hi:[0,0,0] cbsz:2 blgp:2
	v_mfma_scale_f32_16x16x128_f8f6f4 v[138:141], v[128:133], v[20:25], v[138:141], v178, v112 op_sel_hi:[0,0,0] cbsz:2 blgp:2
	v_mfma_scale_f32_16x16x128_f8f6f4 v[138:141], v[128:133], v[56:61], v[138:141], v179, v112 op_sel_hi:[0,0,0] cbsz:2 blgp:2
	v_mfma_scale_f32_16x16x128_f8f6f4 v[142:145], v[128:133], v[32:37], v[142:145], v178, v112 op_sel_hi:[0,0,0] cbsz:2 blgp:2
	v_mfma_scale_f32_16x16x128_f8f6f4 v[142:145], v[128:133], v[68:73], v[142:145], v179, v112 op_sel_hi:[0,0,0] cbsz:2 blgp:2
	v_fma_mix_f32 v158, v134, v100, v147 op_sel_hi:[0,0,1]
	v_exp_f32_e32 v158, v158
	v_fma_mix_f32 v159, v138, v101, v151 op_sel_hi:[0,0,1]
	v_exp_f32_e32 v159, v159
	v_add_f32_e32 v158, 1.0, v158
	v_rcp_f32_e32 v158, v158
	v_add_f32_e32 v159, 1.0, v159
	v_rcp_f32_e32 v159, v159
	v_fma_f32 v160, v142, v102, v103
	v_fma_mix_f32 v161, v158, v160, v155 op_sel_hi:[0,0,1]
	v_exp_f32_e32 v161, v161
	s_add_u32 s48, s48, s40
	v_add_f32_e32 v161, 1.0, v161
	v_rcp_f32_e32 v161, v161
	s_addc_u32 s49, s49, s41
	v_fma_f32 v162, v161, -2.0, 1.0
	v_sub_f32_e32 v163, v176, v162
	v_fma_f32 v176, v159, v163, v162
	v_fma_f32 v164, |v176|, s17, v113
	v_fma_f32 v165, |v176|, s18, v114
	v_fma_f32 v166, |v176|, s19, v115
	v_lshrrev_b32_e32 v167, 26, v176
	v_min3_u32 v164, v164, v165, v166
	v_bfi_b32 v168, 31, v164, v167
	v_lshrrev_b32_e32 v169, v181, v168
	global_store_short_d16_hi v185, v176, s[48:49]
	v_mul_u32_u24_dpp v170, v168, v180 quad_perm:[1,2,3,3] row_mask:0xf bank_mask:0xf bound_ctrl:1
	v_or_b32_e32 v171, v169, v170
	ds_write_b8 v184, v171 offset:416
	s_waitcnt lgkmcnt(0)
	s_barrier
	ds_read_b64 v[122:123], v105 offset:416
	ds_read_b64 v[124:125], v105 offset:424
	ds_read_b64 v[126:127], v105 offset:432
	s_barrier
	ds_read_b64 v[128:129], v105 offset:512
	ds_read_b64 v[130:131], v105 offset:520
	ds_read_b64 v[132:133], v105 offset:528
	s_waitcnt lgkmcnt(3)
	v_mfma_scale_f32_16x16x128_f8f6f4 v[134:137], v[122:127], v[2:7], 0, v178, v112 op_sel_hi:[0,0,0] cbsz:2 blgp:2
	v_mfma_scale_f32_16x16x128_f8f6f4 v[138:141], v[122:127], v[14:19], 0, v178, v112 op_sel_hi:[0,0,0] cbsz:2 blgp:2
	v_mfma_scale_f32_16x16x128_f8f6f4 v[142:145], v[122:127], v[26:31], 0, v178, v112 op_sel_hi:[0,0,0] cbsz:2 blgp:2
	v_mfma_scale_f32_16x16x128_f8f6f4 v[134:137], v[122:127], v[38:43], v[134:137], v179, v112 op_sel_hi:[0,0,0] cbsz:2 blgp:2
	v_mfma_scale_f32_16x16x128_f8f6f4 v[138:141], v[122:127], v[50:55], v[138:141], v179, v112 op_sel_hi:[0,0,0] cbsz:2 blgp:2
	v_mfma_scale_f32_16x16x128_f8f6f4 v[142:145], v[122:127], v[62:67], v[142:145], v179, v112 op_sel_hi:[0,0,0] cbsz:2 blgp:2
	s_waitcnt lgkmcnt(0)
	v_mfma_scale_f32_16x16x128_f8f6f4 v[134:137], v[128:133], v[8:13], v[134:137], v178, v112 op_sel_hi:[0,0,0] cbsz:2 blgp:2
	v_mfma_scale_f32_16x16x128_f8f6f4 v[134:137], v[128:133], v[44:49], v[134:137], v179, v112 op_sel_hi:[0,0,0] cbsz:2 blgp:2
	v_mfma_scale_f32_16x16x128_f8f6f4 v[138:141], v[128:133], v[20:25], v[138:141], v178, v112 op_sel_hi:[0,0,0] cbsz:2 blgp:2
	v_mfma_scale_f32_16x16x128_f8f6f4 v[138:141], v[128:133], v[56:61], v[138:141], v179, v112 op_sel_hi:[0,0,0] cbsz:2 blgp:2
	v_mfma_scale_f32_16x16x128_f8f6f4 v[142:145], v[128:133], v[32:37], v[142:145], v178, v112 op_sel_hi:[0,0,0] cbsz:2 blgp:2
	v_mfma_scale_f32_16x16x128_f8f6f4 v[142:145], v[128:133], v[68:73], v[142:145], v179, v112 op_sel_hi:[0,0,0] cbsz:2 blgp:2
	v_fma_mix_f32 v158, v134, v100, v147 op_sel:[0,0,1] op_sel_hi:[0,0,1]
	v_exp_f32_e32 v158, v158
	v_fma_mix_f32 v159, v138, v101, v151 op_sel:[0,0,1] op_sel_hi:[0,0,1]
	v_exp_f32_e32 v159, v159
	v_add_f32_e32 v158, 1.0, v158
	v_rcp_f32_e32 v158, v158
	v_add_f32_e32 v159, 1.0, v159
	v_rcp_f32_e32 v159, v159
	v_fma_f32 v160, v142, v102, v103
	v_fma_mix_f32 v161, v158, v160, v155 op_sel:[0,0,1] op_sel_hi:[0,0,1]
	v_exp_f32_e32 v161, v161
	s_add_u32 s48, s48, s40
	v_add_f32_e32 v161, 1.0, v161
	v_rcp_f32_e32 v161, v161
	s_addc_u32 s49, s49, s41
	v_fma_f32 v162, v161, -2.0, 1.0
	v_sub_f32_e32 v163, v176, v162
	v_fma_f32 v176, v159, v163, v162
	v_fma_f32 v164, |v176|, s17, v113
	v_fma_f32 v165, |v176|, s18, v114
	v_fma_f32 v166, |v176|, s19, v115
	v_lshrrev_b32_e32 v167, 26, v176
	v_min3_u32 v164, v164, v165, v166
	v_bfi_b32 v168, 31, v164, v167
	v_lshrrev_b32_e32 v169, v181, v168
	global_store_short_d16_hi v185, v176, s[48:49]
	v_mul_u32_u24_dpp v170, v168, v180 quad_perm:[1,2,3,3] row_mask:0xf bank_mask:0xf bound_ctrl:1
	v_or_b32_e32 v171, v169, v170
	ds_write_b8 v184, v171
	s_waitcnt lgkmcnt(0)
	s_barrier
	ds_read_b64 v[122:123], v105 offset:0
	ds_read_b64 v[124:125], v105 offset:8
	ds_read_b64 v[126:127], v105 offset:16
	s_barrier
	ds_read_b64 v[128:129], v105 offset:96
	ds_read_b64 v[130:131], v105 offset:104
	ds_read_b64 v[132:133], v105 offset:112
	s_waitcnt lgkmcnt(3)
	v_mfma_scale_f32_16x16x128_f8f6f4 v[134:137], v[122:127], v[2:7], 0, v178, v112 op_sel_hi:[0,0,0] cbsz:2 blgp:2
	v_mfma_scale_f32_16x16x128_f8f6f4 v[138:141], v[122:127], v[14:19], 0, v178, v112 op_sel_hi:[0,0,0] cbsz:2 blgp:2
	v_mfma_scale_f32_16x16x128_f8f6f4 v[142:145], v[122:127], v[26:31], 0, v178, v112 op_sel_hi:[0,0,0] cbsz:2 blgp:2
	v_mfma_scale_f32_16x16x128_f8f6f4 v[134:137], v[122:127], v[38:43], v[134:137], v179, v112 op_sel_hi:[0,0,0] cbsz:2 blgp:2
	v_mfma_scale_f32_16x16x128_f8f6f4 v[138:141], v[122:127], v[50:55], v[138:141], v179, v112 op_sel_hi:[0,0,0] cbsz:2 blgp:2
	v_mfma_scale_f32_16x16x128_f8f6f4 v[142:145], v[122:127], v[62:67], v[142:145], v179, v112 op_sel_hi:[0,0,0] cbsz:2 blgp:2
	s_waitcnt lgkmcnt(0)
	v_mfma_scale_f32_16x16x128_f8f6f4 v[134:137], v[128:133], v[8:13], v[134:137], v178, v112 op_sel_hi:[0,0,0] cbsz:2 blgp:2
	v_mfma_scale_f32_16x16x128_f8f6f4 v[134:137], v[128:133], v[44:49], v[134:137], v179, v112 op_sel_hi:[0,0,0] cbsz:2 blgp:2
	v_mfma_scale_f32_16x16x128_f8f6f4 v[138:141], v[128:133], v[20:25], v[138:141], v178, v112 op_sel_hi:[0,0,0] cbsz:2 blgp:2
	v_mfma_scale_f32_16x16x128_f8f6f4 v[138:141], v[128:133], v[56:61], v[138:141], v179, v112 op_sel_hi:[0,0,0] cbsz:2 blgp:2
	v_mfma_scale_f32_16x16x128_f8f6f4 v[142:145], v[128:133], v[32:37], v[142:145], v178, v112 op_sel_hi:[0,0,0] cbsz:2 blgp:2
	v_mfma_scale_f32_16x16x128_f8f6f4 v[142:145], v[128:133], v[68:73], v[142:145], v179, v112 op_sel_hi:[0,0,0] cbsz:2 blgp:2
	v_fma_mix_f32 v158, v134, v100, v148 op_sel_hi:[0,0,1]
	v_exp_f32_e32 v158, v158
	v_fma_mix_f32 v159, v138, v101, v152 op_sel_hi:[0,0,1]
	v_exp_f32_e32 v159, v159
	v_add_f32_e32 v158, 1.0, v158
	v_rcp_f32_e32 v158, v158
	v_add_f32_e32 v159, 1.0, v159
	v_rcp_f32_e32 v159, v159
	v_fma_f32 v160, v142, v102, v103
	v_fma_mix_f32 v161, v158, v160, v156 op_sel_hi:[0,0,1]
	v_exp_f32_e32 v161, v161
	s_add_u32 s48, s48, s40
	v_add_f32_e32 v161, 1.0, v161
	v_rcp_f32_e32 v161, v161
	s_addc_u32 s49, s49, s41
	v_fma_f32 v162, v161, -2.0, 1.0
	v_sub_f32_e32 v163, v176, v162
	v_fma_f32 v176, v159, v163, v162
	v_fma_f32 v164, |v176|, s17, v113
	v_fma_f32 v165, |v176|, s18, v114
	v_fma_f32 v166, |v176|, s19, v115
	v_lshrrev_b32_e32 v167, 26, v176
	v_min3_u32 v164, v164, v165, v166
	v_bfi_b32 v168, 31, v164, v167
	v_lshrrev_b32_e32 v169, v181, v168
	global_store_short_d16_hi v185, v176, s[48:49]
	v_mul_u32_u24_dpp v170, v168, v180 quad_perm:[1,2,3,3] row_mask:0xf bank_mask:0xf bound_ctrl:1
	v_or_b32_e32 v171, v169, v170
	ds_write_b8 v184, v171 offset:416
	s_waitcnt lgkmcnt(0)
	s_barrier
	ds_read_b64 v[122:123], v105 offset:416
	ds_read_b64 v[124:125], v105 offset:424
	ds_read_b64 v[126:127], v105 offset:432
	s_barrier
	ds_read_b64 v[128:129], v105 offset:512
	ds_read_b64 v[130:131], v105 offset:520
	ds_read_b64 v[132:133], v105 offset:528
	s_waitcnt lgkmcnt(3)
	v_mfma_scale_f32_16x16x128_f8f6f4 v[134:137], v[122:127], v[2:7], 0, v178, v112 op_sel_hi:[0,0,0] cbsz:2 blgp:2
	v_mfma_scale_f32_16x16x128_f8f6f4 v[138:141], v[122:127], v[14:19], 0, v178, v112 op_sel_hi:[0,0,0] cbsz:2 blgp:2
	v_mfma_scale_f32_16x16x128_f8f6f4 v[142:145], v[122:127], v[26:31], 0, v178, v112 op_sel_hi:[0,0,0] cbsz:2 blgp:2
	v_mfma_scale_f32_16x16x128_f8f6f4 v[134:137], v[122:127], v[38:43], v[134:137], v179, v112 op_sel_hi:[0,0,0] cbsz:2 blgp:2
	v_mfma_scale_f32_16x16x128_f8f6f4 v[138:141], v[122:127], v[50:55], v[138:141], v179, v112 op_sel_hi:[0,0,0] cbsz:2 blgp:2
	v_mfma_scale_f32_16x16x128_f8f6f4 v[142:145], v[122:127], v[62:67], v[142:145], v179, v112 op_sel_hi:[0,0,0] cbsz:2 blgp:2
	s_waitcnt lgkmcnt(0)
	v_mfma_scale_f32_16x16x128_f8f6f4 v[134:137], v[128:133], v[8:13], v[134:137], v178, v112 op_sel_hi:[0,0,0] cbsz:2 blgp:2
	v_mfma_scale_f32_16x16x128_f8f6f4 v[134:137], v[128:133], v[44:49], v[134:137], v179, v112 op_sel_hi:[0,0,0] cbsz:2 blgp:2
	v_mfma_scale_f32_16x16x128_f8f6f4 v[138:141], v[128:133], v[20:25], v[138:141], v178, v112 op_sel_hi:[0,0,0] cbsz:2 blgp:2
	v_mfma_scale_f32_16x16x128_f8f6f4 v[138:141], v[128:133], v[56:61], v[138:141], v179, v112 op_sel_hi:[0,0,0] cbsz:2 blgp:2
	v_mfma_scale_f32_16x16x128_f8f6f4 v[142:145], v[128:133], v[32:37], v[142:145], v178, v112 op_sel_hi:[0,0,0] cbsz:2 blgp:2
	v_mfma_scale_f32_16x16x128_f8f6f4 v[142:145], v[128:133], v[68:73], v[142:145], v179, v112 op_sel_hi:[0,0,0] cbsz:2 blgp:2
	v_fma_mix_f32 v158, v134, v100, v148 op_sel:[0,0,1] op_sel_hi:[0,0,1]
	v_exp_f32_e32 v158, v158
	v_fma_mix_f32 v159, v138, v101, v152 op_sel:[0,0,1] op_sel_hi:[0,0,1]
	v_exp_f32_e32 v159, v159
	v_add_f32_e32 v158, 1.0, v158
	v_rcp_f32_e32 v158, v158
	v_add_f32_e32 v159, 1.0, v159
	v_rcp_f32_e32 v159, v159
	v_fma_f32 v160, v142, v102, v103
	v_fma_mix_f32 v161, v158, v160, v156 op_sel:[0,0,1] op_sel_hi:[0,0,1]
	v_exp_f32_e32 v161, v161
	s_add_u32 s48, s48, s40
	v_add_f32_e32 v161, 1.0, v161
	v_rcp_f32_e32 v161, v161
	s_addc_u32 s49, s49, s41
	v_fma_f32 v162, v161, -2.0, 1.0
	v_sub_f32_e32 v163, v176, v162
	v_fma_f32 v176, v159, v163, v162
	v_fma_f32 v164, |v176|, s17, v113
	v_fma_f32 v165, |v176|, s18, v114
	v_fma_f32 v166, |v176|, s19, v115
	v_lshrrev_b32_e32 v167, 26, v176
	v_min3_u32 v164, v164, v165, v166
	v_bfi_b32 v168, 31, v164, v167
	v_lshrrev_b32_e32 v169, v181, v168
	global_store_short_d16_hi v185, v176, s[48:49]
	v_mul_u32_u24_dpp v170, v168, v180 quad_perm:[1,2,3,3] row_mask:0xf bank_mask:0xf bound_ctrl:1
	v_or_b32_e32 v171, v169, v170
	ds_write_b8 v184, v171
	s_waitcnt lgkmcnt(0)
	s_barrier
	ds_read_b64 v[122:123], v105 offset:0
	ds_read_b64 v[124:125], v105 offset:8
	ds_read_b64 v[126:127], v105 offset:16
	s_barrier
	ds_read_b64 v[128:129], v105 offset:96
	ds_read_b64 v[130:131], v105 offset:104
	ds_read_b64 v[132:133], v105 offset:112
	s_waitcnt lgkmcnt(3)
	v_mfma_scale_f32_16x16x128_f8f6f4 v[134:137], v[122:127], v[2:7], 0, v178, v112 op_sel_hi:[0,0,0] cbsz:2 blgp:2
	v_mfma_scale_f32_16x16x128_f8f6f4 v[138:141], v[122:127], v[14:19], 0, v178, v112 op_sel_hi:[0,0,0] cbsz:2 blgp:2
	v_mfma_scale_f32_16x16x128_f8f6f4 v[142:145], v[122:127], v[26:31], 0, v178, v112 op_sel_hi:[0,0,0] cbsz:2 blgp:2
	v_mfma_scale_f32_16x16x128_f8f6f4 v[134:137], v[122:127], v[38:43], v[134:137], v179, v112 op_sel_hi:[0,0,0] cbsz:2 blgp:2
	v_mfma_scale_f32_16x16x128_f8f6f4 v[138:141], v[122:127], v[50:55], v[138:141], v179, v112 op_sel_hi:[0,0,0] cbsz:2 blgp:2
	v_mfma_scale_f32_16x16x128_f8f6f4 v[142:145], v[122:127], v[62:67], v[142:145], v179, v112 op_sel_hi:[0,0,0] cbsz:2 blgp:2
	s_waitcnt lgkmcnt(0)
	v_mfma_scale_f32_16x16x128_f8f6f4 v[134:137], v[128:133], v[8:13], v[134:137], v178, v112 op_sel_hi:[0,0,0] cbsz:2 blgp:2
	v_mfma_scale_f32_16x16x128_f8f6f4 v[134:137], v[128:133], v[44:49], v[134:137], v179, v112 op_sel_hi:[0,0,0] cbsz:2 blgp:2
	v_mfma_scale_f32_16x16x128_f8f6f4 v[138:141], v[128:133], v[20:25], v[138:141], v178, v112 op_sel_hi:[0,0,0] cbsz:2 blgp:2
	v_mfma_scale_f32_16x16x128_f8f6f4 v[138:141], v[128:133], v[56:61], v[138:141], v179, v112 op_sel_hi:[0,0,0] cbsz:2 blgp:2
	v_mfma_scale_f32_16x16x128_f8f6f4 v[142:145], v[128:133], v[32:37], v[142:145], v178, v112 op_sel_hi:[0,0,0] cbsz:2 blgp:2
	v_mfma_scale_f32_16x16x128_f8f6f4 v[142:145], v[128:133], v[68:73], v[142:145], v179, v112 op_sel_hi:[0,0,0] cbsz:2 blgp:2
	v_fma_mix_f32 v158, v134, v100, v149 op_sel_hi:[0,0,1]
	v_exp_f32_e32 v158, v158
	v_fma_mix_f32 v159, v138, v101, v153 op_sel_hi:[0,0,1]
	v_exp_f32_e32 v159, v159
	v_add_f32_e32 v158, 1.0, v158
	v_rcp_f32_e32 v158, v158
	v_add_f32_e32 v159, 1.0, v159
	v_rcp_f32_e32 v159, v159
	v_fma_f32 v160, v142, v102, v103
	v_fma_mix_f32 v161, v158, v160, v157 op_sel_hi:[0,0,1]
	v_exp_f32_e32 v161, v161
	s_add_u32 s48, s48, s40
	v_add_f32_e32 v161, 1.0, v161
	v_rcp_f32_e32 v161, v161
	s_addc_u32 s49, s49, s41
	v_fma_f32 v162, v161, -2.0, 1.0
	v_sub_f32_e32 v163, v176, v162
	v_fma_f32 v176, v159, v163, v162
	v_fma_f32 v164, |v176|, s17, v113
	v_fma_f32 v165, |v176|, s18, v114
	v_fma_f32 v166, |v176|, s19, v115
	v_lshrrev_b32_e32 v167, 26, v176
	v_min3_u32 v164, v164, v165, v166
	v_bfi_b32 v168, 31, v164, v167
	v_lshrrev_b32_e32 v169, v181, v168
	global_store_short_d16_hi v185, v176, s[48:49]
	v_mul_u32_u24_dpp v170, v168, v180 quad_perm:[1,2,3,3] row_mask:0xf bank_mask:0xf bound_ctrl:1
	v_or_b32_e32 v171, v169, v170
	ds_write_b8 v184, v171 offset:416
	s_waitcnt lgkmcnt(0)
	s_barrier
	ds_read_b64 v[122:123], v105 offset:416
	ds_read_b64 v[124:125], v105 offset:424
	ds_read_b64 v[126:127], v105 offset:432
	s_barrier
	ds_read_b64 v[128:129], v105 offset:512
	ds_read_b64 v[130:131], v105 offset:520
	ds_read_b64 v[132:133], v105 offset:528
	s_add_i32 s44, s44, 16
	s_waitcnt lgkmcnt(3)
	v_mfma_scale_f32_16x16x128_f8f6f4 v[134:137], v[122:127], v[2:7], 0, v178, v112 op_sel_hi:[0,0,0] cbsz:2 blgp:2
	v_mfma_scale_f32_16x16x128_f8f6f4 v[138:141], v[122:127], v[14:19], 0, v178, v112 op_sel_hi:[0,0,0] cbsz:2 blgp:2
	v_mfma_scale_f32_16x16x128_f8f6f4 v[142:145], v[122:127], v[26:31], 0, v178, v112 op_sel_hi:[0,0,0] cbsz:2 blgp:2
	v_mfma_scale_f32_16x16x128_f8f6f4 v[134:137], v[122:127], v[38:43], v[134:137], v179, v112 op_sel_hi:[0,0,0] cbsz:2 blgp:2
	v_mfma_scale_f32_16x16x128_f8f6f4 v[138:141], v[122:127], v[50:55], v[138:141], v179, v112 op_sel_hi:[0,0,0] cbsz:2 blgp:2
	v_mfma_scale_f32_16x16x128_f8f6f4 v[142:145], v[122:127], v[62:67], v[142:145], v179, v112 op_sel_hi:[0,0,0] cbsz:2 blgp:2
	s_waitcnt lgkmcnt(0)
	v_mfma_scale_f32_16x16x128_f8f6f4 v[134:137], v[128:133], v[8:13], v[134:137], v178, v112 op_sel_hi:[0,0,0] cbsz:2 blgp:2
	v_mfma_scale_f32_16x16x128_f8f6f4 v[134:137], v[128:133], v[44:49], v[134:137], v179, v112 op_sel_hi:[0,0,0] cbsz:2 blgp:2
	v_mfma_scale_f32_16x16x128_f8f6f4 v[138:141], v[128:133], v[20:25], v[138:141], v178, v112 op_sel_hi:[0,0,0] cbsz:2 blgp:2
	v_mfma_scale_f32_16x16x128_f8f6f4 v[138:141], v[128:133], v[56:61], v[138:141], v179, v112 op_sel_hi:[0,0,0] cbsz:2 blgp:2
	v_mfma_scale_f32_16x16x128_f8f6f4 v[142:145], v[128:133], v[32:37], v[142:145], v178, v112 op_sel_hi:[0,0,0] cbsz:2 blgp:2
	v_mfma_scale_f32_16x16x128_f8f6f4 v[142:145], v[128:133], v[68:73], v[142:145], v179, v112 op_sel_hi:[0,0,0] cbsz:2 blgp:2
	v_fma_mix_f32 v158, v134, v100, v149 op_sel:[0,0,1] op_sel_hi:[0,0,1]
	v_exp_f32_e32 v158, v158
	v_fma_mix_f32 v159, v138, v101, v153 op_sel:[0,0,1] op_sel_hi:[0,0,1]
	v_exp_f32_e32 v159, v159
	v_add_f32_e32 v158, 1.0, v158
	v_rcp_f32_e32 v158, v158
	v_add_f32_e32 v159, 1.0, v159
	v_rcp_f32_e32 v159, v159
	v_fma_f32 v160, v142, v102, v103
	v_fma_mix_f32 v161, v158, v160, v157 op_sel:[0,0,1] op_sel_hi:[0,0,1]
	v_exp_f32_e32 v161, v161
	s_add_u32 s48, s48, s40
	v_add_f32_e32 v161, 1.0, v161
	v_rcp_f32_e32 v161, v161
	s_addc_u32 s49, s49, s41
	v_fma_f32 v162, v161, -2.0, 1.0
	v_sub_f32_e32 v163, v176, v162
	v_fma_f32 v176, v159, v163, v162
	v_fma_f32 v164, |v176|, s17, v113
	v_fma_f32 v165, |v176|, s18, v114
	v_fma_f32 v166, |v176|, s19, v115
	v_lshrrev_b32_e32 v167, 26, v176
	v_min3_u32 v164, v164, v165, v166
	v_bfi_b32 v168, 31, v164, v167
	v_lshrrev_b32_e32 v169, v181, v168
	global_store_short_d16_hi v185, v176, s[48:49]
	v_mul_u32_u24_dpp v170, v168, v180 quad_perm:[1,2,3,3] row_mask:0xf bank_mask:0xf bound_ctrl:1
	v_or_b32_e32 v171, v169, v170
	ds_write_b8 v184, v171
	s_waitcnt lgkmcnt(0)
	s_barrier
	ds_read_b64 v[122:123], v105 offset:0
	ds_read_b64 v[124:125], v105 offset:8
	ds_read_b64 v[126:127], v105 offset:16
	s_cmp_lt_i32 s44, s45
	s_barrier
	s_cbranch_scc1 .Lscan_loop_a_f2
	s_branch .Lscan_exit_f2
.Lscan_loop_b_f2:
	ds_read_b64 v[128:129], v105 offset:96
	ds_read_b64 v[130:131], v105 offset:104
	ds_read_b64 v[132:133], v105 offset:112
	s_waitcnt vmcnt(8)
	global_load_dwordx4 v[146:149], v[196:197], off
	global_load_dwordx4 v[150:153], v[196:197], off offset:512
	global_load_dwordx4 v[154:157], v[196:197], off offset:1024
	v_lshl_add_u64 v[196:197], v[196:197], 0, s[42:43]
	s_waitcnt lgkmcnt(3)
	v_mfma_scale_f32_16x16x128_f8f6f4 v[134:137], v[122:127], v[2:7], 0, v178, v112 op_sel_hi:[0,0,0] cbsz:2 blgp:2
	v_mfma_scale_f32_16x16x128_f8f6f4 v[138:141], v[122:127], v[14:19], 0, v178, v112 op_sel_hi:[0,0,0] cbsz:2 blgp:2
	v_mfma_scale_f32_16x16x128_f8f6f4 v[142:145], v[122:127], v[26:31], 0, v178, v112 op_sel_hi:[0,0,0] cbsz:2 blgp:2
	v_mfma_scale_f32_16x16x128_f8f6f4 v[134:137], v[122:127], v[38:43], v[134:137], v179, v112 op_sel_hi:[0,0,0] cbsz:2 blgp:2
	v_mfma_scale_f32_16x16x128_f8f6f4 v[138:141], v[122:127], v[50:55], v[138:141], v179, v112 op_sel_hi:[0,0,0] cbsz:2 blgp:2
	v_mfma_scale_f32_16x16x128_f8f6f4 v[142:145], v[122:127], v[62:67], v[142:145], v179, v112 op_sel_hi:[0,0,0] cbsz:2 blgp:2
	s_waitcnt lgkmcnt(0)
	v_mfma_scale_f32_16x16x128_f8f6f4 v[134:137], v[128:133], v[8:13], v[134:137], v178, v112 op_sel_hi:[0,0,0] cbsz:2 blgp:2
	v_mfma_scale_f32_16x16x128_f8f6f4 v[134:137], v[128:133], v[44:49], v[134:137], v179, v112 op_sel_hi:[0,0,0] cbsz:2 blgp:2
	v_mfma_scale_f32_16x16x128_f8f6f4 v[138:141], v[128:133], v[20:25], v[138:141], v178, v112 op_sel_hi:[0,0,0] cbsz:2 blgp:2
	v_mfma_scale_f32_16x16x128_f8f6f4 v[138:141], v[128:133], v[56:61], v[138:141], v179, v112 op_sel_hi:[0,0,0] cbsz:2 blgp:2
	v_mfma_scale_f32_16x16x128_f8f6f4 v[142:145], v[128:133], v[32:37], v[142:145], v178, v112 op_sel_hi:[0,0,0] cbsz:2 blgp:2
	v_mfma_scale_f32_16x16x128_f8f6f4 v[142:145], v[128:133], v[68:73], v[142:145], v179, v112 op_sel_hi:[0,0,0] cbsz:2 blgp:2
	v_fma_mix_f32 v158, v134, v100, v82 op_sel_hi:[0,0,1]
	v_exp_f32_e32 v158, v158
	v_fma_mix_f32 v159, v138, v101, v74 op_sel_hi:[0,0,1]
	v_exp_f32_e32 v159, v159
	v_add_f32_e32 v158, 1.0, v158
	v_rcp_f32_e32 v158, v158
	v_add_f32_e32 v159, 1.0, v159
	v_rcp_f32_e32 v159, v159
	v_fma_f32 v160, v142, v102, v103
	v_fma_mix_f32 v161, v158, v160, v78 op_sel_hi:[0,0,1]
	v_exp_f32_e32 v161, v161
	s_add_u32 s48, s48, s40
	v_add_f32_e32 v161, 1.0, v161
	v_rcp_f32_e32 v161, v161
	s_addc_u32 s49, s49, s41
	v_fma_f32 v162, v161, -2.0, 1.0
	v_sub_f32_e32 v163, v176, v162
	v_fma_f32 v176, v159, v163, v162
	v_fma_f32 v164, |v176|, s17, v113
	v_fma_f32 v165, |v176|, s18, v114
	v_fma_f32 v166, |v176|, s19, v115
	v_lshrrev_b32_e32 v167, 26, v176
	v_min3_u32 v164, v164, v165, v166
	v_bfi_b32 v168, 31, v164, v167
	v_lshrrev_b32_e32 v169, v181, v168
	global_store_short_d16_hi v185, v176, s[48:49]
	v_mul_u32_u24_dpp v170, v168, v180 quad_perm:[1,2,3,3] row_mask:0xf bank_mask:0xf bound_ctrl:1
	v_or_b32_e32 v171, v169, v170
	ds_write_b8 v184, v171 offset:416
	s_barrier
	ds_read_b64 v[122:123], v105 offset:416
	ds_read_b64 v[124:125], v105 offset:424
	ds_read_b64 v[126:127], v105 offset:432
	s_waitcnt lgkmcnt(3)
	s_barrier
	ds_read_b64 v[128:129], v105 offset:512
	ds_read_b64 v[130:131], v105 offset:520
	ds_read_b64 v[132:133], v105 offset:528
	s_waitcnt lgkmcnt(3)
	v_mfma_scale_f32_16x16x128_f8f6f4 v[134:137], v[122:127], v[2:7], 0, v178, v112 op_sel_hi:[0,0,0] cbsz:2 blgp:2
	v_mfma_scale_f32_16x16x128_f8f6f4 v[138:141], v[122:127], v[14:19], 0, v178, v112 op_sel_hi:[0,0,0] cbsz:2 blgp:2
	v_mfma_scale_f32_16x16x128_f8f6f4 v[142:145], v[122:127], v[26:31], 0, v178, v112 op_sel_hi:[0,0,0] cbsz:2 blgp:2
	v_mfma_scale_f32_16x16x128_f8f6f4 v[134:137], v[122:127], v[38:43], v[134:137], v179, v112 op_sel_hi:[0,0,0] cbsz:2 blgp:2
	v_mfma_scale_f32_16x16x128_f8f6f4 v[138:141], v[122:127], v[50:55], v[138:141], v179, v112 op_sel_hi:[0,0,0] cbsz:2 blgp:2
	v_mfma_scale_f32_16x16x128_f8f6f4 v[142:145], v[122:127], v[62:67], v[142:145], v179, v112 op_sel_hi:[0,0,0] cbsz:2 blgp:2
	s_waitcnt lgkmcnt(0)
	v_mfma_scale_f32_16x16x128_f8f6f4 v[134:137], v[128:133], v[8:13], v[134:137], v178, v112 op_sel_hi:[0,0,0] cbsz:2 blgp:2
	v_mfma_scale_f32_16x16x128_f8f6f4 v[134:137], v[128:133], v[44:49], v[134:137], v179, v112 op_sel_hi:[0,0,0] cbsz:2 blgp:2
	v_mfma_scale_f32_16x16x128_f8f6f4 v[138:141], v[128:133], v[20:25], v[138:141], v178, v112 op_sel_hi:[0,0,0] cbsz:2 blgp:2
	v_mfma_scale_f32_16x16x128_f8f6f4 v[138:141], v[128:133], v[56:61], v[138:141], v179, v112 op_sel_hi:[0,0,0] cbsz:2 blgp:2
	v_mfma_scale_f32_16x16x128_f8f6f4 v[142:145], v[128:133], v[32:37], v[142:145], v178, v112 op_sel_hi:[0,0,0] cbsz:2 blgp:2
	v_mfma_scale_f32_16x16x128_f8f6f4 v[142:145], v[128:133], v[68:73], v[142:145], v179, v112 op_sel_hi:[0,0,0] cbsz:2 blgp:2
	v_fma_mix_f32 v158, v134, v100, v82 op_sel:[0,0,1] op_sel_hi:[0,0,1]
	v_exp_f32_e32 v158, v158
	v_fma_mix_f32 v159, v138, v101, v74 op_sel:[0,0,1] op_sel_hi:[0,0,1]
	v_exp_f32_e32 v159, v159
	v_add_f32_e32 v158, 1.0, v158
	v_rcp_f32_e32 v158, v158
	v_add_f32_e32 v159, 1.0, v159
	v_rcp_f32_e32 v159, v159
	v_fma_f32 v160, v142, v102, v103
	v_fma_mix_f32 v161, v158, v160, v78 op_sel:[0,0,1] op_sel_hi:[0,0,1]
	v_exp_f32_e32 v161, v161
	s_add_u32 s48, s48, s40
	v_add_f32_e32 v161, 1.0, v161
	v_rcp_f32_e32 v161, v161
	s_addc_u32 s49, s49, s41
	v_fma_f32 v162, v161, -2.0, 1.0
	v_sub_f32_e32 v163, v176, v162
	v_fma_f32 v176, v159, v163, v162
	v_fma_f32 v164, |v176|, s17, v113
	v_fma_f32 v165, |v176|, s18, v114
	v_fma_f32 v166, |v176|, s19, v115
	v_lshrrev_b32_e32 v167, 26, v176
	v_min3_u32 v164, v164, v165, v166
	v_bfi_b32 v168, 31, v164, v167
	v_lshrrev_b32_e32 v169, v181, v168
	global_store_short_d16_hi v185, v176, s[48:49]
	v_mul_u32_u24_dpp v170, v168, v180 quad_perm:[1,2,3,3] row_mask:0xf bank_mask:0xf bound_ctrl:1
	v_or_b32_e32 v171, v169, v170
	ds_write_b8 v184, v171
	s_barrier
	ds_read_b64 v[122:123], v105 offset:0
	ds_read_b64 v[124:125], v105 offset:8
	ds_read_b64 v[126:127], v105 offset:16
	s_waitcnt lgkmcnt(3)
	s_barrier
	ds_read_b64 v[128:129], v105 offset:96
	ds_read_b64 v[130:131], v105 offset:104
	ds_read_b64 v[132:133], v105 offset:112
	s_waitcnt lgkmcnt(3)
	v_mfma_scale_f32_16x16x128_f8f6f4 v[134:137], v[122:127], v[2:7], 0, v178, v112 op_sel_hi:[0,0,0] cbsz:2 blgp:2
	v_mfma_scale_f32_16x16x128_f8f6f4 v[138:141], v[122:127], v[14:19], 0, v178, v112 op_sel_hi:[0,0,0] cbsz:2 blgp:2
	v_mfma_scale_f32_16x16x128_f8f6f4 v[142:145], v[122:127], v[26:31], 0, v178, v112 op_sel_hi:[0,0,0] cbsz:2 blgp:2
	v_mfma_scale_f32_16x16x128_f8f6f4 v[134:137], v[122:127], v[38:43], v[134:137], v179, v112 op_sel_hi:[0,0,0] cbsz:2 blgp:2
	v_mfma_scale_f32_16x16x128_f8f6f4 v[138:141], v[122:127], v[50:55], v[138:141], v179, v112 op_sel_hi:[0,0,0] cbsz:2 blgp:2
	v_mfma_scale_f32_16x16x128_f8f6f4 v[142:145], v[122:127], v[62:67], v[142:145], v179, v112 op_sel_hi:[0,0,0] cbsz:2 blgp:2
	s_waitcnt lgkmcnt(0)
	v_mfma_scale_f32_16x16x128_f8f6f4 v[134:137], v[128:133], v[8:13], v[134:137], v178, v112 op_sel_hi:[0,0,0] cbsz:2 blgp:2
	v_mfma_scale_f32_16x16x128_f8f6f4 v[134:137], v[128:133], v[44:49], v[134:137], v179, v112 op_sel_hi:[0,0,0] cbsz:2 blgp:2
	v_mfma_scale_f32_16x16x128_f8f6f4 v[138:141], v[128:133], v[20:25], v[138:141], v178, v112 op_sel_hi:[0,0,0] cbsz:2 blgp:2
	v_mfma_scale_f32_16x16x128_f8f6f4 v[138:141], v[128:133], v[56:61], v[138:141], v179, v112 op_sel_hi:[0,0,0] cbsz:2 blgp:2
	v_mfma_scale_f32_16x16x128_f8f6f4 v[142:145], v[128:133], v[32:37], v[142:145], v178, v112 op_sel_hi:[0,0,0] cbsz:2 blgp:2
	v_mfma_scale_f32_16x16x128_f8f6f4 v[142:145], v[128:133], v[68:73], v[142:145], v179, v112 op_sel_hi:[0,0,0] cbsz:2 blgp:2
	v_fma_mix_f32 v158, v134, v100, v83 op_sel_hi:[0,0,1]
	v_exp_f32_e32 v158, v158
	v_fma_mix_f32 v159, v138, v101, v75 op_sel_hi:[0,0,1]
	v_exp_f32_e32 v159, v159
	v_add_f32_e32 v158, 1.0, v158
	v_rcp_f32_e32 v158, v158
	v_add_f32_e32 v159, 1.0, v159
	v_rcp_f32_e32 v159, v159
	v_fma_f32 v160, v142, v102, v103
	v_fma_mix_f32 v161, v158, v160, v79 op_sel_hi:[0,0,1]
	v_exp_f32_e32 v161, v161
	s_add_u32 s48, s48, s40
	v_add_f32_e32 v161, 1.0, v161
	v_rcp_f32_e32 v161, v161
	s_addc_u32 s49, s49, s41
	v_fma_f32 v162, v161, -2.0, 1.0
	v_sub_f32_e32 v163, v176, v162
	v_fma_f32 v176, v159, v163, v162
	v_fma_f32 v164, |v176|, s17, v113
	v_fma_f32 v165, |v176|, s18, v114
	v_fma_f32 v166, |v176|, s19, v115
	v_lshrrev_b32_e32 v167, 26, v176
	v_min3_u32 v164, v164, v165, v166
	v_bfi_b32 v168, 31, v164, v167
	v_lshrrev_b32_e32 v169, v181, v168
	global_store_short_d16_hi v185, v176, s[48:49]
	v_mul_u32_u24_dpp v170, v168, v180 quad_perm:[1,2,3,3] row_mask:0xf bank_mask:0xf bound_ctrl:1
	v_or_b32_e32 v171, v169, v170
	ds_write_b8 v184, v171 offset:416
	s_barrier
	ds_read_b64 v[122:123], v105 offset:416
	ds_read_b64 v[124:125], v105 offset:424
	ds_read_b64 v[126:127], v105 offset:432
	s_waitcnt lgkmcnt(3)
	s_barrier
	ds_read_b64 v[128:129], v105 offset:512
	ds_read_b64 v[130:131], v105 offset:520
	ds_read_b64 v[132:133], v105 offset:528
	s_waitcnt lgkmcnt(3)
	v_mfma_scale_f32_16x16x128_f8f6f4 v[134:137], v[122:127], v[2:7], 0, v178, v112 op_sel_hi:[0,0,0] cbsz:2 blgp:2
	v_mfma_scale_f32_16x16x128_f8f6f4 v[138:141], v[122:127], v[14:19], 0, v178, v112 op_sel_hi:[0,0,0] cbsz:2 blgp:2
	v_mfma_scale_f32_16x16x128_f8f6f4 v[142:145], v[122:127], v[26:31], 0, v178, v112 op_sel_hi:[0,0,0] cbsz:2 blgp:2
	v_mfma_scale_f32_16x16x128_f8f6f4 v[134:137], v[122:127], v[38:43], v[134:137], v179, v112 op_sel_hi:[0,0,0] cbsz:2 blgp:2
	v_mfma_scale_f32_16x16x128_f8f6f4 v[138:141], v[122:127], v[50:55], v[138:141], v179, v112 op_sel_hi:[0,0,0] cbsz:2 blgp:2
	v_mfma_scale_f32_16x16x128_f8f6f4 v[142:145], v[122:127], v[62:67], v[142:145], v179, v112 op_sel_hi:[0,0,0] cbsz:2 blgp:2
	s_waitcnt lgkmcnt(0)
	v_mfma_scale_f32_16x16x128_f8f6f4 v[134:137], v[128:133], v[8:13], v[134:137], v178, v112 op_sel_hi:[0,0,0] cbsz:2 blgp:2
	v_mfma_scale_f32_16x16x128_f8f6f4 v[134:137], v[128:133], v[44:49], v[134:137], v179, v112 op_sel_hi:[0,0,0] cbsz:2 blgp:2
	v_mfma_scale_f32_16x16x128_f8f6f4 v[138:141], v[128:133], v[20:25], v[138:141], v178, v112 op_sel_hi:[0,0,0] cbsz:2 blgp:2
	v_mfma_scale_f32_16x16x128_f8f6f4 v[138:141], v[128:133], v[56:61], v[138:141], v179, v112 op_sel_hi:[0,0,0] cbsz:2 blgp:2
	v_mfma_scale_f32_16x16x128_f8f6f4 v[142:145], v[128:133], v[32:37], v[142:145], v178, v112 op_sel_hi:[0,0,0] cbsz:2 blgp:2
	v_mfma_scale_f32_16x16x128_f8f6f4 v[142:145], v[128:133], v[68:73], v[142:145], v179, v112 op_sel_hi:[0,0,0] cbsz:2 blgp:2
	v_fma_mix_f32 v158, v134, v100, v83 op_sel:[0,0,1] op_sel_hi:[0,0,1]
	v_exp_f32_e32 v158, v158
	v_fma_mix_f32 v159, v138, v101, v75 op_sel:[0,0,1] op_sel_hi:[0,0,1]
	v_exp_f32_e32 v159, v159
	v_add_f32_e32 v158, 1.0, v158
	v_rcp_f32_e32 v158, v158
	v_add_f32_e32 v159, 1.0, v159
	v_rcp_f32_e32 v159, v159
	v_fma_f32 v160, v142, v102, v103
	v_fma_mix_f32 v161, v158, v160, v79 op_sel:[0,0,1] op_sel_hi:[0,0,1]
	v_exp_f32_e32 v161, v161
	s_add_u32 s48, s48, s40
	v_add_f32_e32 v161, 1.0, v161
	v_rcp_f32_e32 v161, v161
	s_addc_u32 s49, s49, s41
	v_fma_f32 v162, v161, -2.0, 1.0
	v_sub_f32_e32 v163, v176, v162
	v_fma_f32 v176, v159, v163, v162
	v_fma_f32 v164, |v176|, s17, v113
	v_fma_f32 v165, |v176|, s18, v114
	v_fma_f32 v166, |v176|, s19, v115
	v_lshrrev_b32_e32 v167, 26, v176
	v_min3_u32 v164, v164, v165, v166
	v_bfi_b32 v168, 31, v164, v167
	v_lshrrev_b32_e32 v169, v181, v168
	global_store_short_d16_hi v185, v176, s[48:49]
	v_mul_u32_u24_dpp v170, v168, v180 quad_perm:[1,2,3,3] row_mask:0xf bank_mask:0xf bound_ctrl:1
	v_or_b32_e32 v171, v169, v170
	ds_write_b8 v184, v171
	s_barrier
	ds_read_b64 v[122:123], v105 offset:0
	ds_read_b64 v[124:125], v105 offset:8
	ds_read_b64 v[126:127], v105 offset:16
	s_waitcnt lgkmcnt(3)
	s_barrier
	ds_read_b64 v[128:129], v105 offset:96
	ds_read_b64 v[130:131], v105 offset:104
	ds_read_b64 v[132:133], v105 offset:112
	s_waitcnt lgkmcnt(3)
	v_mfma_scale_f32_16x16x128_f8f6f4 v[134:137], v[122:127], v[2:7], 0, v178, v112 op_sel_hi:[0,0,0] cbsz:2 blgp:2
	v_mfma_scale_f32_16x16x128_f8f6f4 v[138:141], v[122:127], v[14:19], 0, v178, v112 op_sel_hi:[0,0,0] cbsz:2 blgp:2
	v_mfma_scale_f32_16x16x128_f8f6f4 v[142:145], v[122:127], v[26:31], 0, v178, v112 op_sel_hi:[0,0,0] cbsz:2 blgp:2
	v_mfma_scale_f32_16x16x128_f8f6f4 v[134:137], v[122:127], v[38:43], v[134:137], v179, v112 op_sel_hi:[0,0,0] cbsz:2 blgp:2
	v_mfma_scale_f32_16x16x128_f8f6f4 v[138:141], v[122:127], v[50:55], v[138:141], v179, v112 op_sel_hi:[0,0,0] cbsz:2 blgp:2
	v_mfma_scale_f32_16x16x128_f8f6f4 v[142:145], v[122:127], v[62:67], v[142:145], v179, v112 op_sel_hi:[0,0,0] cbsz:2 blgp:2
	s_waitcnt lgkmcnt(0)
	v_mfma_scale_f32_16x16x128_f8f6f4 v[134:137], v[128:133], v[8:13], v[134:137], v178, v112 op_sel_hi:[0,0,0] cbsz:2 blgp:2
	v_mfma_scale_f32_16x16x128_f8f6f4 v[134:137], v[128:133], v[44:49], v[134:137], v179, v112 op_sel_hi:[0,0,0] cbsz:2 blgp:2
	v_mfma_scale_f32_16x16x128_f8f6f4 v[138:141], v[128:133], v[20:25], v[138:141], v178, v112 op_sel_hi:[0,0,0] cbsz:2 blgp:2
	v_mfma_scale_f32_16x16x128_f8f6f4 v[138:141], v[128:133], v[56:61], v[138:141], v179, v112 op_sel_hi:[0,0,0] cbsz:2 blgp:2
	v_mfma_scale_f32_16x16x128_f8f6f4 v[142:145], v[128:133], v[32:37], v[142:145], v178, v112 op_sel_hi:[0,0,0] cbsz:2 blgp:2
	v_mfma_scale_f32_16x16x128_f8f6f4 v[142:145], v[128:133], v[68:73], v[142:145], v179, v112 op_sel_hi:[0,0,0] cbsz:2 blgp:2
	v_fma_mix_f32 v158, v134, v100, v84 op_sel_hi:[0,0,1]
	v_exp_f32_e32 v158, v158
	v_fma_mix_f32 v159, v138, v101, v76 op_sel_hi:[0,0,1]
	v_exp_f32_e32 v159, v159
	v_add_f32_e32 v158, 1.0, v158
	v_rcp_f32_e32 v158, v158
	v_add_f32_e32 v159, 1.0, v159
	v_rcp_f32_e32 v159, v159
	v_fma_f32 v160, v142, v102, v103
	v_fma_mix_f32 v161, v158, v160, v80 op_sel_hi:[0,0,1]
	v_exp_f32_e32 v161, v161
	s_add_u32 s48, s48, s40
	v_add_f32_e32 v161, 1.0, v161
	v_rcp_f32_e32 v161, v161
	s_addc_u32 s49, s49, s41
	v_fma_f32 v162, v161, -2.0, 1.0
	v_sub_f32_e32 v163, v176, v162
	v_fma_f32 v176, v159, v163, v162
	v_fma_f32 v164, |v176|, s17, v113
	v_fma_f32 v165, |v176|, s18, v114
	v_fma_f32 v166, |v176|, s19, v115
	v_lshrrev_b32_e32 v167, 26, v176
	v_min3_u32 v164, v164, v165, v166
	v_bfi_b32 v168, 31, v164, v167
	v_lshrrev_b32_e32 v169, v181, v168
	global_store_short_d16_hi v185, v176, s[48:49]
	v_mul_u32_u24_dpp v170, v168, v180 quad_perm:[1,2,3,3] row_mask:0xf bank_mask:0xf bound_ctrl:1
	v_or_b32_e32 v171, v169, v170
	ds_write_b8 v184, v171 offset:416
	s_barrier
	ds_read_b64 v[122:123], v105 offset:416
	ds_read_b64 v[124:125], v105 offset:424
	ds_read_b64 v[126:127], v105 offset:432
	s_waitcnt lgkmcnt(3)
	s_barrier
	ds_read_b64 v[128:129], v105 offset:512
	ds_read_b64 v[130:131], v105 offset:520
	ds_read_b64 v[132:133], v105 offset:528
	s_waitcnt lgkmcnt(3)
	v_mfma_scale_f32_16x16x128_f8f6f4 v[134:137], v[122:127], v[2:7], 0, v178, v112 op_sel_hi:[0,0,0] cbsz:2 blgp:2
	v_mfma_scale_f32_16x16x128_f8f6f4 v[138:141], v[122:127], v[14:19], 0, v178, v112 op_sel_hi:[0,0,0] cbsz:2 blgp:2
	v_mfma_scale_f32_16x16x128_f8f6f4 v[142:145], v[122:127], v[26:31], 0, v178, v112 op_sel_hi:[0,0,0] cbsz:2 blgp:2
	v_mfma_scale_f32_16x16x128_f8f6f4 v[134:137], v[122:127], v[38:43], v[134:137], v179, v112 op_sel_hi:[0,0,0] cbsz:2 blgp:2
	v_mfma_scale_f32_16x16x128_f8f6f4 v[138:141], v[122:127], v[50:55], v[138:141], v179, v112 op_sel_hi:[0,0,0] cbsz:2 blgp:2
	v_mfma_scale_f32_16x16x128_f8f6f4 v[142:145], v[122:127], v[62:67], v[142:145], v179, v112 op_sel_hi:[0,0,0] cbsz:2 blgp:2
	s_waitcnt lgkmcnt(0)
	v_mfma_scale_f32_16x16x128_f8f6f4 v[134:137], v[128:133], v[8:13], v[134:137], v178, v112 op_sel_hi:[0,0,0] cbsz:2 blgp:2
	v_mfma_scale_f32_16x16x128_f8f6f4 v[134:137], v[128:133], v[44:49], v[134:137], v179, v112 op_sel_hi:[0,0,0] cbsz:2 blgp:2
	v_mfma_scale_f32_16x16x128_f8f6f4 v[138:141], v[128:133], v[20:25], v[138:141], v178, v112 op_sel_hi:[0,0,0] cbsz:2 blgp:2
	v_mfma_scale_f32_16x16x128_f8f6f4 v[138:141], v[128:133], v[56:61], v[138:141], v179, v112 op_sel_hi:[0,0,0] cbsz:2 blgp:2
	v_mfma_scale_f32_16x16x128_f8f6f4 v[142:145], v[128:133], v[32:37], v[142:145], v178, v112 op_sel_hi:[0,0,0] cbsz:2 blgp:2
	v_mfma_scale_f32_16x16x128_f8f6f4 v[142:145], v[128:133], v[68:73], v[142:145], v179, v112 op_sel_hi:[0,0,0] cbsz:2 blgp:2
	v_fma_mix_f32 v158, v134, v100, v84 op_sel:[0,0,1] op_sel_hi:[0,0,1]
	v_exp_f32_e32 v158, v158
	v_fma_mix_f32 v159, v138, v101, v76 op_sel:[0,0,1] op_sel_hi:[0,0,1]
	v_exp_f32_e32 v159, v159
	v_add_f32_e32 v158, 1.0, v158
	v_rcp_f32_e32 v158, v158
	v_add_f32_e32 v159, 1.0, v159
	v_rcp_f32_e32 v159, v159
	v_fma_f32 v160, v142, v102, v103
	v_fma_mix_f32 v161, v158, v160, v80 op_sel:[0,0,1] op_sel_hi:[0,0,1]
	v_exp_f32_e32 v161, v161
	s_add_u32 s48, s48, s40
	v_add_f32_e32 v161, 1.0, v161
	v_rcp_f32_e32 v161, v161
	s_addc_u32 s49, s49, s41
	v_fma_f32 v162, v161, -2.0, 1.0
	v_sub_f32_e32 v163, v176, v162
	v_fma_f32 v176, v159, v163, v162
	v_fma_f32 v164, |v176|, s17, v113
	v_fma_f32 v165, |v176|, s18, v114
	v_fma_f32 v166, |v176|, s19, v115
	v_lshrrev_b32_e32 v167, 26, v176
	v_min3_u32 v164, v164, v165, v166
	v_bfi_b32 v168, 31, v164, v167
	v_lshrrev_b32_e32 v169, v181, v168
	global_store_short_d16_hi v185, v176, s[48:49]
	v_mul_u32_u24_dpp v170, v168, v180 quad_perm:[1,2,3,3] row_mask:0xf bank_mask:0xf bound_ctrl:1
	v_or_b32_e32 v171, v169, v170
	ds_write_b8 v184, v171
	s_barrier
	ds_read_b64 v[122:123], v105 offset:0
	ds_read_b64 v[124:125], v105 offset:8
	ds_read_b64 v[126:127], v105 offset:16
	s_waitcnt lgkmcnt(3)
	s_barrier
	ds_read_b64 v[128:129], v105 offset:96
	ds_read_b64 v[130:131], v105 offset:104
	ds_read_b64 v[132:133], v105 offset:112
	s_waitcnt lgkmcnt(3)
	v_mfma_scale_f32_16x16x128_f8f6f4 v[134:137], v[122:127], v[2:7], 0, v178, v112 op_sel_hi:[0,0,0] cbsz:2 blgp:2
	v_mfma_scale_f32_16x16x128_f8f6f4 v[138:141], v[122:127], v[14:19], 0, v178, v112 op_sel_hi:[0,0,0] cbsz:2 blgp:2
	v_mfma_scale_f32_16x16x128_f8f6f4 v[142:145], v[122:127], v[26:31], 0, v178, v112 op_sel_hi:[0,0,0] cbsz:2 blgp:2
	v_mfma_scale_f32_16x16x128_f8f6f4 v[134:137], v[122:127], v[38:43], v[134:137], v179, v112 op_sel_hi:[0,0,0] cbsz:2 blgp:2
	v_mfma_scale_f32_16x16x128_f8f6f4 v[138:141], v[122:127], v[50:55], v[138:141], v179, v112 op_sel_hi:[0,0,0] cbsz:2 blgp:2
	v_mfma_scale_f32_16x16x128_f8f6f4 v[142:145], v[122:127], v[62:67], v[142:145], v179, v112 op_sel_hi:[0,0,0] cbsz:2 blgp:2
	s_waitcnt lgkmcnt(0)
	v_mfma_scale_f32_16x16x128_f8f6f4 v[134:137], v[128:133], v[8:13], v[134:137], v178, v112 op_sel_hi:[0,0,0] cbsz:2 blgp:2
	v_mfma_scale_f32_16x16x128_f8f6f4 v[134:137], v[128:133], v[44:49], v[134:137], v179, v112 op_sel_hi:[0,0,0] cbsz:2 blgp:2
	v_mfma_scale_f32_16x16x128_f8f6f4 v[138:141], v[128:133], v[20:25], v[138:141], v178, v112 op_sel_hi:[0,0,0] cbsz:2 blgp:2
	v_mfma_scale_f32_16x16x128_f8f6f4 v[138:141], v[128:133], v[56:61], v[138:141], v179, v112 op_sel_hi:[0,0,0] cbsz:2 blgp:2
	v_mfma_scale_f32_16x16x128_f8f6f4 v[142:145], v[128:133], v[32:37], v[142:145], v178, v112 op_sel_hi:[0,0,0] cbsz:2 blgp:2
	v_mfma_scale_f32_16x16x128_f8f6f4 v[142:145], v[128:133], v[68:73], v[142:145], v179, v112 op_sel_hi:[0,0,0] cbsz:2 blgp:2
	v_fma_mix_f32 v158, v134, v100, v85 op_sel_hi:[0,0,1]
	v_exp_f32_e32 v158, v158
	v_fma_mix_f32 v159, v138, v101, v77 op_sel_hi:[0,0,1]
	v_exp_f32_e32 v159, v159
	v_add_f32_e32 v158, 1.0, v158
	v_rcp_f32_e32 v158, v158
	v_add_f32_e32 v159, 1.0, v159
	v_rcp_f32_e32 v159, v159
	v_fma_f32 v160, v142, v102, v103
	v_fma_mix_f32 v161, v158, v160, v81 op_sel_hi:[0,0,1]
	v_exp_f32_e32 v161, v161
	s_add_u32 s48, s48, s40
	v_add_f32_e32 v161, 1.0, v161
	v_rcp_f32_e32 v161, v161
	s_addc_u32 s49, s49, s41
	v_fma_f32 v162, v161, -2.0, 1.0
	v_sub_f32_e32 v163, v176, v162
	v_fma_f32 v176, v159, v163, v162
	v_fma_f32 v164, |v176|, s17, v113
	v_fma_f32 v165, |v176|, s18, v114
	v_fma_f32 v166, |v176|, s19, v115
	v_lshrrev_b32_e32 v167, 26, v176
	v_min3_u32 v164, v164, v165, v166
	v_bfi_b32 v168, 31, v164, v167
	v_lshrrev_b32_e32 v169, v181, v168
	global_store_short_d16_hi v185, v176, s[48:49]
	v_mul_u32_u24_dpp v170, v168, v180 quad_perm:[1,2,3,3] row_mask:0xf bank_mask:0xf bound_ctrl:1
	v_or_b32_e32 v171, v169, v170
	ds_write_b8 v184, v171 offset:416
	s_barrier
	ds_read_b64 v[122:123], v105 offset:416
	ds_read_b64 v[124:125], v105 offset:424
	ds_read_b64 v[126:127], v105 offset:432
	s_waitcnt lgkmcnt(3)
	s_barrier
	ds_read_b64 v[128:129], v105 offset:512
	ds_read_b64 v[130:131], v105 offset:520
	ds_read_b64 v[132:133], v105 offset:528
	s_waitcnt lgkmcnt(3)
	v_mfma_scale_f32_16x16x128_f8f6f4 v[134:137], v[122:127], v[2:7], 0, v178, v112 op_sel_hi:[0,0,0] cbsz:2 blgp:2
	v_mfma_scale_f32_16x16x128_f8f6f4 v[138:141], v[122:127], v[14:19], 0, v178, v112 op_sel_hi:[0,0,0] cbsz:2 blgp:2
	v_mfma_scale_f32_16x16x128_f8f6f4 v[142:145], v[122:127], v[26:31], 0, v178, v112 op_sel_hi:[0,0,0] cbsz:2 blgp:2
	v_mfma_scale_f32_16x16x128_f8f6f4 v[134:137], v[122:127], v[38:43], v[134:137], v179, v112 op_sel_hi:[0,0,0] cbsz:2 blgp:2
	v_mfma_scale_f32_16x16x128_f8f6f4 v[138:141], v[122:127], v[50:55], v[138:141], v179, v112 op_sel_hi:[0,0,0] cbsz:2 blgp:2
	v_mfma_scale_f32_16x16x128_f8f6f4 v[142:145], v[122:127], v[62:67], v[142:145], v179, v112 op_sel_hi:[0,0,0] cbsz:2 blgp:2
	s_waitcnt lgkmcnt(0)
	v_mfma_scale_f32_16x16x128_f8f6f4 v[134:137], v[128:133], v[8:13], v[134:137], v178, v112 op_sel_hi:[0,0,0] cbsz:2 blgp:2
	v_mfma_scale_f32_16x16x128_f8f6f4 v[134:137], v[128:133], v[44:49], v[134:137], v179, v112 op_sel_hi:[0,0,0] cbsz:2 blgp:2
	v_mfma_scale_f32_16x16x128_f8f6f4 v[138:141], v[128:133], v[20:25], v[138:141], v178, v112 op_sel_hi:[0,0,0] cbsz:2 blgp:2
	v_mfma_scale_f32_16x16x128_f8f6f4 v[138:141], v[128:133], v[56:61], v[138:141], v179, v112 op_sel_hi:[0,0,0] cbsz:2 blgp:2
	v_mfma_scale_f32_16x16x128_f8f6f4 v[142:145], v[128:133], v[32:37], v[142:145], v178, v112 op_sel_hi:[0,0,0] cbsz:2 blgp:2
	v_mfma_scale_f32_16x16x128_f8f6f4 v[142:145], v[128:133], v[68:73], v[142:145], v179, v112 op_sel_hi:[0,0,0] cbsz:2 blgp:2
	v_fma_mix_f32 v158, v134, v100, v85 op_sel:[0,0,1] op_sel_hi:[0,0,1]
	v_exp_f32_e32 v158, v158
	v_fma_mix_f32 v159, v138, v101, v77 op_sel:[0,0,1] op_sel_hi:[0,0,1]
	v_exp_f32_e32 v159, v159
	v_add_f32_e32 v158, 1.0, v158
	v_rcp_f32_e32 v158, v158
	v_add_f32_e32 v159, 1.0, v159
	v_rcp_f32_e32 v159, v159
	v_fma_f32 v160, v142, v102, v103
	v_fma_mix_f32 v161, v158, v160, v81 op_sel:[0,0,1] op_sel_hi:[0,0,1]
	v_exp_f32_e32 v161, v161
	s_add_u32 s48, s48, s40
	v_add_f32_e32 v161, 1.0, v161
	v_rcp_f32_e32 v161, v161
	s_addc_u32 s49, s49, s41
	v_fma_f32 v162, v161, -2.0, 1.0
	v_sub_f32_e32 v163, v176, v162
	v_fma_f32 v176, v159, v163, v162
	v_fma_f32 v164, |v176|, s17, v113
	v_fma_f32 v165, |v176|, s18, v114
	v_fma_f32 v166, |v176|, s19, v115
	v_lshrrev_b32_e32 v167, 26, v176
	v_min3_u32 v164, v164, v165, v166
	v_bfi_b32 v168, 31, v164, v167
	v_lshrrev_b32_e32 v169, v181, v168
	global_store_short_d16_hi v185, v176, s[48:49]
	v_mul_u32_u24_dpp v170, v168, v180 quad_perm:[1,2,3,3] row_mask:0xf bank_mask:0xf bound_ctrl:1
	v_or_b32_e32 v171, v169, v170
	ds_write_b8 v184, v171
	s_barrier
	ds_read_b64 v[122:123], v105 offset:0
	ds_read_b64 v[124:125], v105 offset:8
	ds_read_b64 v[126:127], v105 offset:16
	s_waitcnt lgkmcnt(3)
	s_barrier
	ds_read_b64 v[128:129], v105 offset:96
	ds_read_b64 v[130:131], v105 offset:104
	ds_read_b64 v[132:133], v105 offset:112
	s_waitcnt vmcnt(8)
	global_load_dwordx4 v[82:85], v[196:197], off
	global_load_dwordx4 v[74:77], v[196:197], off offset:512
	global_load_dwordx4 v[78:81], v[196:197], off offset:1024
	v_lshl_add_u64 v[196:197], v[196:197], 0, s[42:43]
	s_waitcnt lgkmcnt(3)
	v_mfma_scale_f32_16x16x128_f8f6f4 v[134:137], v[122:127], v[2:7], 0, v178, v112 op_sel_hi:[0,0,0] cbsz:2 blgp:2
	v_mfma_scale_f32_16x16x128_f8f6f4 v[138:141], v[122:127], v[14:19], 0, v178, v112 op_sel_hi:[0,0,0] cbsz:2 blgp:2
	v_mfma_scale_f32_16x16x128_f8f6f4 v[142:145], v[122:127], v[26:31], 0, v178, v112 op_sel_hi:[0,0,0] cbsz:2 blgp:2
	v_mfma_scale_f32_16x16x128_f8f6f4 v[134:137], v[122:127], v[38:43], v[134:137], v179, v112 op_sel_hi:[0,0,0] cbsz:2 blgp:2
	v_mfma_scale_f32_16x16x128_f8f6f4 v[138:141], v[122:127], v[50:55], v[138:141], v179, v112 op_sel_hi:[0,0,0] cbsz:2 blgp:2
	v_mfma_scale_f32_16x16x128_f8f6f4 v[142:145], v[122:127], v[62:67], v[142:145], v179, v112 op_sel_hi:[0,0,0] cbsz:2 blgp:2
	s_waitcnt lgkmcnt(0)
	v_mfma_scale_f32_16x16x128_f8f6f4 v[134:137], v[128:133], v[8:13], v[134:137], v178, v112 op_sel_hi:[0,0,0] cbsz:2 blgp:2
	v_mfma_scale_f32_16x16x128_f8f6f4 v[134:137], v[128:133], v[44:49], v[134:137], v179, v112 op_sel_hi:[0,0,0] cbsz:2 blgp:2
	v_mfma_scale_f32_16x16x128_f8f6f4 v[138:141], v[128:133], v[20:25], v[138:141], v178, v112 op_sel_hi:[0,0,0] cbsz:2 blgp:2
	v_mfma_scale_f32_16x16x128_f8f6f4 v[138:141], v[128:133], v[56:61], v[138:141], v179, v112 op_sel_hi:[0,0,0] cbsz:2 blgp:2
	v_mfma_scale_f32_16x16x128_f8f6f4 v[142:145], v[128:133], v[32:37], v[142:145], v178, v112 op_sel_hi:[0,0,0] cbsz:2 blgp:2
	v_mfma_scale_f32_16x16x128_f8f6f4 v[142:145], v[128:133], v[68:73], v[142:145], v179, v112 op_sel_hi:[0,0,0] cbsz:2 blgp:2
	v_fma_mix_f32 v158, v134, v100, v146 op_sel_hi:[0,0,1]
	v_exp_f32_e32 v158, v158
	v_fma_mix_f32 v159, v138, v101, v150 op_sel_hi:[0,0,1]
	v_exp_f32_e32 v159, v159
	v_add_f32_e32 v158, 1.0, v158
	v_rcp_f32_e32 v158, v158
	v_add_f32_e32 v159, 1.0, v159
	v_rcp_f32_e32 v159, v159
	v_fma_f32 v160, v142, v102, v103
	v_fma_mix_f32 v161, v158, v160, v154 op_sel_hi:[0,0,1]
	v_exp_f32_e32 v161, v161
	s_add_u32 s48, s48, s40
	v_add_f32_e32 v161, 1.0, v161
	v_rcp_f32_e32 v161, v161
	s_addc_u32 s49, s49, s41
	v_fma_f32 v162, v161, -2.0, 1.0
	v_sub_f32_e32 v163, v176, v162
	v_fma_f32 v176, v159, v163, v162
	v_fma_f32 v164, |v176|, s17, v113
	v_fma_f32 v165, |v176|, s18, v114
	v_fma_f32 v166, |v176|, s19, v115
	v_lshrrev_b32_e32 v167, 26, v176
	v_min3_u32 v164, v164, v165, v166
	v_bfi_b32 v168, 31, v164, v167
	v_lshrrev_b32_e32 v169, v181, v168
	global_store_short_d16_hi v185, v176, s[48:49]
	v_mul_u32_u24_dpp v170, v168, v180 quad_perm:[1,2,3,3] row_mask:0xf bank_mask:0xf bound_ctrl:1
	v_or_b32_e32 v171, v169, v170
	ds_write_b8 v184, v171 offset:416
	s_barrier
	ds_read_b64 v[122:123], v105 offset:416
	ds_read_b64 v[124:125], v105 offset:424
	ds_read_b64 v[126:127], v105 offset:432
	s_waitcnt lgkmcnt(3)
	s_barrier
	ds_read_b64 v[128:129], v105 offset:512
	ds_read_b64 v[130:131], v105 offset:520
	ds_read_b64 v[132:133], v105 offset:528
	s_waitcnt lgkmcnt(3)
	v_mfma_scale_f32_16x16x128_f8f6f4 v[134:137], v[122:127], v[2:7], 0, v178, v112 op_sel_hi:[0,0,0] cbsz:2 blgp:2
	v_mfma_scale_f32_16x16x128_f8f6f4 v[138:141], v[122:127], v[14:19], 0, v178, v112 op_sel_hi:[0,0,0] cbsz:2 blgp:2
	v_mfma_scale_f32_16x16x128_f8f6f4 v[142:145], v[122:127], v[26:31], 0, v178, v112 op_sel_hi:[0,0,0] cbsz:2 blgp:2
	v_mfma_scale_f32_16x16x128_f8f6f4 v[134:137], v[122:127], v[38:43], v[134:137], v179, v112 op_sel_hi:[0,0,0] cbsz:2 blgp:2
	v_mfma_scale_f32_16x16x128_f8f6f4 v[138:141], v[122:127], v[50:55], v[138:141], v179, v112 op_sel_hi:[0,0,0] cbsz:2 blgp:2
	v_mfma_scale_f32_16x16x128_f8f6f4 v[142:145], v[122:127], v[62:67], v[142:145], v179, v112 op_sel_hi:[0,0,0] cbsz:2 blgp:2
	s_waitcnt lgkmcnt(0)
	v_mfma_scale_f32_16x16x128_f8f6f4 v[134:137], v[128:133], v[8:13], v[134:137], v178, v112 op_sel_hi:[0,0,0] cbsz:2 blgp:2
	v_mfma_scale_f32_16x16x128_f8f6f4 v[134:137], v[128:133], v[44:49], v[134:137], v179, v112 op_sel_hi:[0,0,0] cbsz:2 blgp:2
	v_mfma_scale_f32_16x16x128_f8f6f4 v[138:141], v[128:133], v[20:25], v[138:141], v178, v112 op_sel_hi:[0,0,0] cbsz:2 blgp:2
	v_mfma_scale_f32_16x16x128_f8f6f4 v[138:141], v[128:133], v[56:61], v[138:141], v179, v112 op_sel_hi:[0,0,0] cbsz:2 blgp:2
	v_mfma_scale_f32_16x16x128_f8f6f4 v[142:145], v[128:133], v[32:37], v[142:145], v178, v112 op_sel_hi:[0,0,0] cbsz:2 blgp:2
	v_mfma_scale_f32_16x16x128_f8f6f4 v[142:145], v[128:133], v[68:73], v[142:145], v179, v112 op_sel_hi:[0,0,0] cbsz:2 blgp:2
	v_fma_mix_f32 v158, v134, v100, v146 op_sel:[0,0,1] op_sel_hi:[0,0,1]
	v_exp_f32_e32 v158, v158
	v_fma_mix_f32 v159, v138, v101, v150 op_sel:[0,0,1] op_sel_hi:[0,0,1]
	v_exp_f32_e32 v159, v159
	v_add_f32_e32 v158, 1.0, v158
	v_rcp_f32_e32 v158, v158
	v_add_f32_e32 v159, 1.0, v159
	v_rcp_f32_e32 v159, v159
	v_fma_f32 v160, v142, v102, v103
	v_fma_mix_f32 v161, v158, v160, v154 op_sel:[0,0,1] op_sel_hi:[0,0,1]
	v_exp_f32_e32 v161, v161
	s_add_u32 s48, s48, s40
	v_add_f32_e32 v161, 1.0, v161
	v_rcp_f32_e32 v161, v161
	s_addc_u32 s49, s49, s41
	v_fma_f32 v162, v161, -2.0, 1.0
	v_sub_f32_e32 v163, v176, v162
	v_fma_f32 v176, v159, v163, v162
	v_fma_f32 v164, |v176|, s17, v113
	v_fma_f32 v165, |v176|, s18, v114
	v_fma_f32 v166, |v176|, s19, v115
	v_lshrrev_b32_e32 v167, 26, v176
	v_min3_u32 v164, v164, v165, v166
	v_bfi_b32 v168, 31, v164, v167
	v_lshrrev_b32_e32 v169, v181, v168
	global_store_short_d16_hi v185, v176, s[48:49]
	v_mul_u32_u24_dpp v170, v168, v180 quad_perm:[1,2,3,3] row_mask:0xf bank_mask:0xf bound_ctrl:1
	v_or_b32_e32 v171, v169, v170
	ds_write_b8 v184, v171
	s_barrier
	ds_read_b64 v[122:123], v105 offset:0
	ds_read_b64 v[124:125], v105 offset:8
	ds_read_b64 v[126:127], v105 offset:16
	s_waitcnt lgkmcnt(3)
	s_barrier
	ds_read_b64 v[128:129], v105 offset:96
	ds_read_b64 v[130:131], v105 offset:104
	ds_read_b64 v[132:133], v105 offset:112
	s_waitcnt lgkmcnt(3)
	v_mfma_scale_f32_16x16x128_f8f6f4 v[134:137], v[122:127], v[2:7], 0, v178, v112 op_sel_hi:[0,0,0] cbsz:2 blgp:2
	v_mfma_scale_f32_16x16x128_f8f6f4 v[138:141], v[122:127], v[14:19], 0, v178, v112 op_sel_hi:[0,0,0] cbsz:2 blgp:2
	v_mfma_scale_f32_16x16x128_f8f6f4 v[142:145], v[122:127], v[26:31], 0, v178, v112 op_sel_hi:[0,0,0] cbsz:2 blgp:2
	v_mfma_scale_f32_16x16x128_f8f6f4 v[134:137], v[122:127], v[38:43], v[134:137], v179, v112 op_sel_hi:[0,0,0] cbsz:2 blgp:2
	v_mfma_scale_f32_16x16x128_f8f6f4 v[138:141], v[122:127], v[50:55], v[138:141], v179, v112 op_sel_hi:[0,0,0] cbsz:2 blgp:2
	v_mfma_scale_f32_16x16x128_f8f6f4 v[142:145], v[122:127], v[62:67], v[142:145], v179, v112 op_sel_hi:[0,0,0] cbsz:2 blgp:2
	s_waitcnt lgkmcnt(0)
	v_mfma_scale_f32_16x16x128_f8f6f4 v[134:137], v[128:133], v[8:13], v[134:137], v178, v112 op_sel_hi:[0,0,0] cbsz:2 blgp:2
	v_mfma_scale_f32_16x16x128_f8f6f4 v[134:137], v[128:133], v[44:49], v[134:137], v179, v112 op_sel_hi:[0,0,0] cbsz:2 blgp:2
	v_mfma_scale_f32_16x16x128_f8f6f4 v[138:141], v[128:133], v[20:25], v[138:141], v178, v112 op_sel_hi:[0,0,0] cbsz:2 blgp:2
	v_mfma_scale_f32_16x16x128_f8f6f4 v[138:141], v[128:133], v[56:61], v[138:141], v179, v112 op_sel_hi:[0,0,0] cbsz:2 blgp:2
	v_mfma_scale_f32_16x16x128_f8f6f4 v[142:145], v[128:133], v[32:37], v[142:145], v178, v112 op_sel_hi:[0,0,0] cbsz:2 blgp:2
	v_mfma_scale_f32_16x16x128_f8f6f4 v[142:145], v[128:133], v[68:73], v[142:145], v179, v112 op_sel_hi:[0,0,0] cbsz:2 blgp:2
	v_fma_mix_f32 v158, v134, v100, v147 op_sel_hi:[0,0,1]
	v_exp_f32_e32 v158, v158
	v_fma_mix_f32 v159, v138, v101, v151 op_sel_hi:[0,0,1]
	v_exp_f32_e32 v159, v159
	v_add_f32_e32 v158, 1.0, v158
	v_rcp_f32_e32 v158, v158
	v_add_f32_e32 v159, 1.0, v159
	v_rcp_f32_e32 v159, v159
	v_fma_f32 v160, v142, v102, v103
	v_fma_mix_f32 v161, v158, v160, v155 op_sel_hi:[0,0,1]
	v_exp_f32_e32 v161, v161
	s_add_u32 s48, s48, s40
	v_add_f32_e32 v161, 1.0, v161
	v_rcp_f32_e32 v161, v161
	s_addc_u32 s49, s49, s41
	v_fma_f32 v162, v161, -2.0, 1.0
	v_sub_f32_e32 v163, v176, v162
	v_fma_f32 v176, v159, v163, v162
	v_fma_f32 v164, |v176|, s17, v113
	v_fma_f32 v165, |v176|, s18, v114
	v_fma_f32 v166, |v176|, s19, v115
	v_lshrrev_b32_e32 v167, 26, v176
	v_min3_u32 v164, v164, v165, v166
	v_bfi_b32 v168, 31, v164, v167
	v_lshrrev_b32_e32 v169, v181, v168
	global_store_short_d16_hi v185, v176, s[48:49]
	v_mul_u32_u24_dpp v170, v168, v180 quad_perm:[1,2,3,3] row_mask:0xf bank_mask:0xf bound_ctrl:1
	v_or_b32_e32 v171, v169, v170
	ds_write_b8 v184, v171 offset:416
	s_barrier
	ds_read_b64 v[122:123], v105 offset:416
	ds_read_b64 v[124:125], v105 offset:424
	ds_read_b64 v[126:127], v105 offset:432
	s_waitcnt lgkmcnt(3)
	s_barrier
	ds_read_b64 v[128:129], v105 offset:512
	ds_read_b64 v[130:131], v105 offset:520
	ds_read_b64 v[132:133], v105 offset:528
	s_waitcnt lgkmcnt(3)
	v_mfma_scale_f32_16x16x128_f8f6f4 v[134:137], v[122:127], v[2:7], 0, v178, v112 op_sel_hi:[0,0,0] cbsz:2 blgp:2
	v_mfma_scale_f32_16x16x128_f8f6f4 v[138:141], v[122:127], v[14:19], 0, v178, v112 op_sel_hi:[0,0,0] cbsz:2 blgp:2
	v_mfma_scale_f32_16x16x128_f8f6f4 v[142:145], v[122:127], v[26:31], 0, v178, v112 op_sel_hi:[0,0,0] cbsz:2 blgp:2
	v_mfma_scale_f32_16x16x128_f8f6f4 v[134:137], v[122:127], v[38:43], v[134:137], v179, v112 op_sel_hi:[0,0,0] cbsz:2 blgp:2
	v_mfma_scale_f32_16x16x128_f8f6f4 v[138:141], v[122:127], v[50:55], v[138:141], v179, v112 op_sel_hi:[0,0,0] cbsz:2 blgp:2
	v_mfma_scale_f32_16x16x128_f8f6f4 v[142:145], v[122:127], v[62:67], v[142:145], v179, v112 op_sel_hi:[0,0,0] cbsz:2 blgp:2
	s_waitcnt lgkmcnt(0)
	v_mfma_scale_f32_16x16x128_f8f6f4 v[134:137], v[128:133], v[8:13], v[134:137], v178, v112 op_sel_hi:[0,0,0] cbsz:2 blgp:2
	v_mfma_scale_f32_16x16x128_f8f6f4 v[134:137], v[128:133], v[44:49], v[134:137], v179, v112 op_sel_hi:[0,0,0] cbsz:2 blgp:2
	v_mfma_scale_f32_16x16x128_f8f6f4 v[138:141], v[128:133], v[20:25], v[138:141], v178, v112 op_sel_hi:[0,0,0] cbsz:2 blgp:2
	v_mfma_scale_f32_16x16x128_f8f6f4 v[138:141], v[128:133], v[56:61], v[138:141], v179, v112 op_sel_hi:[0,0,0] cbsz:2 blgp:2
	v_mfma_scale_f32_16x16x128_f8f6f4 v[142:145], v[128:133], v[32:37], v[142:145], v178, v112 op_sel_hi:[0,0,0] cbsz:2 blgp:2
	v_mfma_scale_f32_16x16x128_f8f6f4 v[142:145], v[128:133], v[68:73], v[142:145], v179, v112 op_sel_hi:[0,0,0] cbsz:2 blgp:2
	v_fma_mix_f32 v158, v134, v100, v147 op_sel:[0,0,1] op_sel_hi:[0,0,1]
	v_exp_f32_e32 v158, v158
	v_fma_mix_f32 v159, v138, v101, v151 op_sel:[0,0,1] op_sel_hi:[0,0,1]
	v_exp_f32_e32 v159, v159
	v_add_f32_e32 v158, 1.0, v158
	v_rcp_f32_e32 v158, v158
	v_add_f32_e32 v159, 1.0, v159
	v_rcp_f32_e32 v159, v159
	v_fma_f32 v160, v142, v102, v103
	v_fma_mix_f32 v161, v158, v160, v155 op_sel:[0,0,1] op_sel_hi:[0,0,1]
	v_exp_f32_e32 v161, v161
	s_add_u32 s48, s48, s40
	v_add_f32_e32 v161, 1.0, v161
	v_rcp_f32_e32 v161, v161
	s_addc_u32 s49, s49, s41
	v_fma_f32 v162, v161, -2.0, 1.0
	v_sub_f32_e32 v163, v176, v162
	v_fma_f32 v176, v159, v163, v162
	v_fma_f32 v164, |v176|, s17, v113
	v_fma_f32 v165, |v176|, s18, v114
	v_fma_f32 v166, |v176|, s19, v115
	v_lshrrev_b32_e32 v167, 26, v176
	v_min3_u32 v164, v164, v165, v166
	v_bfi_b32 v168, 31, v164, v167
	v_lshrrev_b32_e32 v169, v181, v168
	global_store_short_d16_hi v185, v176, s[48:49]
	v_mul_u32_u24_dpp v170, v168, v180 quad_perm:[1,2,3,3] row_mask:0xf bank_mask:0xf bound_ctrl:1
	v_or_b32_e32 v171, v169, v170
	ds_write_b8 v184, v171
	s_barrier
	ds_read_b64 v[122:123], v105 offset:0
	ds_read_b64 v[124:125], v105 offset:8
	ds_read_b64 v[126:127], v105 offset:16
	s_waitcnt lgkmcnt(3)
	s_barrier
	ds_read_b64 v[128:129], v105 offset:96
	ds_read_b64 v[130:131], v105 offset:104
	ds_read_b64 v[132:133], v105 offset:112
	s_waitcnt lgkmcnt(3)
	v_mfma_scale_f32_16x16x128_f8f6f4 v[134:137], v[122:127], v[2:7], 0, v178, v112 op_sel_hi:[0,0,0] cbsz:2 blgp:2
	v_mfma_scale_f32_16x16x128_f8f6f4 v[138:141], v[122:127], v[14:19], 0, v178, v112 op_sel_hi:[0,0,0] cbsz:2 blgp:2
	v_mfma_scale_f32_16x16x128_f8f6f4 v[142:145], v[122:127], v[26:31], 0, v178, v112 op_sel_hi:[0,0,0] cbsz:2 blgp:2
	v_mfma_scale_f32_16x16x128_f8f6f4 v[134:137], v[122:127], v[38:43], v[134:137], v179, v112 op_sel_hi:[0,0,0] cbsz:2 blgp:2
	v_mfma_scale_f32_16x16x128_f8f6f4 v[138:141], v[122:127], v[50:55], v[138:141], v179, v112 op_sel_hi:[0,0,0] cbsz:2 blgp:2
	v_mfma_scale_f32_16x16x128_f8f6f4 v[142:145], v[122:127], v[62:67], v[142:145], v179, v112 op_sel_hi:[0,0,0] cbsz:2 blgp:2
	s_waitcnt lgkmcnt(0)
	v_mfma_scale_f32_16x16x128_f8f6f4 v[134:137], v[128:133], v[8:13], v[134:137], v178, v112 op_sel_hi:[0,0,0] cbsz:2 blgp:2
	v_mfma_scale_f32_16x16x128_f8f6f4 v[134:137], v[128:133], v[44:49], v[134:137], v179, v112 op_sel_hi:[0,0,0] cbsz:2 blgp:2
	v_mfma_scale_f32_16x16x128_f8f6f4 v[138:141], v[128:133], v[20:25], v[138:141], v178, v112 op_sel_hi:[0,0,0] cbsz:2 blgp:2
	v_mfma_scale_f32_16x16x128_f8f6f4 v[138:141], v[128:133], v[56:61], v[138:141], v179, v112 op_sel_hi:[0,0,0] cbsz:2 blgp:2
	v_mfma_scale_f32_16x16x128_f8f6f4 v[142:145], v[128:133], v[32:37], v[142:145], v178, v112 op_sel_hi:[0,0,0] cbsz:2 blgp:2
	v_mfma_scale_f32_16x16x128_f8f6f4 v[142:145], v[128:133], v[68:73], v[142:145], v179, v112 op_sel_hi:[0,0,0] cbsz:2 blgp:2
	v_fma_mix_f32 v158, v134, v100, v148 op_sel_hi:[0,0,1]
	v_exp_f32_e32 v158, v158
	v_fma_mix_f32 v159, v138, v101, v152 op_sel_hi:[0,0,1]
	v_exp_f32_e32 v159, v159
	v_add_f32_e32 v158, 1.0, v158
	v_rcp_f32_e32 v158, v158
	v_add_f32_e32 v159, 1.0, v159
	v_rcp_f32_e32 v159, v159
	v_fma_f32 v160, v142, v102, v103
	v_fma_mix_f32 v161, v158, v160, v156 op_sel_hi:[0,0,1]
	v_exp_f32_e32 v161, v161
	s_add_u32 s48, s48, s40
	v_add_f32_e32 v161, 1.0, v161
	v_rcp_f32_e32 v161, v161
	s_addc_u32 s49, s49, s41
	v_fma_f32 v162, v161, -2.0, 1.0
	v_sub_f32_e32 v163, v176, v162
	v_fma_f32 v176, v159, v163, v162
	v_fma_f32 v164, |v176|, s17, v113
	v_fma_f32 v165, |v176|, s18, v114
	v_fma_f32 v166, |v176|, s19, v115
	v_lshrrev_b32_e32 v167, 26, v176
	v_min3_u32 v164, v164, v165, v166
	v_bfi_b32 v168, 31, v164, v167
	v_lshrrev_b32_e32 v169, v181, v168
	global_store_short_d16_hi v185, v176, s[48:49]
	v_mul_u32_u24_dpp v170, v168, v180 quad_perm:[1,2,3,3] row_mask:0xf bank_mask:0xf bound_ctrl:1
	v_or_b32_e32 v171, v169, v170
	ds_write_b8 v184, v171 offset:416
	s_barrier
	ds_read_b64 v[122:123], v105 offset:416
	ds_read_b64 v[124:125], v105 offset:424
	ds_read_b64 v[126:127], v105 offset:432
	s_waitcnt lgkmcnt(3)
	s_barrier
	ds_read_b64 v[128:129], v105 offset:512
	ds_read_b64 v[130:131], v105 offset:520
	ds_read_b64 v[132:133], v105 offset:528
	s_waitcnt lgkmcnt(3)
	v_mfma_scale_f32_16x16x128_f8f6f4 v[134:137], v[122:127], v[2:7], 0, v178, v112 op_sel_hi:[0,0,0] cbsz:2 blgp:2
	v_mfma_scale_f32_16x16x128_f8f6f4 v[138:141], v[122:127], v[14:19], 0, v178, v112 op_sel_hi:[0,0,0] cbsz:2 blgp:2
	v_mfma_scale_f32_16x16x128_f8f6f4 v[142:145], v[122:127], v[26:31], 0, v178, v112 op_sel_hi:[0,0,0] cbsz:2 blgp:2
	v_mfma_scale_f32_16x16x128_f8f6f4 v[134:137], v[122:127], v[38:43], v[134:137], v179, v112 op_sel_hi:[0,0,0] cbsz:2 blgp:2
	v_mfma_scale_f32_16x16x128_f8f6f4 v[138:141], v[122:127], v[50:55], v[138:141], v179, v112 op_sel_hi:[0,0,0] cbsz:2 blgp:2
	v_mfma_scale_f32_16x16x128_f8f6f4 v[142:145], v[122:127], v[62:67], v[142:145], v179, v112 op_sel_hi:[0,0,0] cbsz:2 blgp:2
	s_waitcnt lgkmcnt(0)
	v_mfma_scale_f32_16x16x128_f8f6f4 v[134:137], v[128:133], v[8:13], v[134:137], v178, v112 op_sel_hi:[0,0,0] cbsz:2 blgp:2
	v_mfma_scale_f32_16x16x128_f8f6f4 v[134:137], v[128:133], v[44:49], v[134:137], v179, v112 op_sel_hi:[0,0,0] cbsz:2 blgp:2
	v_mfma_scale_f32_16x16x128_f8f6f4 v[138:141], v[128:133], v[20:25], v[138:141], v178, v112 op_sel_hi:[0,0,0] cbsz:2 blgp:2
	v_mfma_scale_f32_16x16x128_f8f6f4 v[138:141], v[128:133], v[56:61], v[138:141], v179, v112 op_sel_hi:[0,0,0] cbsz:2 blgp:2
	v_mfma_scale_f32_16x16x128_f8f6f4 v[142:145], v[128:133], v[32:37], v[142:145], v178, v112 op_sel_hi:[0,0,0] cbsz:2 blgp:2
	v_mfma_scale_f32_16x16x128_f8f6f4 v[142:145], v[128:133], v[68:73], v[142:145], v179, v112 op_sel_hi:[0,0,0] cbsz:2 blgp:2
	v_fma_mix_f32 v158, v134, v100, v148 op_sel:[0,0,1] op_sel_hi:[0,0,1]
	v_exp_f32_e32 v158, v158
	v_fma_mix_f32 v159, v138, v101, v152 op_sel:[0,0,1] op_sel_hi:[0,0,1]
	v_exp_f32_e32 v159, v159
	v_add_f32_e32 v158, 1.0, v158
	v_rcp_f32_e32 v158, v158
	v_add_f32_e32 v159, 1.0, v159
	v_rcp_f32_e32 v159, v159
	v_fma_f32 v160, v142, v102, v103
	v_fma_mix_f32 v161, v158, v160, v156 op_sel:[0,0,1] op_sel_hi:[0,0,1]
	v_exp_f32_e32 v161, v161
	s_add_u32 s48, s48, s40
	v_add_f32_e32 v161, 1.0, v161
	v_rcp_f32_e32 v161, v161
	s_addc_u32 s49, s49, s41
	v_fma_f32 v162, v161, -2.0, 1.0
	v_sub_f32_e32 v163, v176, v162
	v_fma_f32 v176, v159, v163, v162
	v_fma_f32 v164, |v176|, s17, v113
	v_fma_f32 v165, |v176|, s18, v114
	v_fma_f32 v166, |v176|, s19, v115
	v_lshrrev_b32_e32 v167, 26, v176
	v_min3_u32 v164, v164, v165, v166
	v_bfi_b32 v168, 31, v164, v167
	v_lshrrev_b32_e32 v169, v181, v168
	global_store_short_d16_hi v185, v176, s[48:49]
	v_mul_u32_u24_dpp v170, v168, v180 quad_perm:[1,2,3,3] row_mask:0xf bank_mask:0xf bound_ctrl:1
	v_or_b32_e32 v171, v169, v170
	ds_write_b8 v184, v171
	s_barrier
	ds_read_b64 v[122:123], v105 offset:0
	ds_read_b64 v[124:125], v105 offset:8
	ds_read_b64 v[126:127], v105 offset:16
	s_waitcnt lgkmcnt(3)
	s_barrier
	ds_read_b64 v[128:129], v105 offset:96
	ds_read_b64 v[130:131], v105 offset:104
	ds_read_b64 v[132:133], v105 offset:112
	s_waitcnt lgkmcnt(3)
	v_mfma_scale_f32_16x16x128_f8f6f4 v[134:137], v[122:127], v[2:7], 0, v178, v112 op_sel_hi:[0,0,0] cbsz:2 blgp:2
	v_mfma_scale_f32_16x16x128_f8f6f4 v[138:141], v[122:127], v[14:19], 0, v178, v112 op_sel_hi:[0,0,0] cbsz:2 blgp:2
	v_mfma_scale_f32_16x16x128_f8f6f4 v[142:145], v[122:127], v[26:31], 0, v178, v112 op_sel_hi:[0,0,0] cbsz:2 blgp:2
	v_mfma_scale_f32_16x16x128_f8f6f4 v[134:137], v[122:127], v[38:43], v[134:137], v179, v112 op_sel_hi:[0,0,0] cbsz:2 blgp:2
	v_mfma_scale_f32_16x16x128_f8f6f4 v[138:141], v[122:127], v[50:55], v[138:141], v179, v112 op_sel_hi:[0,0,0] cbsz:2 blgp:2
	v_mfma_scale_f32_16x16x128_f8f6f4 v[142:145], v[122:127], v[62:67], v[142:145], v179, v112 op_sel_hi:[0,0,0] cbsz:2 blgp:2
	s_waitcnt lgkmcnt(0)
	v_mfma_scale_f32_16x16x128_f8f6f4 v[134:137], v[128:133], v[8:13], v[134:137], v178, v112 op_sel_hi:[0,0,0] cbsz:2 blgp:2
	v_mfma_scale_f32_16x16x128_f8f6f4 v[134:137], v[128:133], v[44:49], v[134:137], v179, v112 op_sel_hi:[0,0,0] cbsz:2 blgp:2
	v_mfma_scale_f32_16x16x128_f8f6f4 v[138:141], v[128:133], v[20:25], v[138:141], v178, v112 op_sel_hi:[0,0,0] cbsz:2 blgp:2
	v_mfma_scale_f32_16x16x128_f8f6f4 v[138:141], v[128:133], v[56:61], v[138:141], v179, v112 op_sel_hi:[0,0,0] cbsz:2 blgp:2
	v_mfma_scale_f32_16x16x128_f8f6f4 v[142:145], v[128:133], v[32:37], v[142:145], v178, v112 op_sel_hi:[0,0,0] cbsz:2 blgp:2
	v_mfma_scale_f32_16x16x128_f8f6f4 v[142:145], v[128:133], v[68:73], v[142:145], v179, v112 op_sel_hi:[0,0,0] cbsz:2 blgp:2
	v_fma_mix_f32 v158, v134, v100, v149 op_sel_hi:[0,0,1]
	v_exp_f32_e32 v158, v158
	v_fma_mix_f32 v159, v138, v101, v153 op_sel_hi:[0,0,1]
	v_exp_f32_e32 v159, v159
	v_add_f32_e32 v158, 1.0, v158
	v_rcp_f32_e32 v158, v158
	v_add_f32_e32 v159, 1.0, v159
	v_rcp_f32_e32 v159, v159
	v_fma_f32 v160, v142, v102, v103
	v_fma_mix_f32 v161, v158, v160, v157 op_sel_hi:[0,0,1]
	v_exp_f32_e32 v161, v161
	s_add_u32 s48, s48, s40
	v_add_f32_e32 v161, 1.0, v161
	v_rcp_f32_e32 v161, v161
	s_addc_u32 s49, s49, s41
	v_fma_f32 v162, v161, -2.0, 1.0
	v_sub_f32_e32 v163, v176, v162
	v_fma_f32 v176, v159, v163, v162
	v_fma_f32 v164, |v176|, s17, v113
	v_fma_f32 v165, |v176|, s18, v114
	v_fma_f32 v166, |v176|, s19, v115
	v_lshrrev_b32_e32 v167, 26, v176
	v_min3_u32 v164, v164, v165, v166
	v_bfi_b32 v168, 31, v164, v167
	v_lshrrev_b32_e32 v169, v181, v168
	global_store_short_d16_hi v185, v176, s[48:49]
	v_mul_u32_u24_dpp v170, v168, v180 quad_perm:[1,2,3,3] row_mask:0xf bank_mask:0xf bound_ctrl:1
	v_or_b32_e32 v171, v169, v170
	ds_write_b8 v184, v171 offset:416
	s_barrier
	ds_read_b64 v[122:123], v105 offset:416
	ds_read_b64 v[124:125], v105 offset:424
	ds_read_b64 v[126:127], v105 offset:432
	s_waitcnt lgkmcnt(3)
	s_barrier
	ds_read_b64 v[128:129], v105 offset:512
	ds_read_b64 v[130:131], v105 offset:520
	ds_read_b64 v[132:133], v105 offset:528
	s_add_i32 s44, s44, 16
	s_waitcnt lgkmcnt(3)
	v_mfma_scale_f32_16x16x128_f8f6f4 v[134:137], v[122:127], v[2:7], 0, v178, v112 op_sel_hi:[0,0,0] cbsz:2 blgp:2
	v_mfma_scale_f32_16x16x128_f8f6f4 v[138:141], v[122:127], v[14:19], 0, v178, v112 op_sel_hi:[0,0,0] cbsz:2 blgp:2
	v_mfma_scale_f32_16x16x128_f8f6f4 v[142:145], v[122:127], v[26:31], 0, v178, v112 op_sel_hi:[0,0,0] cbsz:2 blgp:2
	v_mfma_scale_f32_16x16x128_f8f6f4 v[134:137], v[122:127], v[38:43], v[134:137], v179, v112 op_sel_hi:[0,0,0] cbsz:2 blgp:2
	v_mfma_scale_f32_16x16x128_f8f6f4 v[138:141], v[122:127], v[50:55], v[138:141], v179, v112 op_sel_hi:[0,0,0] cbsz:2 blgp:2
	v_mfma_scale_f32_16x16x128_f8f6f4 v[142:145], v[122:127], v[62:67], v[142:145], v179, v112 op_sel_hi:[0,0,0] cbsz:2 blgp:2
	s_waitcnt lgkmcnt(0)
	v_mfma_scale_f32_16x16x128_f8f6f4 v[134:137], v[128:133], v[8:13], v[134:137], v178, v112 op_sel_hi:[0,0,0] cbsz:2 blgp:2
	v_mfma_scale_f32_16x16x128_f8f6f4 v[134:137], v[128:133], v[44:49], v[134:137], v179, v112 op_sel_hi:[0,0,0] cbsz:2 blgp:2
	v_mfma_scale_f32_16x16x128_f8f6f4 v[138:141], v[128:133], v[20:25], v[138:141], v178, v112 op_sel_hi:[0,0,0] cbsz:2 blgp:2
	v_mfma_scale_f32_16x16x128_f8f6f4 v[138:141], v[128:133], v[56:61], v[138:141], v179, v112 op_sel_hi:[0,0,0] cbsz:2 blgp:2
	v_mfma_scale_f32_16x16x128_f8f6f4 v[142:145], v[128:133], v[32:37], v[142:145], v178, v112 op_sel_hi:[0,0,0] cbsz:2 blgp:2
	v_mfma_scale_f32_16x16x128_f8f6f4 v[142:145], v[128:133], v[68:73], v[142:145], v179, v112 op_sel_hi:[0,0,0] cbsz:2 blgp:2
	v_fma_mix_f32 v158, v134, v100, v149 op_sel:[0,0,1] op_sel_hi:[0,0,1]
	v_exp_f32_e32 v158, v158
	v_fma_mix_f32 v159, v138, v101, v153 op_sel:[0,0,1] op_sel_hi:[0,0,1]
	v_exp_f32_e32 v159, v159
	v_add_f32_e32 v158, 1.0, v158
	v_rcp_f32_e32 v158, v158
	v_add_f32_e32 v159, 1.0, v159
	v_rcp_f32_e32 v159, v159
	v_fma_f32 v160, v142, v102, v103
	v_fma_mix_f32 v161, v158, v160, v157 op_sel:[0,0,1] op_sel_hi:[0,0,1]
	v_exp_f32_e32 v161, v161
	s_add_u32 s48, s48, s40
	v_add_f32_e32 v161, 1.0, v161
	v_rcp_f32_e32 v161, v161
	s_addc_u32 s49, s49, s41
	v_fma_f32 v162, v161, -2.0, 1.0
	v_sub_f32_e32 v163, v176, v162
	v_fma_f32 v176, v159, v163, v162
	v_fma_f32 v164, |v176|, s17, v113
	v_fma_f32 v165, |v176|, s18, v114
	v_fma_f32 v166, |v176|, s19, v115
	v_lshrrev_b32_e32 v167, 26, v176
	v_min3_u32 v164, v164, v165, v166
	v_bfi_b32 v168, 31, v164, v167
	v_lshrrev_b32_e32 v169, v181, v168
	global_store_short_d16_hi v185, v176, s[48:49]
	v_mul_u32_u24_dpp v170, v168, v180 quad_perm:[1,2,3,3] row_mask:0xf bank_mask:0xf bound_ctrl:1
	v_or_b32_e32 v171, v169, v170
	ds_write_b8 v184, v171
	s_barrier
	ds_read_b64 v[122:123], v105 offset:0
	ds_read_b64 v[124:125], v105 offset:8
	ds_read_b64 v[126:127], v105 offset:16
	s_cmp_lt_i32 s44, s45
	s_waitcnt lgkmcnt(3)
	s_barrier
	s_cbranch_scc1 .Lscan_loop_b_f2
